# P12 down-weight conversion: XCD-contiguous item map (XCD x converts experts 4x..4x+3 as contiguous 4 MB steps instead of a 1 KB column stripe of every row) with the 3-in-flight hand-written converter
# speedup vs baseline: 1.0138x; 1.0138x over previous
;     __device__ __forceinline__ void operator()(const f32x4 (&acc)[2][2][4][2], const Unit& u, int wr, int wc, int fr, int fq) const {
;         asm volatile("" : "+v"(fr), "+v"(fq));
;         const int e = blkE[u.z], c0 = u.pn * 128 + wc * 32 + 8 * fq, row0 = wr * 64 + fr;
;         const float* bg = bup + (size_t)e * 2 * FF + c0; const f32x4 g0 = *(const f32x4*)bg, g1 = *(const f32x4*)(bg + 4), l0 = *(const f32x4*)(bg + FF), l1 = *(const f32x4*)(bg + FF + 4);
;         float rsb[8];
; #pragma unroll
;         for (int q = 0; q < 8; ++q) rsb[q] = ssq[tokTab[u.pm * 256 + row0 + (q >> 2) * 128 + (q & 3) * 16]] * W8_INV;
; #pragma unroll
;         for (int ai = 0; ai < 2; ++ai)
; #pragma unroll
;             for (int m = 0; m < 4; ++m) { const int r = row0 + ai * 128 + m * 16; const float rs = rsb[ai * 4 + m];
;                 float a[8];
; #pragma unroll
;                 for (int j = 0; j < 8; ++j) { const float gb = j < 4 ? g0[j & 3] : g1[j & 3], lb = j < 4 ? l0[j & 3] : l1[j & 3];
;                     const float gl = fminf(acc[ai][0][m][j >> 2][j & 3] * rs + gb, 7.0f), ln = fminf(fmaxf(acc[ai][1][m][j >> 2][j & 3] * rs + lb, -7.0f), 7.0f);
;                     a[j] = gl * __builtin_amdgcn_rcpf(1.0f + __builtin_amdgcn_exp2f(-1.702f * 1.4426950408889634f * gl)) * (ln + 1.0f); }
;                 v2u w; w.x = pk4_fp8(a[0], a[1], a[2], a[3]); w.y = pk4_fp8(a[4], a[5], a[6], a[7]);
;                 *(v2u*)(ACT + ((size_t)u.z * 256 + r) * FF + c0) = w; }
;     __device__ __forceinline__ void done(const Unit& u) const { if (u.pm == (c & 7)) convert_share(); }
.LBB0_1534:
	s_lshl_b32 s4, s40, 7
	v_mov_b32_e32 v2, v218
	v_mov_b32_e32 v3, v219
	s_or_b32 s4, s4, s89
	v_mov_b32_e32 v0, s35
	v_lshl_add_u32 v16, v3, 3, s4
	v_readlane_b32 s0, v254, 2
	v_readlane_b32 s4, v254, 6
	s_lshl_b32 s4, s65, 10
	v_add_u32_e32 v18, s88, v2
	s_add_i32 s4, s4, 0
	v_lshl_add_u32 v2, v18, 2, s4
	v_add_u32_e32 v9, 0x20400, v2
	ds_read2_b32 v[4:5], v9 offset1:16
	ds_read_b32 v0, v0
	v_readlane_b32 s1, v254, 3
	v_ashrrev_i32_e32 v17, 31, v16
	ds_read2_b32 v[20:21], v9 offset0:160 offset1:176
	s_waitcnt lgkmcnt(0)
	v_ashrrev_i32_e32 v11, 31, v4
	v_mov_b32_e32 v10, v4
	v_lshl_add_u64 v[10:11], v[10:11], 2, s[14:15]
	global_load_dword v19, v[10:11], off
	ds_read2_b32 v[10:11], v9 offset0:32 offset1:48
	v_ashrrev_i32_e32 v13, 31, v5
	v_mov_b32_e32 v12, v5
	v_lshl_add_u64 v[4:5], v[12:13], 2, s[14:15]
	global_load_dword v24, v[4:5], off
	s_waitcnt lgkmcnt(0)
	v_ashrrev_i32_e32 v5, 31, v10
	v_mov_b32_e32 v4, v10
	v_lshl_add_u64 v[4:5], v[4:5], 2, s[14:15]
	global_load_dword v25, v[4:5], off
	ds_read2_b32 v[4:5], v9 offset0:128 offset1:144
	v_ashrrev_i32_e32 v13, 31, v11
	v_mov_b32_e32 v12, v11
	v_lshl_add_u64 v[10:11], v[12:13], 2, s[14:15]
	v_ashrrev_i32_e32 v1, 31, v0
	global_load_dword v26, v[10:11], off
	s_waitcnt lgkmcnt(0)
	v_ashrrev_i32_e32 v11, 31, v4
	v_mov_b32_e32 v10, v4
	v_lshlrev_b64 v[0:1], 14, v[0:1]
	v_lshl_add_u64 v[10:11], v[10:11], 2, s[14:15]
	v_lshl_add_u64 v[0:1], s[0:1], 0, v[0:1]
	global_load_dword v27, v[10:11], off
	v_ashrrev_i32_e32 v11, 31, v5
	v_mov_b32_e32 v10, v5
	v_lshl_add_u64 v[6:7], v[16:17], 2, v[0:1]
	v_lshl_add_u64 v[4:5], v[10:11], 2, s[14:15]
	global_load_dwordx4 v[0:3], v[6:7], off
	global_load_dword v28, v[4:5], off
	v_ashrrev_i32_e32 v5, 31, v20
	v_mov_b32_e32 v4, v20
	v_add_co_u32_e32 v8, vcc, s56, v6
	v_lshl_add_u64 v[4:5], v[4:5], 2, s[14:15]
	global_load_dword v29, v[4:5], off
	v_addc_co_u32_e32 v9, vcc, 0, v7, vcc
	global_load_dwordx4 v[8:11], v[8:9], off
	s_nop 0
	global_load_dwordx4 v[12:15], v[6:7], off offset:16
	v_readlane_b32 s5, v254, 7
	s_mov_b64 s[4:5], 0x2000
	v_ashrrev_i32_e32 v23, 31, v21
	v_lshl_add_u64 v[4:5], v[6:7], 0, s[4:5]
	global_load_dwordx4 v[4:7], v[4:5], off offset:16
	v_mov_b32_e32 v22, v21
	v_lshl_add_u64 v[20:21], v[22:23], 2, s[14:15]
	global_load_dword v20, v[20:21], off
	s_ashr_i32 s39, s38, 31
	s_lshl_b64 s[4:5], s[38:39], 19
	s_add_u32 s4, s93, s4
	s_addc_u32 s5, s87, s5
	v_readlane_b32 s0, v254, 10
	s_cmp_lg_u32 s65, s0
	v_readlane_b32 s2, v254, 4
	v_readlane_b32 s3, v254, 5
	v_readlane_b32 s6, v254, 8
	v_readlane_b32 s7, v254, 9
	s_waitcnt vmcnt(0)
	v_mul_f32_e32 v19, 0x3b800000, v19
	v_mul_f32_e32 v30, 0x3b800000, v24
	v_mul_f32_e32 v25, 0x3b800000, v25
	v_mul_f32_e32 v24, 0x3b800000, v26
	v_mul_f32_e32 v23, 0x3b800000, v27
	v_fma_f32 v26, v192, v19, v0
	v_mul_f32_e32 v22, 0x3b800000, v28
	v_fma_f32 v28, v193, v19, v1
	v_min_f32_e32 v26, 0x40e00000, v26
	v_min_f32_e32 v28, 0x40e00000, v28
	v_fma_f32 v31, v194, v19, v2
	v_mul_f32_e32 v34, 0xc01d265f, v26
	v_mul_f32_e32 v35, 0xc01d265f, v28
	v_min_f32_e32 v31, 0x40e00000, v31
	v_exp_f32_e32 v34, v34
	v_exp_f32_e32 v35, v35
	v_mul_f32_e32 v36, 0xc01d265f, v31
	v_fma_f32 v33, v195, v19, v3
	v_exp_f32_e32 v36, v36
	v_min_f32_e32 v33, 0x40e00000, v33
	v_mul_f32_e32 v37, 0xc01d265f, v33
	v_add_f32_e32 v34, 1.0, v34
	v_add_f32_e32 v35, 1.0, v35
	v_exp_f32_e32 v37, v37
	v_rcp_f32_e32 v34, v34
	v_rcp_f32_e32 v35, v35
	v_add_f32_e32 v36, 1.0, v36
	v_mul_f32_e32 v21, 0x3b800000, v29
	v_fma_f32 v27, v188, v19, v8
	v_fma_f32 v29, v189, v19, v9
	v_rcp_f32_e32 v36, v36
	v_med3_f32 v27, v27, s23, v236
	v_med3_f32 v29, v29, s23, v236
	v_fma_f32 v32, v190, v19, v10
	v_add_f32_e32 v27, 1.0, v27
	v_add_f32_e32 v29, 1.0, v29
	v_add_f32_e32 v37, 1.0, v37
	v_mul_f32_e32 v26, v26, v34
	v_mul_f32_e32 v28, v28, v35
	v_med3_f32 v32, v32, s23, v236
	v_mul_f32_e32 v26, v27, v26
	v_mul_f32_e32 v27, v29, v28
	v_rcp_f32_e32 v28, v37
	v_add_f32_e32 v32, 1.0, v32
	v_mul_f32_e32 v31, v31, v36
	v_mul_f32_e32 v29, v32, v31
	v_fma_f32 v32, v184, v19, v12
	v_min_f32_e32 v32, 0x40e00000, v32
	v_mul_f32_e32 v28, v33, v28
	v_mul_f32_e32 v33, 0xc01d265f, v32
	v_exp_f32_e32 v33, v33
	v_fma_f32 v34, v185, v19, v13
	v_min_f32_e32 v34, 0x40e00000, v34
	v_mul_f32_e32 v35, 0xc01d265f, v34
	v_add_f32_e32 v33, 1.0, v33
	v_rcp_f32_e32 v33, v33
	v_exp_f32_e32 v35, v35
	v_fma_f32 v31, v191, v19, v11
	v_fma_f32 v36, v187, v19, v15
	v_mul_f32_e32 v32, v32, v33
	v_add_f32_e32 v33, 1.0, v35
	v_rcp_f32_e32 v33, v33
	v_med3_f32 v31, v31, s23, v236
	v_min_f32_e32 v36, 0x40e00000, v36
	v_add_f32_e32 v31, 1.0, v31
	v_mul_f32_e32 v33, v34, v33
	v_fma_f32 v34, v186, v19, v14
	v_min_f32_e32 v34, 0x40e00000, v34
	v_mul_f32_e32 v35, 0xc01d265f, v34
	v_exp_f32_e32 v35, v35
	v_mul_f32_e32 v37, 0xc01d265f, v36
	v_mul_f32_e32 v28, v31, v28
	v_fma_f32 v31, v180, v19, v4
	v_add_f32_e32 v35, 1.0, v35
	v_rcp_f32_e32 v35, v35
	v_exp_f32_e32 v37, v37
	v_med3_f32 v31, v31, s23, v236
	v_add_f32_e32 v31, 1.0, v31
	v_mul_f32_e32 v31, v31, v32
	v_fma_f32 v32, v181, v19, v5
	v_med3_f32 v32, v32, s23, v236
	v_mul_f32_e32 v34, v34, v35
	v_add_f32_e32 v35, 1.0, v37
	v_add_f32_e32 v32, 1.0, v32
	v_rcp_f32_e32 v35, v35
	v_mul_f32_e32 v32, v32, v33
	v_fma_f32 v33, v182, v19, v6
	v_med3_f32 v33, v33, s23, v236
	v_fma_f32 v19, v183, v19, v7
	v_add_f32_e32 v33, 1.0, v33
	v_med3_f32 v19, v19, s23, v236
	v_mul_f32_e32 v33, v33, v34
	v_mul_f32_e32 v34, v36, v35
	v_add_f32_e32 v19, 1.0, v19
	v_mul_f32_e32 v19, v19, v34
	v_med3_f32 v34, v26, s24, v237
	v_med3_f32 v27, v27, s24, v237
	v_mov_b32_e32 v26, v65
	v_cvt_pk_fp8_f32 v26, v34, v27
	v_med3_f32 v31, v31, s24, v237
	v_med3_f32 v32, v32, s24, v237
;     __device__ __forceinline__ void operator()(const f32x4 (&acc)[2][2][4][2], const Unit& u, int wr, int wc, int fr, int fq) const {
;     ...
; #pragma unroll
;         for (int ai = 0; ai < 2; ++ai)
; #pragma unroll
;             for (int m = 0; m < 4; ++m) { const int r = row0 + ai * 128 + m * 16; const float rs = rsb[ai * 4 + m];
;                 float a[8];
; #pragma unroll
;                 for (int j = 0; j < 8; ++j) { const float gb = j < 4 ? g0[j & 3] : g1[j & 3], lb = j < 4 ? l0[j & 3] : l1[j & 3];
;                     const float gl = fminf(acc[ai][0][m][j >> 2][j & 3] * rs + gb, 7.0f), ln = fminf(fmaxf(acc[ai][1][m][j >> 2][j & 3] * rs + lb, -7.0f), 7.0f);
;                     a[j] = gl * __builtin_amdgcn_rcpf(1.0f + __builtin_amdgcn_exp2f(-1.702f * 1.4426950408889634f * gl)) * (ln + 1.0f); }
;                 v2u w; w.x = pk4_fp8(a[0], a[1], a[2], a[3]); w.y = pk4_fp8(a[4], a[5], a[6], a[7]);
;                 *(v2u*)(ACT + ((size_t)u.z * 256 + r) * FF + c0) = w; }
	v_mov_b32_e32 v27, v65
	v_cvt_pk_fp8_f32 v27, v31, v32
	v_med3_f32 v29, v29, s24, v237
	v_med3_f32 v28, v28, s24, v237
	v_cvt_pk_fp8_f32 v26, v29, v28 op_sel:[0,0,1]
	v_med3_f32 v28, v33, s24, v237
	v_med3_f32 v19, v19, s24, v237
	v_cvt_pk_fp8_f32 v27, v28, v19 op_sel:[0,0,1]
	v_ashrrev_i32_e32 v19, 31, v18
	v_lshlrev_b64 v[18:19], 11, v[18:19]
	v_lshl_add_u64 v[18:19], s[4:5], 0, v[18:19]
	v_lshl_add_u64 v[16:17], v[18:19], 0, v[16:17]
	global_store_dwordx2 v[16:17], v[26:27], off
	v_fma_f32 v26, v177, v30, v1
	v_min_f32_e32 v26, 0x40e00000, v26
	v_fma_f32 v28, v176, v30, v0
	v_mul_f32_e32 v27, 0xc01d265f, v26
	v_min_f32_e32 v28, 0x40e00000, v28
	v_exp_f32_e32 v27, v27
	v_mul_f32_e32 v29, 0xc01d265f, v28
	v_exp_f32_e32 v29, v29
	v_fma_f32 v32, v169, v30, v13
	v_add_f32_e32 v27, 1.0, v27
	v_rcp_f32_e32 v27, v27
	v_add_f32_e32 v19, 1.0, v29
	v_rcp_f32_e32 v19, v19
	v_fma_f32 v29, v179, v30, v3
	v_mul_f32_e32 v26, v26, v27
	v_fma_f32 v27, v178, v30, v2
	v_min_f32_e32 v27, 0x40e00000, v27
	v_mul_f32_e32 v19, v28, v19
	v_mul_f32_e32 v28, 0xc01d265f, v27
	v_exp_f32_e32 v28, v28
	v_min_f32_e32 v29, 0x40e00000, v29
	v_mul_f32_e32 v31, 0xc01d265f, v29
	v_exp_f32_e32 v31, v31
	v_add_f32_e32 v28, 1.0, v28
	v_rcp_f32_e32 v28, v28
	v_min_f32_e32 v32, 0x40e00000, v32
	v_mul_f32_e32 v33, 0xc01d265f, v32
	v_exp_f32_e32 v33, v33
	v_mul_f32_e32 v27, v27, v28
	v_add_f32_e32 v28, 1.0, v31
	v_rcp_f32_e32 v28, v28
	v_fma_f32 v18, v172, v30, v8
	v_med3_f32 v18, v18, s23, v236
	v_add_f32_e32 v18, 1.0, v18
	v_mul_f32_e32 v28, v29, v28
	v_fma_f32 v29, v168, v30, v12
	v_min_f32_e32 v29, 0x40e00000, v29
	v_mul_f32_e32 v31, 0xc01d265f, v29
	v_exp_f32_e32 v31, v31
	v_mul_f32_e32 v18, v18, v19
	v_fma_f32 v19, v173, v30, v9
	v_med3_f32 v19, v19, s23, v236
	v_add_f32_e32 v31, 1.0, v31
	v_rcp_f32_e32 v31, v31
	v_add_f32_e32 v19, 1.0, v19
	v_mul_f32_e32 v19, v19, v26
	v_fma_f32 v26, v174, v30, v10
	v_mul_f32_e32 v29, v29, v31
	v_add_f32_e32 v31, 1.0, v33
	v_rcp_f32_e32 v31, v31
	v_med3_f32 v26, v26, s23, v236
	v_add_f32_e32 v26, 1.0, v26
	v_mul_f32_e32 v26, v26, v27
	v_mul_f32_e32 v31, v32, v31
	v_fma_f32 v32, v170, v30, v14
	v_min_f32_e32 v32, 0x40e00000, v32
	v_mul_f32_e32 v33, 0xc01d265f, v32
	v_exp_f32_e32 v33, v33
	v_fma_f32 v27, v175, v30, v11
	v_fma_f32 v34, v171, v30, v15
	v_med3_f32 v27, v27, s23, v236
	v_min_f32_e32 v34, 0x40e00000, v34
	v_add_f32_e32 v27, 1.0, v27
	v_add_f32_e32 v33, 1.0, v33
	v_mul_f32_e32 v35, 0xc01d265f, v34
	v_mul_f32_e32 v27, v27, v28
	v_fma_f32 v28, v164, v30, v4
	v_rcp_f32_e32 v33, v33
	v_exp_f32_e32 v35, v35
	v_med3_f32 v28, v28, s23, v236
	v_add_f32_e32 v28, 1.0, v28
	v_mul_f32_e32 v28, v28, v29
	v_fma_f32 v29, v165, v30, v5
	v_med3_f32 v29, v29, s23, v236
	v_mul_f32_e32 v32, v32, v33
	v_add_f32_e32 v33, 1.0, v35
	v_add_f32_e32 v29, 1.0, v29
	v_rcp_f32_e32 v33, v33
	v_mul_f32_e32 v29, v29, v31
	v_fma_f32 v31, v166, v30, v6
	v_med3_f32 v31, v31, s23, v236
	v_fma_f32 v30, v167, v30, v7
	v_add_f32_e32 v31, 1.0, v31
	v_med3_f32 v30, v30, s23, v236
	v_mul_f32_e32 v31, v31, v32
	v_mul_f32_e32 v32, v34, v33
	v_add_f32_e32 v30, 1.0, v30
	v_mul_f32_e32 v30, v30, v32
	v_med3_f32 v32, v18, s24, v237
	v_med3_f32 v19, v19, s24, v237
	v_mov_b32_e32 v18, v65
	v_cvt_pk_fp8_f32 v18, v32, v19
	v_med3_f32 v28, v28, s24, v237
	v_med3_f32 v29, v29, s24, v237
	v_mov_b32_e32 v19, v65
	v_cvt_pk_fp8_f32 v19, v28, v29
	v_med3_f32 v26, v26, s24, v237
	v_med3_f32 v27, v27, s24, v237
	v_cvt_pk_fp8_f32 v18, v26, v27 op_sel:[0,0,1]
	v_med3_f32 v26, v31, s24, v237
	v_med3_f32 v27, v30, s24, v237
	v_cvt_pk_fp8_f32 v19, v26, v27 op_sel:[0,0,1]
	v_fma_f32 v27, v160, v25, v0
	v_min_f32_e32 v28, 0x40e00000, v27
	v_add_co_u32_e32 v26, vcc, s73, v16
	v_mul_f32_e32 v27, 0xc01d265f, v28
	v_exp_f32_e32 v29, v27
	v_addc_co_u32_e32 v27, vcc, 0, v17, vcc
	global_store_dwordx2 v[26:27], v[18:19], off
	v_fma_f32 v26, v161, v25, v1
	v_min_f32_e32 v26, 0x40e00000, v26
	v_mul_f32_e32 v27, 0xc01d265f, v26
	v_exp_f32_e32 v27, v27
	v_add_f32_e32 v19, 1.0, v29
	v_rcp_f32_e32 v19, v19
	v_fma_f32 v29, v163, v25, v3
	v_add_f32_e32 v27, 1.0, v27
	v_rcp_f32_e32 v27, v27
	v_mul_f32_e32 v19, v28, v19
	v_min_f32_e32 v29, 0x40e00000, v29
	v_mul_f32_e32 v30, 0xc01d265f, v29
	v_mul_f32_e32 v26, v26, v27
	v_fma_f32 v27, v162, v25, v2
	v_min_f32_e32 v27, 0x40e00000, v27
	v_mul_f32_e32 v28, 0xc01d265f, v27
	v_exp_f32_e32 v28, v28
	v_exp_f32_e32 v30, v30
	v_fma_f32 v31, v153, v25, v13
	v_min_f32_e32 v31, 0x40e00000, v31
	v_add_f32_e32 v28, 1.0, v28
	v_rcp_f32_e32 v28, v28
	v_mul_f32_e32 v32, 0xc01d265f, v31
	v_exp_f32_e32 v32, v32
	v_fma_f32 v18, v156, v25, v8
	v_mul_f32_e32 v27, v27, v28
	v_add_f32_e32 v28, 1.0, v30
	v_rcp_f32_e32 v28, v28
	v_med3_f32 v18, v18, s23, v236
	v_add_f32_e32 v18, 1.0, v18
	v_mul_f32_e32 v18, v18, v19
	v_mul_f32_e32 v28, v29, v28
	v_fma_f32 v29, v152, v25, v12
	v_min_f32_e32 v29, 0x40e00000, v29
	v_mul_f32_e32 v30, 0xc01d265f, v29
	v_exp_f32_e32 v30, v30
	v_fma_f32 v19, v157, v25, v9
	v_med3_f32 v19, v19, s23, v236
	v_add_f32_e32 v19, 1.0, v19
	v_add_f32_e32 v30, 1.0, v30
	v_rcp_f32_e32 v30, v30
	v_mul_f32_e32 v19, v19, v26
	v_fma_f32 v26, v158, v25, v10
	v_med3_f32 v26, v26, s23, v236
	v_mul_f32_e32 v29, v29, v30
	v_add_f32_e32 v30, 1.0, v32
	v_rcp_f32_e32 v30, v30
	v_add_f32_e32 v26, 1.0, v26
	v_mul_f32_e32 v26, v26, v27
	v_fma_f32 v27, v159, v25, v11
	v_mul_f32_e32 v30, v31, v30
	v_fma_f32 v31, v154, v25, v14
	v_min_f32_e32 v31, 0x40e00000, v31
	v_mul_f32_e32 v32, 0xc01d265f, v31
	v_exp_f32_e32 v32, v32
	v_fma_f32 v33, v155, v25, v15
	v_med3_f32 v27, v27, s23, v236
	v_min_f32_e32 v33, 0x40e00000, v33
	v_add_f32_e32 v27, 1.0, v27
	v_add_f32_e32 v32, 1.0, v32
;     __device__ __forceinline__ void operator()(const f32x4 (&acc)[2][2][4][2], const Unit& u, int wr, int wc, int fr, int fq) const {
;     ...
; #pragma unroll
;         for (int ai = 0; ai < 2; ++ai)
; #pragma unroll
;             for (int m = 0; m < 4; ++m) { const int r = row0 + ai * 128 + m * 16; const float rs = rsb[ai * 4 + m];
;                 float a[8];
; #pragma unroll
;                 for (int j = 0; j < 8; ++j) { const float gb = j < 4 ? g0[j & 3] : g1[j & 3], lb = j < 4 ? l0[j & 3] : l1[j & 3];
;                     const float gl = fminf(acc[ai][0][m][j >> 2][j & 3] * rs + gb, 7.0f), ln = fminf(fmaxf(acc[ai][1][m][j >> 2][j & 3] * rs + lb, -7.0f), 7.0f);
;                     a[j] = gl * __builtin_amdgcn_rcpf(1.0f + __builtin_amdgcn_exp2f(-1.702f * 1.4426950408889634f * gl)) * (ln + 1.0f); }
;                 v2u w; w.x = pk4_fp8(a[0], a[1], a[2], a[3]); w.y = pk4_fp8(a[4], a[5], a[6], a[7]);
;                 *(v2u*)(ACT + ((size_t)u.z * 256 + r) * FF + c0) = w; }
	v_mul_f32_e32 v34, 0xc01d265f, v33
	v_mul_f32_e32 v27, v27, v28
	v_fma_f32 v28, v148, v25, v4
	v_rcp_f32_e32 v32, v32
	v_exp_f32_e32 v34, v34
	v_med3_f32 v28, v28, s23, v236
	v_add_f32_e32 v28, 1.0, v28
	v_mul_f32_e32 v28, v28, v29
	v_fma_f32 v29, v149, v25, v5
	v_med3_f32 v29, v29, s23, v236
	v_mul_f32_e32 v31, v31, v32
	v_add_f32_e32 v32, 1.0, v34
	v_add_f32_e32 v29, 1.0, v29
	v_rcp_f32_e32 v32, v32
	v_mul_f32_e32 v29, v29, v30
	v_fma_f32 v30, v150, v25, v6
	v_med3_f32 v30, v30, s23, v236
	v_fma_f32 v25, v151, v25, v7
	v_add_f32_e32 v30, 1.0, v30
	v_med3_f32 v25, v25, s23, v236
	v_mul_f32_e32 v30, v30, v31
	v_mul_f32_e32 v31, v33, v32
	v_add_f32_e32 v25, 1.0, v25
	v_mul_f32_e32 v25, v25, v31
	v_med3_f32 v31, v18, s24, v237
	v_med3_f32 v19, v19, s24, v237
	v_mov_b32_e32 v18, v65
	v_cvt_pk_fp8_f32 v18, v31, v19
	v_med3_f32 v28, v28, s24, v237
	v_med3_f32 v29, v29, s24, v237
	v_mov_b32_e32 v19, v65
	v_cvt_pk_fp8_f32 v19, v28, v29
	v_med3_f32 v26, v26, s24, v237
	v_med3_f32 v27, v27, s24, v237
	v_cvt_pk_fp8_f32 v18, v26, v27 op_sel:[0,0,1]
	v_med3_f32 v26, v30, s24, v237
	v_med3_f32 v25, v25, s24, v237
	v_cvt_pk_fp8_f32 v19, v26, v25 op_sel:[0,0,1]
	v_fma_f32 v25, v144, v24, v0
	v_min_f32_e32 v25, 0x40e00000, v25
	v_mul_f32_e32 v27, 0xc01d265f, v25
	v_add_co_u32_e32 v26, vcc, s57, v16
	v_exp_f32_e32 v28, v27
	s_nop 0
	v_addc_co_u32_e32 v27, vcc, 0, v17, vcc
	global_store_dwordx2 v[26:27], v[18:19], off
	v_fma_f32 v26, v145, v24, v1
	v_min_f32_e32 v26, 0x40e00000, v26
	v_add_f32_e32 v19, 1.0, v28
	v_mul_f32_e32 v27, 0xc01d265f, v26
	v_rcp_f32_e32 v19, v19
	v_exp_f32_e32 v27, v27
	v_fma_f32 v28, v147, v24, v3
	v_min_f32_e32 v28, 0x40e00000, v28
	v_mul_f32_e32 v19, v25, v19
	v_add_f32_e32 v25, 1.0, v27
	v_rcp_f32_e32 v25, v25
	v_mul_f32_e32 v29, 0xc01d265f, v28
	v_exp_f32_e32 v29, v29
	v_fma_f32 v30, v137, v24, v13
	v_mul_f32_e32 v25, v26, v25
	v_fma_f32 v26, v146, v24, v2
	v_min_f32_e32 v26, 0x40e00000, v26
	v_mul_f32_e32 v27, 0xc01d265f, v26
	v_exp_f32_e32 v27, v27
	v_min_f32_e32 v30, 0x40e00000, v30
	v_mul_f32_e32 v31, 0xc01d265f, v30
	v_exp_f32_e32 v31, v31
	v_add_f32_e32 v27, 1.0, v27
	v_rcp_f32_e32 v27, v27
	v_fma_f32 v18, v140, v24, v8
	v_med3_f32 v18, v18, s23, v236
	v_add_f32_e32 v18, 1.0, v18
	v_mul_f32_e32 v26, v26, v27
	v_add_f32_e32 v27, 1.0, v29
	v_rcp_f32_e32 v27, v27
	v_mul_f32_e32 v18, v18, v19
	v_fma_f32 v19, v141, v24, v9
	v_med3_f32 v19, v19, s23, v236
	v_mul_f32_e32 v27, v28, v27
	v_fma_f32 v28, v136, v24, v12
	v_min_f32_e32 v28, 0x40e00000, v28
	v_mul_f32_e32 v29, 0xc01d265f, v28
	v_exp_f32_e32 v29, v29
	v_add_f32_e32 v19, 1.0, v19
	v_mul_f32_e32 v19, v19, v25
	v_fma_f32 v25, v142, v24, v10
	v_add_f32_e32 v29, 1.0, v29
	v_rcp_f32_e32 v29, v29
	v_med3_f32 v25, v25, s23, v236
	v_add_f32_e32 v25, 1.0, v25
	v_mul_f32_e32 v25, v25, v26
	v_mul_f32_e32 v28, v28, v29
	v_add_f32_e32 v29, 1.0, v31
	v_rcp_f32_e32 v29, v29
	v_fma_f32 v26, v143, v24, v11
	v_fma_f32 v32, v139, v24, v15
	v_med3_f32 v26, v26, s23, v236
	v_mul_f32_e32 v29, v30, v29
	v_fma_f32 v30, v138, v24, v14
	v_min_f32_e32 v30, 0x40e00000, v30
	v_mul_f32_e32 v31, 0xc01d265f, v30
	v_exp_f32_e32 v31, v31
	v_min_f32_e32 v32, 0x40e00000, v32
	v_add_f32_e32 v26, 1.0, v26
	v_mul_f32_e32 v33, 0xc01d265f, v32
	v_add_f32_e32 v31, 1.0, v31
	v_mul_f32_e32 v26, v26, v27
	v_fma_f32 v27, v132, v24, v4
	v_rcp_f32_e32 v31, v31
	v_exp_f32_e32 v33, v33
	v_med3_f32 v27, v27, s23, v236
	v_add_f32_e32 v27, 1.0, v27
	v_mul_f32_e32 v27, v27, v28
	v_fma_f32 v28, v133, v24, v5
	v_med3_f32 v28, v28, s23, v236
	v_mul_f32_e32 v30, v30, v31
	v_add_f32_e32 v31, 1.0, v33
	v_add_f32_e32 v28, 1.0, v28
	v_rcp_f32_e32 v31, v31
	v_mul_f32_e32 v28, v28, v29
	v_fma_f32 v29, v134, v24, v6
	v_med3_f32 v29, v29, s23, v236
	v_fma_f32 v24, v135, v24, v7
	v_add_f32_e32 v29, 1.0, v29
	v_med3_f32 v24, v24, s23, v236
	v_mul_f32_e32 v29, v29, v30
	v_mul_f32_e32 v30, v32, v31
	v_add_f32_e32 v24, 1.0, v24
	v_mul_f32_e32 v24, v24, v30
	v_med3_f32 v30, v18, s24, v237
	v_med3_f32 v19, v19, s24, v237
	v_mov_b32_e32 v18, v65
	v_cvt_pk_fp8_f32 v18, v30, v19
	v_med3_f32 v27, v27, s24, v237
	v_med3_f32 v28, v28, s24, v237
	v_mov_b32_e32 v19, v65
	v_cvt_pk_fp8_f32 v19, v27, v28
	v_med3_f32 v25, v25, s24, v237
	v_med3_f32 v26, v26, s24, v237
	v_cvt_pk_fp8_f32 v18, v25, v26 op_sel:[0,0,1]
	v_med3_f32 v25, v29, s24, v237
	v_med3_f32 v24, v24, s24, v237
	v_cvt_pk_fp8_f32 v19, v25, v24 op_sel:[0,0,1]
	v_fma_f32 v25, v128, v23, v0
	v_min_f32_e32 v26, 0x40e00000, v25
	v_add_co_u32_e32 v24, vcc, s69, v16
	v_mul_f32_e32 v25, 0xc01d265f, v26
	v_exp_f32_e32 v27, v25
	v_addc_co_u32_e32 v25, vcc, 0, v17, vcc
	global_store_dwordx2 v[24:25], v[18:19], off
	v_fma_f32 v24, v129, v23, v1
	v_min_f32_e32 v24, 0x40e00000, v24
	v_mul_f32_e32 v25, 0xc01d265f, v24
	v_exp_f32_e32 v25, v25
	v_add_f32_e32 v19, 1.0, v27
	v_rcp_f32_e32 v19, v19
	v_fma_f32 v27, v131, v23, v3
	v_add_f32_e32 v25, 1.0, v25
	v_rcp_f32_e32 v25, v25
	v_mul_f32_e32 v19, v26, v19
	v_min_f32_e32 v27, 0x40e00000, v27
	v_mul_f32_e32 v28, 0xc01d265f, v27
	v_mul_f32_e32 v24, v24, v25
	v_fma_f32 v25, v130, v23, v2
	v_min_f32_e32 v25, 0x40e00000, v25
	v_mul_f32_e32 v26, 0xc01d265f, v25
	v_exp_f32_e32 v26, v26
	v_exp_f32_e32 v28, v28
	v_fma_f32 v29, v121, v23, v13
	v_min_f32_e32 v29, 0x40e00000, v29
	v_add_f32_e32 v26, 1.0, v26
	v_rcp_f32_e32 v26, v26
	v_mul_f32_e32 v30, 0xc01d265f, v29
	v_exp_f32_e32 v30, v30
	v_fma_f32 v18, v124, v23, v8
	v_mul_f32_e32 v25, v25, v26
	v_add_f32_e32 v26, 1.0, v28
	v_rcp_f32_e32 v26, v26
	v_med3_f32 v18, v18, s23, v236
	v_add_f32_e32 v18, 1.0, v18
	v_mul_f32_e32 v18, v18, v19
	v_mul_f32_e32 v26, v27, v26
	v_fma_f32 v27, v120, v23, v12
;     __device__ __forceinline__ void operator()(const f32x4 (&acc)[2][2][4][2], const Unit& u, int wr, int wc, int fr, int fq) const {
;     ...
; #pragma unroll
;         for (int ai = 0; ai < 2; ++ai)
; #pragma unroll
;             for (int m = 0; m < 4; ++m) { const int r = row0 + ai * 128 + m * 16; const float rs = rsb[ai * 4 + m];
;                 float a[8];
; #pragma unroll
;                 for (int j = 0; j < 8; ++j) { const float gb = j < 4 ? g0[j & 3] : g1[j & 3], lb = j < 4 ? l0[j & 3] : l1[j & 3];
;                     const float gl = fminf(acc[ai][0][m][j >> 2][j & 3] * rs + gb, 7.0f), ln = fminf(fmaxf(acc[ai][1][m][j >> 2][j & 3] * rs + lb, -7.0f), 7.0f);
;                     a[j] = gl * __builtin_amdgcn_rcpf(1.0f + __builtin_amdgcn_exp2f(-1.702f * 1.4426950408889634f * gl)) * (ln + 1.0f); }
;                 v2u w; w.x = pk4_fp8(a[0], a[1], a[2], a[3]); w.y = pk4_fp8(a[4], a[5], a[6], a[7]);
;                 *(v2u*)(ACT + ((size_t)u.z * 256 + r) * FF + c0) = w; }
	v_min_f32_e32 v27, 0x40e00000, v27
	v_mul_f32_e32 v28, 0xc01d265f, v27
	v_exp_f32_e32 v28, v28
	v_fma_f32 v19, v125, v23, v9
	v_med3_f32 v19, v19, s23, v236
	v_add_f32_e32 v19, 1.0, v19
	v_add_f32_e32 v28, 1.0, v28
	v_rcp_f32_e32 v28, v28
	v_mul_f32_e32 v19, v19, v24
	v_fma_f32 v24, v126, v23, v10
	v_med3_f32 v24, v24, s23, v236
	v_mul_f32_e32 v27, v27, v28
	v_add_f32_e32 v28, 1.0, v30
	v_rcp_f32_e32 v28, v28
	v_add_f32_e32 v24, 1.0, v24
	v_mul_f32_e32 v24, v24, v25
	v_fma_f32 v25, v127, v23, v11
	v_mul_f32_e32 v28, v29, v28
	v_fma_f32 v29, v122, v23, v14
	v_min_f32_e32 v29, 0x40e00000, v29
	v_mul_f32_e32 v30, 0xc01d265f, v29
	v_exp_f32_e32 v30, v30
	v_fma_f32 v31, v123, v23, v15
	v_med3_f32 v25, v25, s23, v236
	v_min_f32_e32 v31, 0x40e00000, v31
	v_add_f32_e32 v25, 1.0, v25
	v_add_f32_e32 v30, 1.0, v30
	v_mul_f32_e32 v32, 0xc01d265f, v31
	v_mul_f32_e32 v25, v25, v26
	v_fma_f32 v26, v116, v23, v4
	v_rcp_f32_e32 v30, v30
	v_exp_f32_e32 v32, v32
	v_med3_f32 v26, v26, s23, v236
	v_add_f32_e32 v26, 1.0, v26
	v_mul_f32_e32 v26, v26, v27
	v_fma_f32 v27, v117, v23, v5
	v_med3_f32 v27, v27, s23, v236
	v_mul_f32_e32 v29, v29, v30
	v_add_f32_e32 v30, 1.0, v32
	v_add_f32_e32 v27, 1.0, v27
	v_rcp_f32_e32 v30, v30
	v_mul_f32_e32 v27, v27, v28
	v_fma_f32 v28, v118, v23, v6
	v_med3_f32 v28, v28, s23, v236
	v_fma_f32 v23, v119, v23, v7
	v_add_f32_e32 v28, 1.0, v28
	v_med3_f32 v23, v23, s23, v236
	v_mul_f32_e32 v28, v28, v29
	v_mul_f32_e32 v29, v31, v30
	v_add_f32_e32 v23, 1.0, v23
	v_mul_f32_e32 v23, v23, v29
	v_med3_f32 v29, v18, s24, v237
	v_med3_f32 v19, v19, s24, v237
	v_mov_b32_e32 v18, v65
	v_cvt_pk_fp8_f32 v18, v29, v19
	v_med3_f32 v26, v26, s24, v237
	v_med3_f32 v27, v27, s24, v237
	v_mov_b32_e32 v19, v65
	v_cvt_pk_fp8_f32 v19, v26, v27
	v_med3_f32 v24, v24, s24, v237
	v_med3_f32 v25, v25, s24, v237
	v_cvt_pk_fp8_f32 v18, v24, v25 op_sel:[0,0,1]
	v_med3_f32 v24, v28, s24, v237
	v_med3_f32 v23, v23, s24, v237
	v_cvt_pk_fp8_f32 v19, v24, v23 op_sel:[0,0,1]
	v_fma_f32 v23, v112, v22, v0
	v_min_f32_e32 v23, 0x40e00000, v23
	s_mov_b32 s4, 0x40000
	v_mul_f32_e32 v25, 0xc01d265f, v23
	v_add_co_u32_e32 v24, vcc, s4, v16
	v_exp_f32_e32 v26, v25
	s_nop 0
	v_addc_co_u32_e32 v25, vcc, 0, v17, vcc
	global_store_dwordx2 v[24:25], v[18:19], off
	v_fma_f32 v24, v113, v22, v1
	v_min_f32_e32 v24, 0x40e00000, v24
	v_add_f32_e32 v19, 1.0, v26
	v_mul_f32_e32 v25, 0xc01d265f, v24
	v_rcp_f32_e32 v19, v19
	v_exp_f32_e32 v25, v25
	v_fma_f32 v26, v115, v22, v3
	v_min_f32_e32 v26, 0x40e00000, v26
	v_mul_f32_e32 v19, v23, v19
	v_add_f32_e32 v23, 1.0, v25
	v_rcp_f32_e32 v23, v23
	v_mul_f32_e32 v27, 0xc01d265f, v26
	v_exp_f32_e32 v27, v27
	v_fma_f32 v28, v105, v22, v13
	v_mul_f32_e32 v23, v24, v23
	v_fma_f32 v24, v114, v22, v2
	v_min_f32_e32 v24, 0x40e00000, v24
	v_mul_f32_e32 v25, 0xc01d265f, v24
	v_exp_f32_e32 v25, v25
	v_min_f32_e32 v28, 0x40e00000, v28
	v_mul_f32_e32 v29, 0xc01d265f, v28
	v_exp_f32_e32 v29, v29
	v_add_f32_e32 v25, 1.0, v25
	v_rcp_f32_e32 v25, v25
	v_fma_f32 v18, v108, v22, v8
	v_med3_f32 v18, v18, s23, v236
	v_add_f32_e32 v18, 1.0, v18
	v_mul_f32_e32 v24, v24, v25
	v_add_f32_e32 v25, 1.0, v27
	v_rcp_f32_e32 v25, v25
	v_mul_f32_e32 v18, v18, v19
	v_fma_f32 v19, v109, v22, v9
	v_med3_f32 v19, v19, s23, v236
	v_mul_f32_e32 v25, v26, v25
	v_fma_f32 v26, v104, v22, v12
	v_min_f32_e32 v26, 0x40e00000, v26
	v_mul_f32_e32 v27, 0xc01d265f, v26
	v_exp_f32_e32 v27, v27
	v_add_f32_e32 v19, 1.0, v19
	v_mul_f32_e32 v19, v19, v23
	v_fma_f32 v23, v110, v22, v10
	v_add_f32_e32 v27, 1.0, v27
	v_rcp_f32_e32 v27, v27
	v_med3_f32 v23, v23, s23, v236
	v_add_f32_e32 v23, 1.0, v23
	v_mul_f32_e32 v23, v23, v24
	v_mul_f32_e32 v26, v26, v27
	v_add_f32_e32 v27, 1.0, v29
	v_rcp_f32_e32 v27, v27
	v_fma_f32 v24, v111, v22, v11
	v_fma_f32 v30, v107, v22, v15
	v_med3_f32 v24, v24, s23, v236
	v_mul_f32_e32 v27, v28, v27
	v_fma_f32 v28, v106, v22, v14
	v_min_f32_e32 v28, 0x40e00000, v28
	v_mul_f32_e32 v29, 0xc01d265f, v28
	v_exp_f32_e32 v29, v29
	v_min_f32_e32 v30, 0x40e00000, v30
	v_add_f32_e32 v24, 1.0, v24
	v_mul_f32_e32 v31, 0xc01d265f, v30
	v_add_f32_e32 v29, 1.0, v29
	v_mul_f32_e32 v24, v24, v25
	v_fma_f32 v25, v100, v22, v4
	v_rcp_f32_e32 v29, v29
	v_exp_f32_e32 v31, v31
	v_med3_f32 v25, v25, s23, v236
	v_add_f32_e32 v25, 1.0, v25
	v_mul_f32_e32 v25, v25, v26
	v_fma_f32 v26, v101, v22, v5
	v_med3_f32 v26, v26, s23, v236
	v_mul_f32_e32 v28, v28, v29
	v_add_f32_e32 v29, 1.0, v31
	v_add_f32_e32 v26, 1.0, v26
	v_rcp_f32_e32 v29, v29
	v_mul_f32_e32 v26, v26, v27
	v_fma_f32 v27, v102, v22, v6
	v_med3_f32 v27, v27, s23, v236
	v_fma_f32 v22, v103, v22, v7
	v_add_f32_e32 v27, 1.0, v27
	v_med3_f32 v22, v22, s23, v236
	v_mul_f32_e32 v27, v27, v28
	v_mul_f32_e32 v28, v30, v29
	v_add_f32_e32 v22, 1.0, v22
	v_mul_f32_e32 v22, v22, v28
	v_med3_f32 v28, v18, s24, v237
	v_med3_f32 v19, v19, s24, v237
	v_mov_b32_e32 v18, v65
	v_cvt_pk_fp8_f32 v18, v28, v19
	v_med3_f32 v25, v25, s24, v237
	v_med3_f32 v26, v26, s24, v237
	v_mov_b32_e32 v19, v65
	v_cvt_pk_fp8_f32 v19, v25, v26
	v_med3_f32 v23, v23, s24, v237
	v_med3_f32 v24, v24, s24, v237
	v_cvt_pk_fp8_f32 v18, v23, v24 op_sel:[0,0,1]
	v_med3_f32 v23, v27, s24, v237
	v_med3_f32 v22, v22, s24, v237
	v_cvt_pk_fp8_f32 v19, v23, v22 op_sel:[0,0,1]
	v_fma_f32 v23, v96, v21, v0
	s_mov_b32 s4, 0x48000
	v_min_f32_e32 v24, 0x40e00000, v23
	v_add_co_u32_e32 v22, vcc, s4, v16
	v_mul_f32_e32 v23, 0xc01d265f, v24
	v_exp_f32_e32 v25, v23
	v_addc_co_u32_e32 v23, vcc, 0, v17, vcc
	global_store_dwordx2 v[22:23], v[18:19], off
	v_fma_f32 v22, v97, v21, v1
	v_min_f32_e32 v22, 0x40e00000, v22
	v_mul_f32_e32 v23, 0xc01d265f, v22
	v_exp_f32_e32 v23, v23
	v_add_f32_e32 v19, 1.0, v25
;     __device__ __forceinline__ void operator()(const f32x4 (&acc)[2][2][4][2], const Unit& u, int wr, int wc, int fr, int fq) const {
;     ...
; #pragma unroll
;         for (int ai = 0; ai < 2; ++ai)
; #pragma unroll
;             for (int m = 0; m < 4; ++m) { const int r = row0 + ai * 128 + m * 16; const float rs = rsb[ai * 4 + m];
;                 float a[8];
; #pragma unroll
;                 for (int j = 0; j < 8; ++j) { const float gb = j < 4 ? g0[j & 3] : g1[j & 3], lb = j < 4 ? l0[j & 3] : l1[j & 3];
;                     const float gl = fminf(acc[ai][0][m][j >> 2][j & 3] * rs + gb, 7.0f), ln = fminf(fmaxf(acc[ai][1][m][j >> 2][j & 3] * rs + lb, -7.0f), 7.0f);
;                     a[j] = gl * __builtin_amdgcn_rcpf(1.0f + __builtin_amdgcn_exp2f(-1.702f * 1.4426950408889634f * gl)) * (ln + 1.0f); }
;                 v2u w; w.x = pk4_fp8(a[0], a[1], a[2], a[3]); w.y = pk4_fp8(a[4], a[5], a[6], a[7]);
;                 *(v2u*)(ACT + ((size_t)u.z * 256 + r) * FF + c0) = w; }
;     __device__ __forceinline__ void done(const Unit& u) const { if (u.pm == (c & 7)) convert_share(); }
	v_rcp_f32_e32 v19, v19
	v_fma_f32 v25, v99, v21, v3
	v_add_f32_e32 v23, 1.0, v23
	v_rcp_f32_e32 v23, v23
	v_mul_f32_e32 v19, v24, v19
	v_min_f32_e32 v25, 0x40e00000, v25
	v_mul_f32_e32 v26, 0xc01d265f, v25
	v_mul_f32_e32 v22, v22, v23
	v_fma_f32 v23, v98, v21, v2
	v_min_f32_e32 v23, 0x40e00000, v23
	v_mul_f32_e32 v24, 0xc01d265f, v23
	v_exp_f32_e32 v24, v24
	v_exp_f32_e32 v26, v26
	v_fma_f32 v27, v89, v21, v13
	v_min_f32_e32 v27, 0x40e00000, v27
	v_add_f32_e32 v24, 1.0, v24
	v_rcp_f32_e32 v24, v24
	v_mul_f32_e32 v28, 0xc01d265f, v27
	v_exp_f32_e32 v28, v28
	v_fma_f32 v18, v92, v21, v8
	v_mul_f32_e32 v23, v23, v24
	v_add_f32_e32 v24, 1.0, v26
	v_rcp_f32_e32 v24, v24
	v_med3_f32 v18, v18, s23, v236
	v_add_f32_e32 v18, 1.0, v18
	v_mul_f32_e32 v18, v18, v19
	v_mul_f32_e32 v24, v25, v24
	v_fma_f32 v25, v88, v21, v12
	v_min_f32_e32 v25, 0x40e00000, v25
	v_mul_f32_e32 v26, 0xc01d265f, v25
	v_exp_f32_e32 v26, v26
	v_fma_f32 v19, v93, v21, v9
	v_med3_f32 v19, v19, s23, v236
	v_add_f32_e32 v19, 1.0, v19
	v_add_f32_e32 v26, 1.0, v26
	v_rcp_f32_e32 v26, v26
	v_mul_f32_e32 v19, v19, v22
	v_fma_f32 v22, v94, v21, v10
	v_med3_f32 v22, v22, s23, v236
	v_mul_f32_e32 v25, v25, v26
	v_add_f32_e32 v26, 1.0, v28
	v_rcp_f32_e32 v26, v26
	v_add_f32_e32 v22, 1.0, v22
	v_mul_f32_e32 v22, v22, v23
	v_fma_f32 v23, v95, v21, v11
	v_mul_f32_e32 v26, v27, v26
	v_fma_f32 v27, v90, v21, v14
	v_min_f32_e32 v27, 0x40e00000, v27
	v_mul_f32_e32 v28, 0xc01d265f, v27
	v_exp_f32_e32 v28, v28
	v_fma_f32 v29, v91, v21, v15
	v_med3_f32 v23, v23, s23, v236
	v_min_f32_e32 v29, 0x40e00000, v29
	v_add_f32_e32 v23, 1.0, v23
	v_add_f32_e32 v28, 1.0, v28
	v_mul_f32_e32 v30, 0xc01d265f, v29
	v_mul_f32_e32 v23, v23, v24
	v_fma_f32 v24, v84, v21, v4
	v_rcp_f32_e32 v28, v28
	v_exp_f32_e32 v30, v30
	v_med3_f32 v24, v24, s23, v236
	v_add_f32_e32 v24, 1.0, v24
	v_mul_f32_e32 v24, v24, v25
	v_fma_f32 v25, v85, v21, v5
	v_med3_f32 v25, v25, s23, v236
	v_mul_f32_e32 v27, v27, v28
	v_add_f32_e32 v28, 1.0, v30
	v_add_f32_e32 v25, 1.0, v25
	v_rcp_f32_e32 v28, v28
	v_mul_f32_e32 v25, v25, v26
	v_fma_f32 v26, v86, v21, v6
	v_med3_f32 v26, v26, s23, v236
	v_fma_f32 v21, v87, v21, v7
	v_add_f32_e32 v26, 1.0, v26
	v_med3_f32 v21, v21, s23, v236
	v_mul_f32_e32 v26, v26, v27
	v_mul_f32_e32 v27, v29, v28
	v_add_f32_e32 v21, 1.0, v21
	v_mul_f32_e32 v21, v21, v27
	v_med3_f32 v27, v18, s24, v237
	v_med3_f32 v19, v19, s24, v237
	v_mov_b32_e32 v18, v65
	v_cvt_pk_fp8_f32 v18, v27, v19
	v_med3_f32 v24, v24, s24, v237
	v_med3_f32 v25, v25, s24, v237
	v_mov_b32_e32 v19, v65
	v_cvt_pk_fp8_f32 v19, v24, v25
	v_mul_f32_e32 v20, 0x3b800000, v20
	v_med3_f32 v22, v22, s24, v237
	v_med3_f32 v23, v23, s24, v237
	v_fma_f32 v14, v74, v20, v14
	v_cvt_pk_fp8_f32 v18, v22, v23 op_sel:[0,0,1]
	v_med3_f32 v22, v26, s24, v237
	v_med3_f32 v21, v21, s24, v237
	v_min_f32_e32 v14, 0x40e00000, v14
	v_cvt_pk_fp8_f32 v19, v22, v21 op_sel:[0,0,1]
	v_mul_f32_e32 v21, 0xc01d265f, v14
	v_exp_f32_e32 v21, v21
	s_mov_b32 s4, 0x50000
	v_add_co_u32_e32 v22, vcc, s4, v16
	v_fma_f32 v13, v73, v20, v13
	s_nop 0
	v_addc_co_u32_e32 v23, vcc, 0, v17, vcc
	global_store_dwordx2 v[22:23], v[18:19], off
	v_add_f32_e32 v18, 1.0, v21
	v_rcp_f32_e32 v18, v18
	v_min_f32_e32 v13, 0x40e00000, v13
	v_fma_f32 v6, v70, v20, v6
	v_med3_f32 v6, v6, s23, v236
	v_mul_f32_e32 v14, v14, v18
	v_mul_f32_e32 v18, 0xc01d265f, v13
	v_exp_f32_e32 v18, v18
	v_add_f32_e32 v6, 1.0, v6
	v_fma_f32 v12, v72, v20, v12
	v_mul_f32_e32 v6, v6, v14
	v_add_f32_e32 v14, 1.0, v18
	v_min_f32_e32 v12, 0x40e00000, v12
	v_rcp_f32_e32 v14, v14
	v_mul_f32_e32 v18, 0xc01d265f, v12
	v_exp_f32_e32 v18, v18
	v_fma_f32 v5, v69, v20, v5
	v_med3_f32 v5, v5, s23, v236
	v_add_f32_e32 v5, 1.0, v5
	v_mul_f32_e32 v13, v13, v14
	v_mul_f32_e32 v5, v5, v13
	v_add_f32_e32 v13, 1.0, v18
	v_rcp_f32_e32 v13, v13
	v_fma_f32 v3, v83, v20, v3
	v_min_f32_e32 v3, 0x40e00000, v3
	v_fma_f32 v4, v68, v20, v4
	v_mul_f32_e32 v12, v12, v13
	v_mul_f32_e32 v13, 0xc01d265f, v3
	v_exp_f32_e32 v13, v13
	v_med3_f32 v4, v4, s23, v236
	v_add_f32_e32 v4, 1.0, v4
	v_fma_f32 v2, v82, v20, v2
	v_mul_f32_e32 v4, v4, v12
	v_add_f32_e32 v12, 1.0, v13
	v_min_f32_e32 v2, 0x40e00000, v2
	v_rcp_f32_e32 v12, v12
	v_mul_f32_e32 v13, 0xc01d265f, v2
	v_exp_f32_e32 v13, v13
	v_fma_f32 v11, v79, v20, v11
	v_med3_f32 v11, v11, s23, v236
	v_add_f32_e32 v11, 1.0, v11
	v_mul_f32_e32 v3, v3, v12
	v_mul_f32_e32 v3, v11, v3
	v_add_f32_e32 v11, 1.0, v13
	v_rcp_f32_e32 v11, v11
	v_fma_f32 v10, v78, v20, v10
	v_med3_f32 v10, v10, s23, v236
	v_fma_f32 v1, v81, v20, v1
	v_add_f32_e32 v10, 1.0, v10
	v_mul_f32_e32 v2, v2, v11
	v_min_f32_e32 v1, 0x40e00000, v1
	v_mul_f32_e32 v2, v10, v2
	v_mul_f32_e32 v10, 0xc01d265f, v1
	v_exp_f32_e32 v10, v10
	v_fmac_f32_e32 v0, v80, v20
	v_min_f32_e32 v0, 0x40e00000, v0
	v_mul_f32_e32 v11, 0xc01d265f, v0
	v_add_f32_e32 v10, 1.0, v10
	v_rcp_f32_e32 v10, v10
	v_exp_f32_e32 v11, v11
	v_fma_f32 v9, v77, v20, v9
	v_med3_f32 v9, v9, s23, v236
	v_fmac_f32_e32 v15, v75, v20
	v_add_f32_e32 v9, 1.0, v9
	v_mul_f32_e32 v1, v1, v10
	v_min_f32_e32 v10, 0x40e00000, v15
	v_mul_f32_e32 v1, v9, v1
	v_add_f32_e32 v9, 1.0, v11
	v_mul_f32_e32 v11, 0xc01d265f, v10
	v_rcp_f32_e32 v9, v9
	v_exp_f32_e32 v11, v11
	v_fmac_f32_e32 v8, v76, v20
	v_med3_f32 v8, v8, s23, v236
	v_mul_f32_e32 v0, v0, v9
	v_add_f32_e32 v9, 1.0, v11
	v_rcp_f32_e32 v9, v9
	v_fmac_f32_e32 v7, v71, v20
	v_add_f32_e32 v8, 1.0, v8
	v_med3_f32 v7, v7, s23, v236
	v_mul_f32_e32 v0, v8, v0
	v_mul_f32_e32 v8, v10, v9
	v_add_f32_e32 v7, 1.0, v7
	v_mul_f32_e32 v7, v7, v8
	v_med3_f32 v8, v0, s24, v237
	v_med3_f32 v1, v1, s24, v237
	v_mov_b32_e32 v0, v65
	v_cvt_pk_fp8_f32 v0, v8, v1
	v_med3_f32 v4, v4, s24, v237
	v_med3_f32 v5, v5, s24, v237
	v_mov_b32_e32 v1, v65
	v_cvt_pk_fp8_f32 v1, v4, v5
	v_med3_f32 v2, v2, s24, v237
	v_med3_f32 v3, v3, s24, v237
	v_cvt_pk_fp8_f32 v0, v2, v3 op_sel:[0,0,1]
	v_med3_f32 v2, v6, s24, v237
	v_med3_f32 v3, v7, s24, v237
	v_cvt_pk_fp8_f32 v1, v2, v3 op_sel:[0,0,1]
	v_add_co_u32_e32 v2, vcc, 0x58000, v16
	s_nop 1
	v_addc_co_u32_e32 v3, vcc, 0, v17, vcc
	global_store_dwordx2 v[2:3], v[0:1], off
	s_cbranch_scc1 .LBB0_1541
; __device__ __forceinline__ int lane_id_now() { unsigned z = 0u; asm volatile("" : "+v"(z)); return (int)__builtin_amdgcn_mbcnt_hi(~0u, __builtin_amdgcn_mbcnt_lo(~0u, z)); }
; #define GAS __attribute__((address_space(1)))
; template <bool GAIN, bool NT = false> __device__ __forceinline__ void titem8_load(const TItem& d, int lane, f32x4 (&r)[16], f32x4 (&g)[4]) {
;     const int q = lane & 7, kg = lane >> 3; const unsigned lo = (unsigned)((16 * kg) * d.N + 4 * q) * 4u;
;     const GAS char* base = (const GAS char*)d.src;
; #pragma unroll
;     for (int j = 0; j < 16; ++j) { const GAS f32x4* p = (const GAS f32x4*)(base + (size_t)j * (size_t)d.N * 4 + lo); r[j] = NT ? __builtin_nontemporal_load(p) : *p; }
;     if constexpr (GAIN) { const GAS char* gb = (const GAS char*)d.gain; const unsigned go = (unsigned)(16 * kg) * 4u;
; #pragma unroll
;         for (int j4 = 0; j4 < 4; ++j4) g[j4] = *(const GAS f32x4*)(gb + 16 * j4 + go); }
;     asm volatile("" ::: "memory"); __builtin_amdgcn_sched_barrier(0);
; }
;     __device__ __forceinline__ void convert_share() const {
;         const int lane = lane_id_now(), gw = c * NWAVES + wave, NGW = G * NWAVES;
;         constexpr int NIT = E * (FF / 128) * (D / 32);
;         TSTREAM(NIT, dec_dn, TI8L_NT, TI8S_NT);
	v_readlane_b32 s0, v254, 26
	v_readlane_b32 s1, v254, 27
	v_mov_b32_e32 v0, v65
	s_andn2_b64 vcc, exec, s[0:1]
	s_cbranch_vccnz .LBB0_1541
	v_mbcnt_lo_u32_b32 v64, -1, 0
	v_mbcnt_hi_u32_b32 v64, -1, v64
	v_and_b32_e32 v194, 7, v64
	v_lshrrev_b32_e32 v195, 3, v64
	v_lshlrev_b32_e32 v246, 17, v195
	v_lshl_or_b32 v246, v194, 4, v246
	v_add_u32_e32 v247, 0x2000, v246
	v_add_u32_e32 v248, 0x4000, v246
	v_add_u32_e32 v249, 0x6000, v246
	v_lshlrev_b32_e32 v250, 13, v194
	v_lshl_or_b32 v250, v195, 4, v250
	v_add_u32_e32 v251, 0x1000, v250
	v_readlane_b32 s0, v254, 60
	v_readlane_b32 s4, v254, 4
	v_readlane_b32 s5, v254, 5
	s_nop 3
	s_lshr_b32 s1, s92, 3
	s_lshl_b32 s1, s1, 3
	s_add_i32 s0, s0, s1
	s_and_b32 s1, s92, 7
	s_lshr_b32 s2, s0, 6
	s_and_b32 s0, s0, 63
	s_lshl_b32 s35, s1, 26
	s_lshl_b32 s38, s2, 20
	s_add_i32 s35, s35, s38
	s_lshl_b32 s38, s0, 7
	s_add_i32 s35, s35, s38
	s_add_u32 s4, s4, s35
	s_addc_u32 s5, s5, 0
	s_add_u32 s6, s4, 0x8000
	s_addc_u32 s7, s5, 0
	s_add_u32 s8, s4, 0x10000
	s_addc_u32 s9, s5, 0
	s_add_u32 s38, s4, 0x18000
	s_addc_u32 s39, s5, 0
	s_lshl_b32 s35, s1, 24
	s_lshl_b32 s40, s0, 16
	s_add_i32 s35, s35, s40
	s_lshl_b32 s40, s2, 7
	s_add_i32 s35, s35, s40
	s_add_u32 s42, s78, 0x57dc8000
	s_addc_u32 s43, s79, 0
	s_add_u32 s42, s42, s35
	s_addc_u32 s43, s43, 0
	global_load_dwordx4 v[0:3], v246, s[4:5] nt
	global_load_dwordx4 v[4:7], v247, s[4:5] nt
	global_load_dwordx4 v[8:11], v248, s[4:5] nt
	global_load_dwordx4 v[12:15], v249, s[4:5] nt
	global_load_dwordx4 v[16:19], v246, s[6:7] nt
	global_load_dwordx4 v[20:23], v247, s[6:7] nt
	global_load_dwordx4 v[24:27], v248, s[6:7] nt
	global_load_dwordx4 v[28:31], v249, s[6:7] nt
	global_load_dwordx4 v[32:35], v246, s[8:9] nt
	global_load_dwordx4 v[36:39], v247, s[8:9] nt
	global_load_dwordx4 v[40:43], v248, s[8:9] nt
	global_load_dwordx4 v[44:47], v249, s[8:9] nt
	global_load_dwordx4 v[48:51], v246, s[38:39] nt
	global_load_dwordx4 v[52:55], v247, s[38:39] nt
	global_load_dwordx4 v[56:59], v248, s[38:39] nt
	global_load_dwordx4 v[60:63], v249, s[38:39] nt
	s_add_u32 s4, s4, 0x400000
	s_addc_u32 s5, s5, 0
	s_add_u32 s6, s6, 0x400000
	s_addc_u32 s7, s7, 0
	s_add_u32 s8, s8, 0x400000
	s_addc_u32 s9, s9, 0
	s_add_u32 s38, s38, 0x400000
	s_addc_u32 s39, s39, 0
	global_load_dwordx4 v[66:69], v246, s[4:5] nt
	global_load_dwordx4 v[70:73], v247, s[4:5] nt
	global_load_dwordx4 v[74:77], v248, s[4:5] nt
	global_load_dwordx4 v[78:81], v249, s[4:5] nt
	global_load_dwordx4 v[82:85], v246, s[6:7] nt
	global_load_dwordx4 v[86:89], v247, s[6:7] nt
	global_load_dwordx4 v[90:93], v248, s[6:7] nt
	global_load_dwordx4 v[94:97], v249, s[6:7] nt
	global_load_dwordx4 v[98:101], v246, s[8:9] nt
	global_load_dwordx4 v[102:105], v247, s[8:9] nt
	global_load_dwordx4 v[106:109], v248, s[8:9] nt
	global_load_dwordx4 v[110:113], v249, s[8:9] nt
	global_load_dwordx4 v[114:117], v246, s[38:39] nt
	global_load_dwordx4 v[118:121], v247, s[38:39] nt
	global_load_dwordx4 v[122:125], v248, s[38:39] nt
	global_load_dwordx4 v[126:129], v249, s[38:39] nt
	s_add_u32 s4, s4, 0x400000
	s_addc_u32 s5, s5, 0
	s_add_u32 s6, s6, 0x400000
	s_addc_u32 s7, s7, 0
	s_add_u32 s8, s8, 0x400000
	s_addc_u32 s9, s9, 0
	s_add_u32 s38, s38, 0x400000
	s_addc_u32 s39, s39, 0
	global_load_dwordx4 v[130:133], v246, s[4:5] nt
	global_load_dwordx4 v[134:137], v247, s[4:5] nt
	global_load_dwordx4 v[138:141], v248, s[4:5] nt
	global_load_dwordx4 v[142:145], v249, s[4:5] nt
	global_load_dwordx4 v[146:149], v246, s[6:7] nt
	global_load_dwordx4 v[150:153], v247, s[6:7] nt
	global_load_dwordx4 v[154:157], v248, s[6:7] nt
	global_load_dwordx4 v[158:161], v249, s[6:7] nt
	global_load_dwordx4 v[162:165], v246, s[8:9] nt
	global_load_dwordx4 v[166:169], v247, s[8:9] nt
	global_load_dwordx4 v[170:173], v248, s[8:9] nt
	global_load_dwordx4 v[174:177], v249, s[8:9] nt
	global_load_dwordx4 v[178:181], v246, s[38:39] nt
	global_load_dwordx4 v[182:185], v247, s[38:39] nt
	global_load_dwordx4 v[186:189], v248, s[38:39] nt
	global_load_dwordx4 v[190:193], v249, s[38:39] nt
	s_add_u32 s4, s4, 0x400000
	s_addc_u32 s5, s5, 0
	s_add_u32 s6, s6, 0x400000
	s_addc_u32 s7, s7, 0
	s_add_u32 s8, s8, 0x400000
	s_addc_u32 s9, s9, 0
	s_add_u32 s38, s38, 0x400000
	s_addc_u32 s39, s39, 0
	s_waitcnt vmcnt(32)
; #define GAS __attribute__((address_space(1)))
; template <bool GAIN, bool NT = false> __device__ __forceinline__ void titem8_load(const TItem& d, int lane, f32x4 (&r)[16], f32x4 (&g)[4]) {
;     const int q = lane & 7, kg = lane >> 3; const unsigned lo = (unsigned)((16 * kg) * d.N + 4 * q) * 4u;
;     const GAS char* base = (const GAS char*)d.src;
; #pragma unroll
;     for (int j = 0; j < 16; ++j) { const GAS f32x4* p = (const GAS f32x4*)(base + (size_t)j * (size_t)d.N * 4 + lo); r[j] = NT ? __builtin_nontemporal_load(p) : *p; }
;     if constexpr (GAIN) { const GAS char* gb = (const GAS char*)d.gain; const unsigned go = (unsigned)(16 * kg) * 4u;
; #pragma unroll
;         for (int j4 = 0; j4 < 4; ++j4) g[j4] = *(const GAS f32x4*)(gb + 16 * j4 + go); }
;     asm volatile("" ::: "memory"); __builtin_amdgcn_sched_barrier(0);
; }
; template <bool GAIN, bool NT = false> __device__ __forceinline__ void titem8_store(const TItem& d, int lane, const f32x4 (&r)[16], const f32x4 (&g)[4]) {
;     const int q = lane & 7, kg = lane >> 3; const unsigned lo = (unsigned)((4 * q) * d.ldk + 16 * kg);
;     GAS char* base = (GAS char*)d.dst;
;     f32x4 s[16];
; #pragma unroll
;     for (int j = 0; j < 16; ++j) s[j] = r[j] * ((GAIN ? g[j >> 2][j & 3] : 1.0f) * W8_SCALE);
; #pragma unroll
;     for (int i = 0; i < 4; ++i) { v4u w;
;         w.x = pk4_fp8w(s[0][i], s[1][i], s[2][i], s[3][i]); w.y = pk4_fp8w(s[4][i], s[5][i], s[6][i], s[7][i]);
;         w.z = pk4_fp8w(s[8][i], s[9][i], s[10][i], s[11][i]); w.w = pk4_fp8w(s[12][i], s[13][i], s[14][i], s[15][i]);
;         GAS v4u* p = (GAS v4u*)(base + (size_t)i * (size_t)d.ldk + lo);
;         if (NT) __builtin_nontemporal_store(w, p); else *p = w; }
; }
	v_pk_mul_f32 v[0:1], v[0:1], s[30:31] op_sel_hi:[1,0]
	v_pk_mul_f32 v[2:3], v[2:3], s[30:31] op_sel_hi:[1,0]
	v_pk_mul_f32 v[4:5], v[4:5], s[30:31] op_sel_hi:[1,0]
	v_pk_mul_f32 v[6:7], v[6:7], s[30:31] op_sel_hi:[1,0]
	v_pk_mul_f32 v[8:9], v[8:9], s[30:31] op_sel_hi:[1,0]
	v_pk_mul_f32 v[10:11], v[10:11], s[30:31] op_sel_hi:[1,0]
	v_pk_mul_f32 v[12:13], v[12:13], s[30:31] op_sel_hi:[1,0]
	v_pk_mul_f32 v[14:15], v[14:15], s[30:31] op_sel_hi:[1,0]
	v_pk_mul_f32 v[16:17], v[16:17], s[30:31] op_sel_hi:[1,0]
	v_pk_mul_f32 v[18:19], v[18:19], s[30:31] op_sel_hi:[1,0]
	v_pk_mul_f32 v[20:21], v[20:21], s[30:31] op_sel_hi:[1,0]
	v_pk_mul_f32 v[22:23], v[22:23], s[30:31] op_sel_hi:[1,0]
	v_pk_mul_f32 v[24:25], v[24:25], s[30:31] op_sel_hi:[1,0]
	v_pk_mul_f32 v[26:27], v[26:27], s[30:31] op_sel_hi:[1,0]
	v_pk_mul_f32 v[28:29], v[28:29], s[30:31] op_sel_hi:[1,0]
	v_pk_mul_f32 v[30:31], v[30:31], s[30:31] op_sel_hi:[1,0]
	v_pk_mul_f32 v[32:33], v[32:33], s[30:31] op_sel_hi:[1,0]
	v_pk_mul_f32 v[34:35], v[34:35], s[30:31] op_sel_hi:[1,0]
	v_pk_mul_f32 v[36:37], v[36:37], s[30:31] op_sel_hi:[1,0]
	v_pk_mul_f32 v[38:39], v[38:39], s[30:31] op_sel_hi:[1,0]
	v_pk_mul_f32 v[40:41], v[40:41], s[30:31] op_sel_hi:[1,0]
	v_pk_mul_f32 v[42:43], v[42:43], s[30:31] op_sel_hi:[1,0]
	v_pk_mul_f32 v[44:45], v[44:45], s[30:31] op_sel_hi:[1,0]
	v_pk_mul_f32 v[46:47], v[46:47], s[30:31] op_sel_hi:[1,0]
	v_pk_mul_f32 v[48:49], v[48:49], s[30:31] op_sel_hi:[1,0]
	v_pk_mul_f32 v[50:51], v[50:51], s[30:31] op_sel_hi:[1,0]
	v_pk_mul_f32 v[52:53], v[52:53], s[30:31] op_sel_hi:[1,0]
	v_pk_mul_f32 v[54:55], v[54:55], s[30:31] op_sel_hi:[1,0]
	v_pk_mul_f32 v[56:57], v[56:57], s[30:31] op_sel_hi:[1,0]
	v_pk_mul_f32 v[58:59], v[58:59], s[30:31] op_sel_hi:[1,0]
	v_pk_mul_f32 v[60:61], v[60:61], s[30:31] op_sel_hi:[1,0]
	v_pk_mul_f32 v[62:63], v[62:63], s[30:31] op_sel_hi:[1,0]
	v_med3_f32 v0, v0, s24, v237
	v_med3_f32 v1, v1, s24, v237
	v_med3_f32 v2, v2, s24, v237
	v_med3_f32 v3, v3, s24, v237
	v_med3_f32 v4, v4, s24, v237
	v_med3_f32 v5, v5, s24, v237
	v_med3_f32 v6, v6, s24, v237
	v_med3_f32 v7, v7, s24, v237
	v_med3_f32 v8, v8, s24, v237
	v_med3_f32 v9, v9, s24, v237
	v_med3_f32 v10, v10, s24, v237
	v_med3_f32 v11, v11, s24, v237
	v_med3_f32 v12, v12, s24, v237
	v_med3_f32 v13, v13, s24, v237
	v_med3_f32 v14, v14, s24, v237
	v_med3_f32 v15, v15, s24, v237
	v_med3_f32 v16, v16, s24, v237
	v_med3_f32 v17, v17, s24, v237
	v_med3_f32 v18, v18, s24, v237
	v_med3_f32 v19, v19, s24, v237
	v_med3_f32 v20, v20, s24, v237
	v_med3_f32 v21, v21, s24, v237
	v_med3_f32 v22, v22, s24, v237
	v_med3_f32 v23, v23, s24, v237
	v_med3_f32 v24, v24, s24, v237
	v_med3_f32 v25, v25, s24, v237
	v_med3_f32 v26, v26, s24, v237
	v_med3_f32 v27, v27, s24, v237
	v_med3_f32 v28, v28, s24, v237
	v_med3_f32 v29, v29, s24, v237
	v_med3_f32 v30, v30, s24, v237
	v_med3_f32 v31, v31, s24, v237
	v_med3_f32 v32, v32, s24, v237
	v_med3_f32 v33, v33, s24, v237
	v_med3_f32 v34, v34, s24, v237
	v_med3_f32 v35, v35, s24, v237
	v_med3_f32 v36, v36, s24, v237
	v_med3_f32 v37, v37, s24, v237
	v_med3_f32 v38, v38, s24, v237
	v_med3_f32 v39, v39, s24, v237
	v_med3_f32 v40, v40, s24, v237
	v_med3_f32 v41, v41, s24, v237
	v_med3_f32 v42, v42, s24, v237
	v_med3_f32 v43, v43, s24, v237
	v_med3_f32 v44, v44, s24, v237
	v_med3_f32 v45, v45, s24, v237
	v_med3_f32 v46, v46, s24, v237
	v_med3_f32 v47, v47, s24, v237
	v_med3_f32 v48, v48, s24, v237
	v_med3_f32 v49, v49, s24, v237
	v_med3_f32 v50, v50, s24, v237
	v_med3_f32 v51, v51, s24, v237
	v_med3_f32 v52, v52, s24, v237
	v_med3_f32 v53, v53, s24, v237
	v_med3_f32 v54, v54, s24, v237
	v_med3_f32 v55, v55, s24, v237
	v_med3_f32 v56, v56, s24, v237
	v_med3_f32 v57, v57, s24, v237
	v_med3_f32 v58, v58, s24, v237
	v_med3_f32 v59, v59, s24, v237
	v_med3_f32 v60, v60, s24, v237
	v_med3_f32 v61, v61, s24, v237
	v_med3_f32 v62, v62, s24, v237
	v_med3_f32 v63, v63, s24, v237
	v_cvt_pk_fp8_f32 v0, v0, v4
	v_cvt_pk_fp8_f32 v0, v8, v12 op_sel:[0,0,1]
	v_cvt_pk_fp8_f32 v4, v1, v5
	v_cvt_pk_fp8_f32 v4, v9, v13 op_sel:[0,0,1]
	v_cvt_pk_fp8_f32 v8, v2, v6
	v_cvt_pk_fp8_f32 v8, v10, v14 op_sel:[0,0,1]
	v_cvt_pk_fp8_f32 v12, v3, v7
	v_cvt_pk_fp8_f32 v12, v11, v15 op_sel:[0,0,1]
	v_cvt_pk_fp8_f32 v1, v16, v20
	v_cvt_pk_fp8_f32 v1, v24, v28 op_sel:[0,0,1]
	v_cvt_pk_fp8_f32 v5, v17, v21
	v_cvt_pk_fp8_f32 v5, v25, v29 op_sel:[0,0,1]
	v_cvt_pk_fp8_f32 v9, v18, v22
	v_cvt_pk_fp8_f32 v9, v26, v30 op_sel:[0,0,1]
	v_cvt_pk_fp8_f32 v13, v19, v23
	v_cvt_pk_fp8_f32 v13, v27, v31 op_sel:[0,0,1]
	v_cvt_pk_fp8_f32 v2, v32, v36
	v_cvt_pk_fp8_f32 v2, v40, v44 op_sel:[0,0,1]
	v_cvt_pk_fp8_f32 v6, v33, v37
	v_cvt_pk_fp8_f32 v6, v41, v45 op_sel:[0,0,1]
	v_cvt_pk_fp8_f32 v10, v34, v38
	v_cvt_pk_fp8_f32 v10, v42, v46 op_sel:[0,0,1]
	v_cvt_pk_fp8_f32 v14, v35, v39
	v_cvt_pk_fp8_f32 v14, v43, v47 op_sel:[0,0,1]
	v_cvt_pk_fp8_f32 v3, v48, v52
	v_cvt_pk_fp8_f32 v3, v56, v60 op_sel:[0,0,1]
	v_cvt_pk_fp8_f32 v7, v49, v53
	v_cvt_pk_fp8_f32 v7, v57, v61 op_sel:[0,0,1]
	v_cvt_pk_fp8_f32 v11, v50, v54
	v_cvt_pk_fp8_f32 v11, v58, v62 op_sel:[0,0,1]
	v_cvt_pk_fp8_f32 v15, v51, v55
	v_cvt_pk_fp8_f32 v15, v59, v63 op_sel:[0,0,1]
	global_store_dwordx4 v250, v[0:3], s[42:43] nt
	global_store_dwordx4 v250, v[4:7], s[42:43] offset:2048 nt
	global_store_dwordx4 v251, v[8:11], s[42:43] nt
	global_store_dwordx4 v251, v[12:15], s[42:43] offset:2048 nt
	s_add_u32 s42, s42, 0x200
	s_addc_u32 s43, s43, 0
	global_load_dwordx4 v[0:3], v246, s[4:5] nt
	global_load_dwordx4 v[4:7], v247, s[4:5] nt
	global_load_dwordx4 v[8:11], v248, s[4:5] nt
	global_load_dwordx4 v[12:15], v249, s[4:5] nt
	global_load_dwordx4 v[16:19], v246, s[6:7] nt
	global_load_dwordx4 v[20:23], v247, s[6:7] nt
	global_load_dwordx4 v[24:27], v248, s[6:7] nt
	global_load_dwordx4 v[28:31], v249, s[6:7] nt
	global_load_dwordx4 v[32:35], v246, s[8:9] nt
	global_load_dwordx4 v[36:39], v247, s[8:9] nt
	global_load_dwordx4 v[40:43], v248, s[8:9] nt
	global_load_dwordx4 v[44:47], v249, s[8:9] nt
	global_load_dwordx4 v[48:51], v246, s[38:39] nt
	global_load_dwordx4 v[52:55], v247, s[38:39] nt
	global_load_dwordx4 v[56:59], v248, s[38:39] nt
	global_load_dwordx4 v[60:63], v249, s[38:39] nt
	s_add_u32 s4, s4, 0x400000
	s_addc_u32 s5, s5, 0
	s_add_u32 s6, s6, 0x400000
	s_addc_u32 s7, s7, 0
	s_add_u32 s8, s8, 0x400000
	s_addc_u32 s9, s9, 0
	s_add_u32 s38, s38, 0x400000
	s_addc_u32 s39, s39, 0
	s_waitcnt vmcnt(36)
; #define GAS __attribute__((address_space(1)))
; template <bool GAIN, bool NT = false> __device__ __forceinline__ void titem8_load(const TItem& d, int lane, f32x4 (&r)[16], f32x4 (&g)[4]) {
;     const int q = lane & 7, kg = lane >> 3; const unsigned lo = (unsigned)((16 * kg) * d.N + 4 * q) * 4u;
;     const GAS char* base = (const GAS char*)d.src;
; #pragma unroll
;     for (int j = 0; j < 16; ++j) { const GAS f32x4* p = (const GAS f32x4*)(base + (size_t)j * (size_t)d.N * 4 + lo); r[j] = NT ? __builtin_nontemporal_load(p) : *p; }
;     if constexpr (GAIN) { const GAS char* gb = (const GAS char*)d.gain; const unsigned go = (unsigned)(16 * kg) * 4u;
; #pragma unroll
;         for (int j4 = 0; j4 < 4; ++j4) g[j4] = *(const GAS f32x4*)(gb + 16 * j4 + go); }
;     asm volatile("" ::: "memory"); __builtin_amdgcn_sched_barrier(0);
; }
; template <bool GAIN, bool NT = false> __device__ __forceinline__ void titem8_store(const TItem& d, int lane, const f32x4 (&r)[16], const f32x4 (&g)[4]) {
;     const int q = lane & 7, kg = lane >> 3; const unsigned lo = (unsigned)((4 * q) * d.ldk + 16 * kg);
;     GAS char* base = (GAS char*)d.dst;
;     f32x4 s[16];
; #pragma unroll
;     for (int j = 0; j < 16; ++j) s[j] = r[j] * ((GAIN ? g[j >> 2][j & 3] : 1.0f) * W8_SCALE);
; #pragma unroll
;     for (int i = 0; i < 4; ++i) { v4u w;
;         w.x = pk4_fp8w(s[0][i], s[1][i], s[2][i], s[3][i]); w.y = pk4_fp8w(s[4][i], s[5][i], s[6][i], s[7][i]);
;         w.z = pk4_fp8w(s[8][i], s[9][i], s[10][i], s[11][i]); w.w = pk4_fp8w(s[12][i], s[13][i], s[14][i], s[15][i]);
;         GAS v4u* p = (GAS v4u*)(base + (size_t)i * (size_t)d.ldk + lo);
;         if (NT) __builtin_nontemporal_store(w, p); else *p = w; }
; }
	v_pk_mul_f32 v[66:67], v[66:67], s[30:31] op_sel_hi:[1,0]
	v_pk_mul_f32 v[68:69], v[68:69], s[30:31] op_sel_hi:[1,0]
	v_pk_mul_f32 v[70:71], v[70:71], s[30:31] op_sel_hi:[1,0]
	v_pk_mul_f32 v[72:73], v[72:73], s[30:31] op_sel_hi:[1,0]
	v_pk_mul_f32 v[74:75], v[74:75], s[30:31] op_sel_hi:[1,0]
	v_pk_mul_f32 v[76:77], v[76:77], s[30:31] op_sel_hi:[1,0]
	v_pk_mul_f32 v[78:79], v[78:79], s[30:31] op_sel_hi:[1,0]
	v_pk_mul_f32 v[80:81], v[80:81], s[30:31] op_sel_hi:[1,0]
	v_pk_mul_f32 v[82:83], v[82:83], s[30:31] op_sel_hi:[1,0]
	v_pk_mul_f32 v[84:85], v[84:85], s[30:31] op_sel_hi:[1,0]
	v_pk_mul_f32 v[86:87], v[86:87], s[30:31] op_sel_hi:[1,0]
	v_pk_mul_f32 v[88:89], v[88:89], s[30:31] op_sel_hi:[1,0]
	v_pk_mul_f32 v[90:91], v[90:91], s[30:31] op_sel_hi:[1,0]
	v_pk_mul_f32 v[92:93], v[92:93], s[30:31] op_sel_hi:[1,0]
	v_pk_mul_f32 v[94:95], v[94:95], s[30:31] op_sel_hi:[1,0]
	v_pk_mul_f32 v[96:97], v[96:97], s[30:31] op_sel_hi:[1,0]
	v_pk_mul_f32 v[98:99], v[98:99], s[30:31] op_sel_hi:[1,0]
	v_pk_mul_f32 v[100:101], v[100:101], s[30:31] op_sel_hi:[1,0]
	v_pk_mul_f32 v[102:103], v[102:103], s[30:31] op_sel_hi:[1,0]
	v_pk_mul_f32 v[104:105], v[104:105], s[30:31] op_sel_hi:[1,0]
	v_pk_mul_f32 v[106:107], v[106:107], s[30:31] op_sel_hi:[1,0]
	v_pk_mul_f32 v[108:109], v[108:109], s[30:31] op_sel_hi:[1,0]
	v_pk_mul_f32 v[110:111], v[110:111], s[30:31] op_sel_hi:[1,0]
	v_pk_mul_f32 v[112:113], v[112:113], s[30:31] op_sel_hi:[1,0]
	v_pk_mul_f32 v[114:115], v[114:115], s[30:31] op_sel_hi:[1,0]
	v_pk_mul_f32 v[116:117], v[116:117], s[30:31] op_sel_hi:[1,0]
	v_pk_mul_f32 v[118:119], v[118:119], s[30:31] op_sel_hi:[1,0]
	v_pk_mul_f32 v[120:121], v[120:121], s[30:31] op_sel_hi:[1,0]
	v_pk_mul_f32 v[122:123], v[122:123], s[30:31] op_sel_hi:[1,0]
	v_pk_mul_f32 v[124:125], v[124:125], s[30:31] op_sel_hi:[1,0]
	v_pk_mul_f32 v[126:127], v[126:127], s[30:31] op_sel_hi:[1,0]
	v_pk_mul_f32 v[128:129], v[128:129], s[30:31] op_sel_hi:[1,0]
	v_med3_f32 v66, v66, s24, v237
	v_med3_f32 v67, v67, s24, v237
	v_med3_f32 v68, v68, s24, v237
	v_med3_f32 v69, v69, s24, v237
	v_med3_f32 v70, v70, s24, v237
	v_med3_f32 v71, v71, s24, v237
	v_med3_f32 v72, v72, s24, v237
	v_med3_f32 v73, v73, s24, v237
	v_med3_f32 v74, v74, s24, v237
	v_med3_f32 v75, v75, s24, v237
	v_med3_f32 v76, v76, s24, v237
	v_med3_f32 v77, v77, s24, v237
	v_med3_f32 v78, v78, s24, v237
	v_med3_f32 v79, v79, s24, v237
	v_med3_f32 v80, v80, s24, v237
	v_med3_f32 v81, v81, s24, v237
	v_med3_f32 v82, v82, s24, v237
	v_med3_f32 v83, v83, s24, v237
	v_med3_f32 v84, v84, s24, v237
	v_med3_f32 v85, v85, s24, v237
	v_med3_f32 v86, v86, s24, v237
	v_med3_f32 v87, v87, s24, v237
	v_med3_f32 v88, v88, s24, v237
	v_med3_f32 v89, v89, s24, v237
	v_med3_f32 v90, v90, s24, v237
	v_med3_f32 v91, v91, s24, v237
	v_med3_f32 v92, v92, s24, v237
	v_med3_f32 v93, v93, s24, v237
	v_med3_f32 v94, v94, s24, v237
	v_med3_f32 v95, v95, s24, v237
	v_med3_f32 v96, v96, s24, v237
	v_med3_f32 v97, v97, s24, v237
	v_med3_f32 v98, v98, s24, v237
	v_med3_f32 v99, v99, s24, v237
	v_med3_f32 v100, v100, s24, v237
	v_med3_f32 v101, v101, s24, v237
	v_med3_f32 v102, v102, s24, v237
	v_med3_f32 v103, v103, s24, v237
	v_med3_f32 v104, v104, s24, v237
	v_med3_f32 v105, v105, s24, v237
	v_med3_f32 v106, v106, s24, v237
	v_med3_f32 v107, v107, s24, v237
	v_med3_f32 v108, v108, s24, v237
	v_med3_f32 v109, v109, s24, v237
	v_med3_f32 v110, v110, s24, v237
	v_med3_f32 v111, v111, s24, v237
	v_med3_f32 v112, v112, s24, v237
	v_med3_f32 v113, v113, s24, v237
	v_med3_f32 v114, v114, s24, v237
	v_med3_f32 v115, v115, s24, v237
	v_med3_f32 v116, v116, s24, v237
	v_med3_f32 v117, v117, s24, v237
	v_med3_f32 v118, v118, s24, v237
	v_med3_f32 v119, v119, s24, v237
	v_med3_f32 v120, v120, s24, v237
	v_med3_f32 v121, v121, s24, v237
	v_med3_f32 v122, v122, s24, v237
	v_med3_f32 v123, v123, s24, v237
	v_med3_f32 v124, v124, s24, v237
	v_med3_f32 v125, v125, s24, v237
	v_med3_f32 v126, v126, s24, v237
	v_med3_f32 v127, v127, s24, v237
	v_med3_f32 v128, v128, s24, v237
	v_med3_f32 v129, v129, s24, v237
	v_cvt_pk_fp8_f32 v66, v66, v70
	v_cvt_pk_fp8_f32 v66, v74, v78 op_sel:[0,0,1]
	v_cvt_pk_fp8_f32 v70, v67, v71
	v_cvt_pk_fp8_f32 v70, v75, v79 op_sel:[0,0,1]
	v_cvt_pk_fp8_f32 v74, v68, v72
	v_cvt_pk_fp8_f32 v74, v76, v80 op_sel:[0,0,1]
	v_cvt_pk_fp8_f32 v78, v69, v73
	v_cvt_pk_fp8_f32 v78, v77, v81 op_sel:[0,0,1]
	v_cvt_pk_fp8_f32 v67, v82, v86
	v_cvt_pk_fp8_f32 v67, v90, v94 op_sel:[0,0,1]
	v_cvt_pk_fp8_f32 v71, v83, v87
	v_cvt_pk_fp8_f32 v71, v91, v95 op_sel:[0,0,1]
	v_cvt_pk_fp8_f32 v75, v84, v88
	v_cvt_pk_fp8_f32 v75, v92, v96 op_sel:[0,0,1]
	v_cvt_pk_fp8_f32 v79, v85, v89
	v_cvt_pk_fp8_f32 v79, v93, v97 op_sel:[0,0,1]
	v_cvt_pk_fp8_f32 v68, v98, v102
	v_cvt_pk_fp8_f32 v68, v106, v110 op_sel:[0,0,1]
	v_cvt_pk_fp8_f32 v72, v99, v103
	v_cvt_pk_fp8_f32 v72, v107, v111 op_sel:[0,0,1]
	v_cvt_pk_fp8_f32 v76, v100, v104
	v_cvt_pk_fp8_f32 v76, v108, v112 op_sel:[0,0,1]
	v_cvt_pk_fp8_f32 v80, v101, v105
	v_cvt_pk_fp8_f32 v80, v109, v113 op_sel:[0,0,1]
	v_cvt_pk_fp8_f32 v69, v114, v118
	v_cvt_pk_fp8_f32 v69, v122, v126 op_sel:[0,0,1]
	v_cvt_pk_fp8_f32 v73, v115, v119
	v_cvt_pk_fp8_f32 v73, v123, v127 op_sel:[0,0,1]
	v_cvt_pk_fp8_f32 v77, v116, v120
	v_cvt_pk_fp8_f32 v77, v124, v128 op_sel:[0,0,1]
	v_cvt_pk_fp8_f32 v81, v117, v121
	v_cvt_pk_fp8_f32 v81, v125, v129 op_sel:[0,0,1]
	global_store_dwordx4 v250, v[66:69], s[42:43] nt
	global_store_dwordx4 v250, v[70:73], s[42:43] offset:2048 nt
	global_store_dwordx4 v251, v[74:77], s[42:43] nt
	global_store_dwordx4 v251, v[78:81], s[42:43] offset:2048 nt
	s_add_u32 s42, s42, 0x200
	s_addc_u32 s43, s43, 0
	global_load_dwordx4 v[66:69], v246, s[4:5] nt
	global_load_dwordx4 v[70:73], v247, s[4:5] nt
	global_load_dwordx4 v[74:77], v248, s[4:5] nt
	global_load_dwordx4 v[78:81], v249, s[4:5] nt
	global_load_dwordx4 v[82:85], v246, s[6:7] nt
	global_load_dwordx4 v[86:89], v247, s[6:7] nt
	global_load_dwordx4 v[90:93], v248, s[6:7] nt
	global_load_dwordx4 v[94:97], v249, s[6:7] nt
	global_load_dwordx4 v[98:101], v246, s[8:9] nt
	global_load_dwordx4 v[102:105], v247, s[8:9] nt
	global_load_dwordx4 v[106:109], v248, s[8:9] nt
	global_load_dwordx4 v[110:113], v249, s[8:9] nt
	global_load_dwordx4 v[114:117], v246, s[38:39] nt
	global_load_dwordx4 v[118:121], v247, s[38:39] nt
	global_load_dwordx4 v[122:125], v248, s[38:39] nt
	global_load_dwordx4 v[126:129], v249, s[38:39] nt
	s_add_u32 s4, s4, 0x400000
	s_addc_u32 s5, s5, 0
	s_add_u32 s6, s6, 0x400000
	s_addc_u32 s7, s7, 0
	s_add_u32 s8, s8, 0x400000
	s_addc_u32 s9, s9, 0
	s_add_u32 s38, s38, 0x400000
	s_addc_u32 s39, s39, 0
	s_waitcnt vmcnt(40)
; #define GAS __attribute__((address_space(1)))
; template <bool GAIN, bool NT = false> __device__ __forceinline__ void titem8_load(const TItem& d, int lane, f32x4 (&r)[16], f32x4 (&g)[4]) {
;     const int q = lane & 7, kg = lane >> 3; const unsigned lo = (unsigned)((16 * kg) * d.N + 4 * q) * 4u;
;     const GAS char* base = (const GAS char*)d.src;
; #pragma unroll
;     for (int j = 0; j < 16; ++j) { const GAS f32x4* p = (const GAS f32x4*)(base + (size_t)j * (size_t)d.N * 4 + lo); r[j] = NT ? __builtin_nontemporal_load(p) : *p; }
;     if constexpr (GAIN) { const GAS char* gb = (const GAS char*)d.gain; const unsigned go = (unsigned)(16 * kg) * 4u;
; #pragma unroll
;         for (int j4 = 0; j4 < 4; ++j4) g[j4] = *(const GAS f32x4*)(gb + 16 * j4 + go); }
;     asm volatile("" ::: "memory"); __builtin_amdgcn_sched_barrier(0);
; }
; template <bool GAIN, bool NT = false> __device__ __forceinline__ void titem8_store(const TItem& d, int lane, const f32x4 (&r)[16], const f32x4 (&g)[4]) {
;     const int q = lane & 7, kg = lane >> 3; const unsigned lo = (unsigned)((4 * q) * d.ldk + 16 * kg);
;     GAS char* base = (GAS char*)d.dst;
;     f32x4 s[16];
; #pragma unroll
;     for (int j = 0; j < 16; ++j) s[j] = r[j] * ((GAIN ? g[j >> 2][j & 3] : 1.0f) * W8_SCALE);
; #pragma unroll
;     for (int i = 0; i < 4; ++i) { v4u w;
;         w.x = pk4_fp8w(s[0][i], s[1][i], s[2][i], s[3][i]); w.y = pk4_fp8w(s[4][i], s[5][i], s[6][i], s[7][i]);
;         w.z = pk4_fp8w(s[8][i], s[9][i], s[10][i], s[11][i]); w.w = pk4_fp8w(s[12][i], s[13][i], s[14][i], s[15][i]);
;         GAS v4u* p = (GAS v4u*)(base + (size_t)i * (size_t)d.ldk + lo);
;         if (NT) __builtin_nontemporal_store(w, p); else *p = w; }
; }
	v_pk_mul_f32 v[130:131], v[130:131], s[30:31] op_sel_hi:[1,0]
	v_pk_mul_f32 v[132:133], v[132:133], s[30:31] op_sel_hi:[1,0]
	v_pk_mul_f32 v[134:135], v[134:135], s[30:31] op_sel_hi:[1,0]
	v_pk_mul_f32 v[136:137], v[136:137], s[30:31] op_sel_hi:[1,0]
	v_pk_mul_f32 v[138:139], v[138:139], s[30:31] op_sel_hi:[1,0]
	v_pk_mul_f32 v[140:141], v[140:141], s[30:31] op_sel_hi:[1,0]
	v_pk_mul_f32 v[142:143], v[142:143], s[30:31] op_sel_hi:[1,0]
	v_pk_mul_f32 v[144:145], v[144:145], s[30:31] op_sel_hi:[1,0]
	v_pk_mul_f32 v[146:147], v[146:147], s[30:31] op_sel_hi:[1,0]
	v_pk_mul_f32 v[148:149], v[148:149], s[30:31] op_sel_hi:[1,0]
	v_pk_mul_f32 v[150:151], v[150:151], s[30:31] op_sel_hi:[1,0]
	v_pk_mul_f32 v[152:153], v[152:153], s[30:31] op_sel_hi:[1,0]
	v_pk_mul_f32 v[154:155], v[154:155], s[30:31] op_sel_hi:[1,0]
	v_pk_mul_f32 v[156:157], v[156:157], s[30:31] op_sel_hi:[1,0]
	v_pk_mul_f32 v[158:159], v[158:159], s[30:31] op_sel_hi:[1,0]
	v_pk_mul_f32 v[160:161], v[160:161], s[30:31] op_sel_hi:[1,0]
	v_pk_mul_f32 v[162:163], v[162:163], s[30:31] op_sel_hi:[1,0]
	v_pk_mul_f32 v[164:165], v[164:165], s[30:31] op_sel_hi:[1,0]
	v_pk_mul_f32 v[166:167], v[166:167], s[30:31] op_sel_hi:[1,0]
	v_pk_mul_f32 v[168:169], v[168:169], s[30:31] op_sel_hi:[1,0]
	v_pk_mul_f32 v[170:171], v[170:171], s[30:31] op_sel_hi:[1,0]
	v_pk_mul_f32 v[172:173], v[172:173], s[30:31] op_sel_hi:[1,0]
	v_pk_mul_f32 v[174:175], v[174:175], s[30:31] op_sel_hi:[1,0]
	v_pk_mul_f32 v[176:177], v[176:177], s[30:31] op_sel_hi:[1,0]
	v_pk_mul_f32 v[178:179], v[178:179], s[30:31] op_sel_hi:[1,0]
	v_pk_mul_f32 v[180:181], v[180:181], s[30:31] op_sel_hi:[1,0]
	v_pk_mul_f32 v[182:183], v[182:183], s[30:31] op_sel_hi:[1,0]
	v_pk_mul_f32 v[184:185], v[184:185], s[30:31] op_sel_hi:[1,0]
	v_pk_mul_f32 v[186:187], v[186:187], s[30:31] op_sel_hi:[1,0]
	v_pk_mul_f32 v[188:189], v[188:189], s[30:31] op_sel_hi:[1,0]
	v_pk_mul_f32 v[190:191], v[190:191], s[30:31] op_sel_hi:[1,0]
	v_pk_mul_f32 v[192:193], v[192:193], s[30:31] op_sel_hi:[1,0]
	v_med3_f32 v130, v130, s24, v237
	v_med3_f32 v131, v131, s24, v237
	v_med3_f32 v132, v132, s24, v237
	v_med3_f32 v133, v133, s24, v237
	v_med3_f32 v134, v134, s24, v237
	v_med3_f32 v135, v135, s24, v237
	v_med3_f32 v136, v136, s24, v237
	v_med3_f32 v137, v137, s24, v237
	v_med3_f32 v138, v138, s24, v237
	v_med3_f32 v139, v139, s24, v237
	v_med3_f32 v140, v140, s24, v237
	v_med3_f32 v141, v141, s24, v237
	v_med3_f32 v142, v142, s24, v237
	v_med3_f32 v143, v143, s24, v237
	v_med3_f32 v144, v144, s24, v237
	v_med3_f32 v145, v145, s24, v237
	v_med3_f32 v146, v146, s24, v237
	v_med3_f32 v147, v147, s24, v237
	v_med3_f32 v148, v148, s24, v237
	v_med3_f32 v149, v149, s24, v237
	v_med3_f32 v150, v150, s24, v237
	v_med3_f32 v151, v151, s24, v237
	v_med3_f32 v152, v152, s24, v237
	v_med3_f32 v153, v153, s24, v237
	v_med3_f32 v154, v154, s24, v237
	v_med3_f32 v155, v155, s24, v237
	v_med3_f32 v156, v156, s24, v237
	v_med3_f32 v157, v157, s24, v237
	v_med3_f32 v158, v158, s24, v237
	v_med3_f32 v159, v159, s24, v237
	v_med3_f32 v160, v160, s24, v237
	v_med3_f32 v161, v161, s24, v237
	v_med3_f32 v162, v162, s24, v237
	v_med3_f32 v163, v163, s24, v237
	v_med3_f32 v164, v164, s24, v237
	v_med3_f32 v165, v165, s24, v237
	v_med3_f32 v166, v166, s24, v237
	v_med3_f32 v167, v167, s24, v237
	v_med3_f32 v168, v168, s24, v237
	v_med3_f32 v169, v169, s24, v237
	v_med3_f32 v170, v170, s24, v237
	v_med3_f32 v171, v171, s24, v237
	v_med3_f32 v172, v172, s24, v237
	v_med3_f32 v173, v173, s24, v237
	v_med3_f32 v174, v174, s24, v237
	v_med3_f32 v175, v175, s24, v237
	v_med3_f32 v176, v176, s24, v237
	v_med3_f32 v177, v177, s24, v237
	v_med3_f32 v178, v178, s24, v237
	v_med3_f32 v179, v179, s24, v237
	v_med3_f32 v180, v180, s24, v237
	v_med3_f32 v181, v181, s24, v237
	v_med3_f32 v182, v182, s24, v237
	v_med3_f32 v183, v183, s24, v237
	v_med3_f32 v184, v184, s24, v237
	v_med3_f32 v185, v185, s24, v237
	v_med3_f32 v186, v186, s24, v237
	v_med3_f32 v187, v187, s24, v237
	v_med3_f32 v188, v188, s24, v237
	v_med3_f32 v189, v189, s24, v237
	v_med3_f32 v190, v190, s24, v237
	v_med3_f32 v191, v191, s24, v237
	v_med3_f32 v192, v192, s24, v237
	v_med3_f32 v193, v193, s24, v237
	v_cvt_pk_fp8_f32 v130, v130, v134
	v_cvt_pk_fp8_f32 v130, v138, v142 op_sel:[0,0,1]
	v_cvt_pk_fp8_f32 v134, v131, v135
	v_cvt_pk_fp8_f32 v134, v139, v143 op_sel:[0,0,1]
	v_cvt_pk_fp8_f32 v138, v132, v136
	v_cvt_pk_fp8_f32 v138, v140, v144 op_sel:[0,0,1]
	v_cvt_pk_fp8_f32 v142, v133, v137
	v_cvt_pk_fp8_f32 v142, v141, v145 op_sel:[0,0,1]
	v_cvt_pk_fp8_f32 v131, v146, v150
	v_cvt_pk_fp8_f32 v131, v154, v158 op_sel:[0,0,1]
	v_cvt_pk_fp8_f32 v135, v147, v151
	v_cvt_pk_fp8_f32 v135, v155, v159 op_sel:[0,0,1]
	v_cvt_pk_fp8_f32 v139, v148, v152
	v_cvt_pk_fp8_f32 v139, v156, v160 op_sel:[0,0,1]
	v_cvt_pk_fp8_f32 v143, v149, v153
	v_cvt_pk_fp8_f32 v143, v157, v161 op_sel:[0,0,1]
	v_cvt_pk_fp8_f32 v132, v162, v166
	v_cvt_pk_fp8_f32 v132, v170, v174 op_sel:[0,0,1]
	v_cvt_pk_fp8_f32 v136, v163, v167
	v_cvt_pk_fp8_f32 v136, v171, v175 op_sel:[0,0,1]
	v_cvt_pk_fp8_f32 v140, v164, v168
	v_cvt_pk_fp8_f32 v140, v172, v176 op_sel:[0,0,1]
	v_cvt_pk_fp8_f32 v144, v165, v169
	v_cvt_pk_fp8_f32 v144, v173, v177 op_sel:[0,0,1]
	v_cvt_pk_fp8_f32 v133, v178, v182
	v_cvt_pk_fp8_f32 v133, v186, v190 op_sel:[0,0,1]
	v_cvt_pk_fp8_f32 v137, v179, v183
	v_cvt_pk_fp8_f32 v137, v187, v191 op_sel:[0,0,1]
	v_cvt_pk_fp8_f32 v141, v180, v184
	v_cvt_pk_fp8_f32 v141, v188, v192 op_sel:[0,0,1]
	v_cvt_pk_fp8_f32 v145, v181, v185
	v_cvt_pk_fp8_f32 v145, v189, v193 op_sel:[0,0,1]
	global_store_dwordx4 v250, v[130:133], s[42:43] nt
	global_store_dwordx4 v250, v[134:137], s[42:43] offset:2048 nt
	global_store_dwordx4 v251, v[138:141], s[42:43] nt
	global_store_dwordx4 v251, v[142:145], s[42:43] offset:2048 nt
	s_add_u32 s42, s42, 0x200
	s_addc_u32 s43, s43, 0
	global_load_dwordx4 v[130:133], v246, s[4:5] nt
	global_load_dwordx4 v[134:137], v247, s[4:5] nt
	global_load_dwordx4 v[138:141], v248, s[4:5] nt
	global_load_dwordx4 v[142:145], v249, s[4:5] nt
	global_load_dwordx4 v[146:149], v246, s[6:7] nt
	global_load_dwordx4 v[150:153], v247, s[6:7] nt
	global_load_dwordx4 v[154:157], v248, s[6:7] nt
	global_load_dwordx4 v[158:161], v249, s[6:7] nt
	global_load_dwordx4 v[162:165], v246, s[8:9] nt
	global_load_dwordx4 v[166:169], v247, s[8:9] nt
	global_load_dwordx4 v[170:173], v248, s[8:9] nt
	global_load_dwordx4 v[174:177], v249, s[8:9] nt
	global_load_dwordx4 v[178:181], v246, s[38:39] nt
	global_load_dwordx4 v[182:185], v247, s[38:39] nt
	global_load_dwordx4 v[186:189], v248, s[38:39] nt
	global_load_dwordx4 v[190:193], v249, s[38:39] nt
	s_add_u32 s4, s4, 0x400000
	s_addc_u32 s5, s5, 0
	s_add_u32 s6, s6, 0x400000
	s_addc_u32 s7, s7, 0
	s_add_u32 s8, s8, 0x400000
	s_addc_u32 s9, s9, 0
	s_add_u32 s38, s38, 0x400000
	s_addc_u32 s39, s39, 0
	s_waitcnt vmcnt(40)
; #define GAS __attribute__((address_space(1)))
; template <bool GAIN, bool NT = false> __device__ __forceinline__ void titem8_load(const TItem& d, int lane, f32x4 (&r)[16], f32x4 (&g)[4]) {
;     const int q = lane & 7, kg = lane >> 3; const unsigned lo = (unsigned)((16 * kg) * d.N + 4 * q) * 4u;
;     const GAS char* base = (const GAS char*)d.src;
; #pragma unroll
;     for (int j = 0; j < 16; ++j) { const GAS f32x4* p = (const GAS f32x4*)(base + (size_t)j * (size_t)d.N * 4 + lo); r[j] = NT ? __builtin_nontemporal_load(p) : *p; }
;     if constexpr (GAIN) { const GAS char* gb = (const GAS char*)d.gain; const unsigned go = (unsigned)(16 * kg) * 4u;
; #pragma unroll
;         for (int j4 = 0; j4 < 4; ++j4) g[j4] = *(const GAS f32x4*)(gb + 16 * j4 + go); }
;     asm volatile("" ::: "memory"); __builtin_amdgcn_sched_barrier(0);
; }
; template <bool GAIN, bool NT = false> __device__ __forceinline__ void titem8_store(const TItem& d, int lane, const f32x4 (&r)[16], const f32x4 (&g)[4]) {
;     const int q = lane & 7, kg = lane >> 3; const unsigned lo = (unsigned)((4 * q) * d.ldk + 16 * kg);
;     GAS char* base = (GAS char*)d.dst;
;     f32x4 s[16];
; #pragma unroll
;     for (int j = 0; j < 16; ++j) s[j] = r[j] * ((GAIN ? g[j >> 2][j & 3] : 1.0f) * W8_SCALE);
; #pragma unroll
;     for (int i = 0; i < 4; ++i) { v4u w;
;         w.x = pk4_fp8w(s[0][i], s[1][i], s[2][i], s[3][i]); w.y = pk4_fp8w(s[4][i], s[5][i], s[6][i], s[7][i]);
;         w.z = pk4_fp8w(s[8][i], s[9][i], s[10][i], s[11][i]); w.w = pk4_fp8w(s[12][i], s[13][i], s[14][i], s[15][i]);
;         GAS v4u* p = (GAS v4u*)(base + (size_t)i * (size_t)d.ldk + lo);
;         if (NT) __builtin_nontemporal_store(w, p); else *p = w; }
; }
	v_pk_mul_f32 v[0:1], v[0:1], s[30:31] op_sel_hi:[1,0]
	v_pk_mul_f32 v[2:3], v[2:3], s[30:31] op_sel_hi:[1,0]
	v_pk_mul_f32 v[4:5], v[4:5], s[30:31] op_sel_hi:[1,0]
	v_pk_mul_f32 v[6:7], v[6:7], s[30:31] op_sel_hi:[1,0]
	v_pk_mul_f32 v[8:9], v[8:9], s[30:31] op_sel_hi:[1,0]
	v_pk_mul_f32 v[10:11], v[10:11], s[30:31] op_sel_hi:[1,0]
	v_pk_mul_f32 v[12:13], v[12:13], s[30:31] op_sel_hi:[1,0]
	v_pk_mul_f32 v[14:15], v[14:15], s[30:31] op_sel_hi:[1,0]
	v_pk_mul_f32 v[16:17], v[16:17], s[30:31] op_sel_hi:[1,0]
	v_pk_mul_f32 v[18:19], v[18:19], s[30:31] op_sel_hi:[1,0]
	v_pk_mul_f32 v[20:21], v[20:21], s[30:31] op_sel_hi:[1,0]
	v_pk_mul_f32 v[22:23], v[22:23], s[30:31] op_sel_hi:[1,0]
	v_pk_mul_f32 v[24:25], v[24:25], s[30:31] op_sel_hi:[1,0]
	v_pk_mul_f32 v[26:27], v[26:27], s[30:31] op_sel_hi:[1,0]
	v_pk_mul_f32 v[28:29], v[28:29], s[30:31] op_sel_hi:[1,0]
	v_pk_mul_f32 v[30:31], v[30:31], s[30:31] op_sel_hi:[1,0]
	v_pk_mul_f32 v[32:33], v[32:33], s[30:31] op_sel_hi:[1,0]
	v_pk_mul_f32 v[34:35], v[34:35], s[30:31] op_sel_hi:[1,0]
	v_pk_mul_f32 v[36:37], v[36:37], s[30:31] op_sel_hi:[1,0]
	v_pk_mul_f32 v[38:39], v[38:39], s[30:31] op_sel_hi:[1,0]
	v_pk_mul_f32 v[40:41], v[40:41], s[30:31] op_sel_hi:[1,0]
	v_pk_mul_f32 v[42:43], v[42:43], s[30:31] op_sel_hi:[1,0]
	v_pk_mul_f32 v[44:45], v[44:45], s[30:31] op_sel_hi:[1,0]
	v_pk_mul_f32 v[46:47], v[46:47], s[30:31] op_sel_hi:[1,0]
	v_pk_mul_f32 v[48:49], v[48:49], s[30:31] op_sel_hi:[1,0]
	v_pk_mul_f32 v[50:51], v[50:51], s[30:31] op_sel_hi:[1,0]
	v_pk_mul_f32 v[52:53], v[52:53], s[30:31] op_sel_hi:[1,0]
	v_pk_mul_f32 v[54:55], v[54:55], s[30:31] op_sel_hi:[1,0]
	v_pk_mul_f32 v[56:57], v[56:57], s[30:31] op_sel_hi:[1,0]
	v_pk_mul_f32 v[58:59], v[58:59], s[30:31] op_sel_hi:[1,0]
	v_pk_mul_f32 v[60:61], v[60:61], s[30:31] op_sel_hi:[1,0]
	v_pk_mul_f32 v[62:63], v[62:63], s[30:31] op_sel_hi:[1,0]
	v_med3_f32 v0, v0, s24, v237
	v_med3_f32 v1, v1, s24, v237
	v_med3_f32 v2, v2, s24, v237
	v_med3_f32 v3, v3, s24, v237
	v_med3_f32 v4, v4, s24, v237
	v_med3_f32 v5, v5, s24, v237
	v_med3_f32 v6, v6, s24, v237
	v_med3_f32 v7, v7, s24, v237
	v_med3_f32 v8, v8, s24, v237
	v_med3_f32 v9, v9, s24, v237
	v_med3_f32 v10, v10, s24, v237
	v_med3_f32 v11, v11, s24, v237
	v_med3_f32 v12, v12, s24, v237
	v_med3_f32 v13, v13, s24, v237
	v_med3_f32 v14, v14, s24, v237
	v_med3_f32 v15, v15, s24, v237
	v_med3_f32 v16, v16, s24, v237
	v_med3_f32 v17, v17, s24, v237
	v_med3_f32 v18, v18, s24, v237
	v_med3_f32 v19, v19, s24, v237
	v_med3_f32 v20, v20, s24, v237
	v_med3_f32 v21, v21, s24, v237
	v_med3_f32 v22, v22, s24, v237
	v_med3_f32 v23, v23, s24, v237
	v_med3_f32 v24, v24, s24, v237
	v_med3_f32 v25, v25, s24, v237
	v_med3_f32 v26, v26, s24, v237
	v_med3_f32 v27, v27, s24, v237
	v_med3_f32 v28, v28, s24, v237
	v_med3_f32 v29, v29, s24, v237
	v_med3_f32 v30, v30, s24, v237
	v_med3_f32 v31, v31, s24, v237
	v_med3_f32 v32, v32, s24, v237
	v_med3_f32 v33, v33, s24, v237
	v_med3_f32 v34, v34, s24, v237
	v_med3_f32 v35, v35, s24, v237
	v_med3_f32 v36, v36, s24, v237
	v_med3_f32 v37, v37, s24, v237
	v_med3_f32 v38, v38, s24, v237
	v_med3_f32 v39, v39, s24, v237
	v_med3_f32 v40, v40, s24, v237
	v_med3_f32 v41, v41, s24, v237
	v_med3_f32 v42, v42, s24, v237
	v_med3_f32 v43, v43, s24, v237
	v_med3_f32 v44, v44, s24, v237
	v_med3_f32 v45, v45, s24, v237
	v_med3_f32 v46, v46, s24, v237
	v_med3_f32 v47, v47, s24, v237
	v_med3_f32 v48, v48, s24, v237
	v_med3_f32 v49, v49, s24, v237
	v_med3_f32 v50, v50, s24, v237
	v_med3_f32 v51, v51, s24, v237
	v_med3_f32 v52, v52, s24, v237
	v_med3_f32 v53, v53, s24, v237
	v_med3_f32 v54, v54, s24, v237
	v_med3_f32 v55, v55, s24, v237
	v_med3_f32 v56, v56, s24, v237
	v_med3_f32 v57, v57, s24, v237
	v_med3_f32 v58, v58, s24, v237
	v_med3_f32 v59, v59, s24, v237
	v_med3_f32 v60, v60, s24, v237
	v_med3_f32 v61, v61, s24, v237
	v_med3_f32 v62, v62, s24, v237
	v_med3_f32 v63, v63, s24, v237
	v_cvt_pk_fp8_f32 v0, v0, v4
	v_cvt_pk_fp8_f32 v0, v8, v12 op_sel:[0,0,1]
	v_cvt_pk_fp8_f32 v4, v1, v5
	v_cvt_pk_fp8_f32 v4, v9, v13 op_sel:[0,0,1]
	v_cvt_pk_fp8_f32 v8, v2, v6
	v_cvt_pk_fp8_f32 v8, v10, v14 op_sel:[0,0,1]
	v_cvt_pk_fp8_f32 v12, v3, v7
	v_cvt_pk_fp8_f32 v12, v11, v15 op_sel:[0,0,1]
	v_cvt_pk_fp8_f32 v1, v16, v20
	v_cvt_pk_fp8_f32 v1, v24, v28 op_sel:[0,0,1]
	v_cvt_pk_fp8_f32 v5, v17, v21
	v_cvt_pk_fp8_f32 v5, v25, v29 op_sel:[0,0,1]
	v_cvt_pk_fp8_f32 v9, v18, v22
	v_cvt_pk_fp8_f32 v9, v26, v30 op_sel:[0,0,1]
	v_cvt_pk_fp8_f32 v13, v19, v23
	v_cvt_pk_fp8_f32 v13, v27, v31 op_sel:[0,0,1]
	v_cvt_pk_fp8_f32 v2, v32, v36
	v_cvt_pk_fp8_f32 v2, v40, v44 op_sel:[0,0,1]
	v_cvt_pk_fp8_f32 v6, v33, v37
	v_cvt_pk_fp8_f32 v6, v41, v45 op_sel:[0,0,1]
	v_cvt_pk_fp8_f32 v10, v34, v38
	v_cvt_pk_fp8_f32 v10, v42, v46 op_sel:[0,0,1]
	v_cvt_pk_fp8_f32 v14, v35, v39
	v_cvt_pk_fp8_f32 v14, v43, v47 op_sel:[0,0,1]
	v_cvt_pk_fp8_f32 v3, v48, v52
	v_cvt_pk_fp8_f32 v3, v56, v60 op_sel:[0,0,1]
	v_cvt_pk_fp8_f32 v7, v49, v53
	v_cvt_pk_fp8_f32 v7, v57, v61 op_sel:[0,0,1]
	v_cvt_pk_fp8_f32 v11, v50, v54
	v_cvt_pk_fp8_f32 v11, v58, v62 op_sel:[0,0,1]
	v_cvt_pk_fp8_f32 v15, v51, v55
	v_cvt_pk_fp8_f32 v15, v59, v63 op_sel:[0,0,1]
	global_store_dwordx4 v250, v[0:3], s[42:43] nt
	global_store_dwordx4 v250, v[4:7], s[42:43] offset:2048 nt
	global_store_dwordx4 v251, v[8:11], s[42:43] nt
	global_store_dwordx4 v251, v[12:15], s[42:43] offset:2048 nt
	s_add_u32 s42, s42, 0x3ffa00
	s_addc_u32 s43, s43, 0
	global_load_dwordx4 v[0:3], v246, s[4:5] nt
	global_load_dwordx4 v[4:7], v247, s[4:5] nt
	global_load_dwordx4 v[8:11], v248, s[4:5] nt
	global_load_dwordx4 v[12:15], v249, s[4:5] nt
	global_load_dwordx4 v[16:19], v246, s[6:7] nt
	global_load_dwordx4 v[20:23], v247, s[6:7] nt
	global_load_dwordx4 v[24:27], v248, s[6:7] nt
	global_load_dwordx4 v[28:31], v249, s[6:7] nt
	global_load_dwordx4 v[32:35], v246, s[8:9] nt
	global_load_dwordx4 v[36:39], v247, s[8:9] nt
	global_load_dwordx4 v[40:43], v248, s[8:9] nt
	global_load_dwordx4 v[44:47], v249, s[8:9] nt
	global_load_dwordx4 v[48:51], v246, s[38:39] nt
	global_load_dwordx4 v[52:55], v247, s[38:39] nt
	global_load_dwordx4 v[56:59], v248, s[38:39] nt
	global_load_dwordx4 v[60:63], v249, s[38:39] nt
	s_add_u32 s4, s4, 0x400000
	s_addc_u32 s5, s5, 0
	s_add_u32 s6, s6, 0x400000
	s_addc_u32 s7, s7, 0
	s_add_u32 s8, s8, 0x400000
	s_addc_u32 s9, s9, 0
	s_add_u32 s38, s38, 0x400000
	s_addc_u32 s39, s39, 0
	s_waitcnt vmcnt(40)
; #define GAS __attribute__((address_space(1)))
; template <bool GAIN, bool NT = false> __device__ __forceinline__ void titem8_load(const TItem& d, int lane, f32x4 (&r)[16], f32x4 (&g)[4]) {
;     const int q = lane & 7, kg = lane >> 3; const unsigned lo = (unsigned)((16 * kg) * d.N + 4 * q) * 4u;
;     const GAS char* base = (const GAS char*)d.src;
; #pragma unroll
;     for (int j = 0; j < 16; ++j) { const GAS f32x4* p = (const GAS f32x4*)(base + (size_t)j * (size_t)d.N * 4 + lo); r[j] = NT ? __builtin_nontemporal_load(p) : *p; }
;     if constexpr (GAIN) { const GAS char* gb = (const GAS char*)d.gain; const unsigned go = (unsigned)(16 * kg) * 4u;
; #pragma unroll
;         for (int j4 = 0; j4 < 4; ++j4) g[j4] = *(const GAS f32x4*)(gb + 16 * j4 + go); }
;     asm volatile("" ::: "memory"); __builtin_amdgcn_sched_barrier(0);
; }
; template <bool GAIN, bool NT = false> __device__ __forceinline__ void titem8_store(const TItem& d, int lane, const f32x4 (&r)[16], const f32x4 (&g)[4]) {
;     const int q = lane & 7, kg = lane >> 3; const unsigned lo = (unsigned)((4 * q) * d.ldk + 16 * kg);
;     GAS char* base = (GAS char*)d.dst;
;     f32x4 s[16];
; #pragma unroll
;     for (int j = 0; j < 16; ++j) s[j] = r[j] * ((GAIN ? g[j >> 2][j & 3] : 1.0f) * W8_SCALE);
; #pragma unroll
;     for (int i = 0; i < 4; ++i) { v4u w;
;         w.x = pk4_fp8w(s[0][i], s[1][i], s[2][i], s[3][i]); w.y = pk4_fp8w(s[4][i], s[5][i], s[6][i], s[7][i]);
;         w.z = pk4_fp8w(s[8][i], s[9][i], s[10][i], s[11][i]); w.w = pk4_fp8w(s[12][i], s[13][i], s[14][i], s[15][i]);
;         GAS v4u* p = (GAS v4u*)(base + (size_t)i * (size_t)d.ldk + lo);
;         if (NT) __builtin_nontemporal_store(w, p); else *p = w; }
; }
	v_pk_mul_f32 v[66:67], v[66:67], s[30:31] op_sel_hi:[1,0]
	v_pk_mul_f32 v[68:69], v[68:69], s[30:31] op_sel_hi:[1,0]
	v_pk_mul_f32 v[70:71], v[70:71], s[30:31] op_sel_hi:[1,0]
	v_pk_mul_f32 v[72:73], v[72:73], s[30:31] op_sel_hi:[1,0]
	v_pk_mul_f32 v[74:75], v[74:75], s[30:31] op_sel_hi:[1,0]
	v_pk_mul_f32 v[76:77], v[76:77], s[30:31] op_sel_hi:[1,0]
	v_pk_mul_f32 v[78:79], v[78:79], s[30:31] op_sel_hi:[1,0]
	v_pk_mul_f32 v[80:81], v[80:81], s[30:31] op_sel_hi:[1,0]
	v_pk_mul_f32 v[82:83], v[82:83], s[30:31] op_sel_hi:[1,0]
	v_pk_mul_f32 v[84:85], v[84:85], s[30:31] op_sel_hi:[1,0]
	v_pk_mul_f32 v[86:87], v[86:87], s[30:31] op_sel_hi:[1,0]
	v_pk_mul_f32 v[88:89], v[88:89], s[30:31] op_sel_hi:[1,0]
	v_pk_mul_f32 v[90:91], v[90:91], s[30:31] op_sel_hi:[1,0]
	v_pk_mul_f32 v[92:93], v[92:93], s[30:31] op_sel_hi:[1,0]
	v_pk_mul_f32 v[94:95], v[94:95], s[30:31] op_sel_hi:[1,0]
	v_pk_mul_f32 v[96:97], v[96:97], s[30:31] op_sel_hi:[1,0]
	v_pk_mul_f32 v[98:99], v[98:99], s[30:31] op_sel_hi:[1,0]
	v_pk_mul_f32 v[100:101], v[100:101], s[30:31] op_sel_hi:[1,0]
	v_pk_mul_f32 v[102:103], v[102:103], s[30:31] op_sel_hi:[1,0]
	v_pk_mul_f32 v[104:105], v[104:105], s[30:31] op_sel_hi:[1,0]
	v_pk_mul_f32 v[106:107], v[106:107], s[30:31] op_sel_hi:[1,0]
	v_pk_mul_f32 v[108:109], v[108:109], s[30:31] op_sel_hi:[1,0]
	v_pk_mul_f32 v[110:111], v[110:111], s[30:31] op_sel_hi:[1,0]
	v_pk_mul_f32 v[112:113], v[112:113], s[30:31] op_sel_hi:[1,0]
	v_pk_mul_f32 v[114:115], v[114:115], s[30:31] op_sel_hi:[1,0]
	v_pk_mul_f32 v[116:117], v[116:117], s[30:31] op_sel_hi:[1,0]
	v_pk_mul_f32 v[118:119], v[118:119], s[30:31] op_sel_hi:[1,0]
	v_pk_mul_f32 v[120:121], v[120:121], s[30:31] op_sel_hi:[1,0]
	v_pk_mul_f32 v[122:123], v[122:123], s[30:31] op_sel_hi:[1,0]
	v_pk_mul_f32 v[124:125], v[124:125], s[30:31] op_sel_hi:[1,0]
	v_pk_mul_f32 v[126:127], v[126:127], s[30:31] op_sel_hi:[1,0]
	v_pk_mul_f32 v[128:129], v[128:129], s[30:31] op_sel_hi:[1,0]
	v_med3_f32 v66, v66, s24, v237
	v_med3_f32 v67, v67, s24, v237
	v_med3_f32 v68, v68, s24, v237
	v_med3_f32 v69, v69, s24, v237
	v_med3_f32 v70, v70, s24, v237
	v_med3_f32 v71, v71, s24, v237
	v_med3_f32 v72, v72, s24, v237
	v_med3_f32 v73, v73, s24, v237
	v_med3_f32 v74, v74, s24, v237
	v_med3_f32 v75, v75, s24, v237
	v_med3_f32 v76, v76, s24, v237
	v_med3_f32 v77, v77, s24, v237
	v_med3_f32 v78, v78, s24, v237
	v_med3_f32 v79, v79, s24, v237
	v_med3_f32 v80, v80, s24, v237
	v_med3_f32 v81, v81, s24, v237
	v_med3_f32 v82, v82, s24, v237
	v_med3_f32 v83, v83, s24, v237
	v_med3_f32 v84, v84, s24, v237
	v_med3_f32 v85, v85, s24, v237
	v_med3_f32 v86, v86, s24, v237
	v_med3_f32 v87, v87, s24, v237
	v_med3_f32 v88, v88, s24, v237
	v_med3_f32 v89, v89, s24, v237
	v_med3_f32 v90, v90, s24, v237
	v_med3_f32 v91, v91, s24, v237
	v_med3_f32 v92, v92, s24, v237
	v_med3_f32 v93, v93, s24, v237
	v_med3_f32 v94, v94, s24, v237
	v_med3_f32 v95, v95, s24, v237
	v_med3_f32 v96, v96, s24, v237
	v_med3_f32 v97, v97, s24, v237
	v_med3_f32 v98, v98, s24, v237
	v_med3_f32 v99, v99, s24, v237
	v_med3_f32 v100, v100, s24, v237
	v_med3_f32 v101, v101, s24, v237
	v_med3_f32 v102, v102, s24, v237
	v_med3_f32 v103, v103, s24, v237
	v_med3_f32 v104, v104, s24, v237
	v_med3_f32 v105, v105, s24, v237
	v_med3_f32 v106, v106, s24, v237
	v_med3_f32 v107, v107, s24, v237
	v_med3_f32 v108, v108, s24, v237
	v_med3_f32 v109, v109, s24, v237
	v_med3_f32 v110, v110, s24, v237
	v_med3_f32 v111, v111, s24, v237
	v_med3_f32 v112, v112, s24, v237
	v_med3_f32 v113, v113, s24, v237
	v_med3_f32 v114, v114, s24, v237
	v_med3_f32 v115, v115, s24, v237
	v_med3_f32 v116, v116, s24, v237
	v_med3_f32 v117, v117, s24, v237
	v_med3_f32 v118, v118, s24, v237
	v_med3_f32 v119, v119, s24, v237
	v_med3_f32 v120, v120, s24, v237
	v_med3_f32 v121, v121, s24, v237
	v_med3_f32 v122, v122, s24, v237
	v_med3_f32 v123, v123, s24, v237
	v_med3_f32 v124, v124, s24, v237
	v_med3_f32 v125, v125, s24, v237
	v_med3_f32 v126, v126, s24, v237
	v_med3_f32 v127, v127, s24, v237
	v_med3_f32 v128, v128, s24, v237
	v_med3_f32 v129, v129, s24, v237
	v_cvt_pk_fp8_f32 v66, v66, v70
	v_cvt_pk_fp8_f32 v66, v74, v78 op_sel:[0,0,1]
	v_cvt_pk_fp8_f32 v70, v67, v71
	v_cvt_pk_fp8_f32 v70, v75, v79 op_sel:[0,0,1]
	v_cvt_pk_fp8_f32 v74, v68, v72
	v_cvt_pk_fp8_f32 v74, v76, v80 op_sel:[0,0,1]
	v_cvt_pk_fp8_f32 v78, v69, v73
	v_cvt_pk_fp8_f32 v78, v77, v81 op_sel:[0,0,1]
	v_cvt_pk_fp8_f32 v67, v82, v86
	v_cvt_pk_fp8_f32 v67, v90, v94 op_sel:[0,0,1]
	v_cvt_pk_fp8_f32 v71, v83, v87
	v_cvt_pk_fp8_f32 v71, v91, v95 op_sel:[0,0,1]
	v_cvt_pk_fp8_f32 v75, v84, v88
	v_cvt_pk_fp8_f32 v75, v92, v96 op_sel:[0,0,1]
	v_cvt_pk_fp8_f32 v79, v85, v89
	v_cvt_pk_fp8_f32 v79, v93, v97 op_sel:[0,0,1]
	v_cvt_pk_fp8_f32 v68, v98, v102
	v_cvt_pk_fp8_f32 v68, v106, v110 op_sel:[0,0,1]
	v_cvt_pk_fp8_f32 v72, v99, v103
	v_cvt_pk_fp8_f32 v72, v107, v111 op_sel:[0,0,1]
	v_cvt_pk_fp8_f32 v76, v100, v104
	v_cvt_pk_fp8_f32 v76, v108, v112 op_sel:[0,0,1]
	v_cvt_pk_fp8_f32 v80, v101, v105
	v_cvt_pk_fp8_f32 v80, v109, v113 op_sel:[0,0,1]
	v_cvt_pk_fp8_f32 v69, v114, v118
	v_cvt_pk_fp8_f32 v69, v122, v126 op_sel:[0,0,1]
	v_cvt_pk_fp8_f32 v73, v115, v119
	v_cvt_pk_fp8_f32 v73, v123, v127 op_sel:[0,0,1]
	v_cvt_pk_fp8_f32 v77, v116, v120
	v_cvt_pk_fp8_f32 v77, v124, v128 op_sel:[0,0,1]
	v_cvt_pk_fp8_f32 v81, v117, v121
	v_cvt_pk_fp8_f32 v81, v125, v129 op_sel:[0,0,1]
	global_store_dwordx4 v250, v[66:69], s[42:43] nt
	global_store_dwordx4 v250, v[70:73], s[42:43] offset:2048 nt
	global_store_dwordx4 v251, v[74:77], s[42:43] nt
	global_store_dwordx4 v251, v[78:81], s[42:43] offset:2048 nt
	s_add_u32 s42, s42, 0x200
	s_addc_u32 s43, s43, 0
	global_load_dwordx4 v[66:69], v246, s[4:5] nt
	global_load_dwordx4 v[70:73], v247, s[4:5] nt
	global_load_dwordx4 v[74:77], v248, s[4:5] nt
	global_load_dwordx4 v[78:81], v249, s[4:5] nt
	global_load_dwordx4 v[82:85], v246, s[6:7] nt
	global_load_dwordx4 v[86:89], v247, s[6:7] nt
	global_load_dwordx4 v[90:93], v248, s[6:7] nt
	global_load_dwordx4 v[94:97], v249, s[6:7] nt
	global_load_dwordx4 v[98:101], v246, s[8:9] nt
	global_load_dwordx4 v[102:105], v247, s[8:9] nt
	global_load_dwordx4 v[106:109], v248, s[8:9] nt
	global_load_dwordx4 v[110:113], v249, s[8:9] nt
	global_load_dwordx4 v[114:117], v246, s[38:39] nt
	global_load_dwordx4 v[118:121], v247, s[38:39] nt
	global_load_dwordx4 v[122:125], v248, s[38:39] nt
	global_load_dwordx4 v[126:129], v249, s[38:39] nt
	s_add_u32 s4, s4, 0x400000
	s_addc_u32 s5, s5, 0
	s_add_u32 s6, s6, 0x400000
	s_addc_u32 s7, s7, 0
	s_add_u32 s8, s8, 0x400000
	s_addc_u32 s9, s9, 0
	s_add_u32 s38, s38, 0x400000
	s_addc_u32 s39, s39, 0
	s_waitcnt vmcnt(40)
; #define GAS __attribute__((address_space(1)))
; template <bool GAIN, bool NT = false> __device__ __forceinline__ void titem8_load(const TItem& d, int lane, f32x4 (&r)[16], f32x4 (&g)[4]) {
;     const int q = lane & 7, kg = lane >> 3; const unsigned lo = (unsigned)((16 * kg) * d.N + 4 * q) * 4u;
;     const GAS char* base = (const GAS char*)d.src;
; #pragma unroll
;     for (int j = 0; j < 16; ++j) { const GAS f32x4* p = (const GAS f32x4*)(base + (size_t)j * (size_t)d.N * 4 + lo); r[j] = NT ? __builtin_nontemporal_load(p) : *p; }
;     if constexpr (GAIN) { const GAS char* gb = (const GAS char*)d.gain; const unsigned go = (unsigned)(16 * kg) * 4u;
; #pragma unroll
;         for (int j4 = 0; j4 < 4; ++j4) g[j4] = *(const GAS f32x4*)(gb + 16 * j4 + go); }
;     asm volatile("" ::: "memory"); __builtin_amdgcn_sched_barrier(0);
; }
; template <bool GAIN, bool NT = false> __device__ __forceinline__ void titem8_store(const TItem& d, int lane, const f32x4 (&r)[16], const f32x4 (&g)[4]) {
;     const int q = lane & 7, kg = lane >> 3; const unsigned lo = (unsigned)((4 * q) * d.ldk + 16 * kg);
;     GAS char* base = (GAS char*)d.dst;
;     f32x4 s[16];
; #pragma unroll
;     for (int j = 0; j < 16; ++j) s[j] = r[j] * ((GAIN ? g[j >> 2][j & 3] : 1.0f) * W8_SCALE);
; #pragma unroll
;     for (int i = 0; i < 4; ++i) { v4u w;
;         w.x = pk4_fp8w(s[0][i], s[1][i], s[2][i], s[3][i]); w.y = pk4_fp8w(s[4][i], s[5][i], s[6][i], s[7][i]);
;         w.z = pk4_fp8w(s[8][i], s[9][i], s[10][i], s[11][i]); w.w = pk4_fp8w(s[12][i], s[13][i], s[14][i], s[15][i]);
;         GAS v4u* p = (GAS v4u*)(base + (size_t)i * (size_t)d.ldk + lo);
;         if (NT) __builtin_nontemporal_store(w, p); else *p = w; }
; }
	v_pk_mul_f32 v[130:131], v[130:131], s[30:31] op_sel_hi:[1,0]
	v_pk_mul_f32 v[132:133], v[132:133], s[30:31] op_sel_hi:[1,0]
	v_pk_mul_f32 v[134:135], v[134:135], s[30:31] op_sel_hi:[1,0]
	v_pk_mul_f32 v[136:137], v[136:137], s[30:31] op_sel_hi:[1,0]
	v_pk_mul_f32 v[138:139], v[138:139], s[30:31] op_sel_hi:[1,0]
	v_pk_mul_f32 v[140:141], v[140:141], s[30:31] op_sel_hi:[1,0]
	v_pk_mul_f32 v[142:143], v[142:143], s[30:31] op_sel_hi:[1,0]
	v_pk_mul_f32 v[144:145], v[144:145], s[30:31] op_sel_hi:[1,0]
	v_pk_mul_f32 v[146:147], v[146:147], s[30:31] op_sel_hi:[1,0]
	v_pk_mul_f32 v[148:149], v[148:149], s[30:31] op_sel_hi:[1,0]
	v_pk_mul_f32 v[150:151], v[150:151], s[30:31] op_sel_hi:[1,0]
	v_pk_mul_f32 v[152:153], v[152:153], s[30:31] op_sel_hi:[1,0]
	v_pk_mul_f32 v[154:155], v[154:155], s[30:31] op_sel_hi:[1,0]
	v_pk_mul_f32 v[156:157], v[156:157], s[30:31] op_sel_hi:[1,0]
	v_pk_mul_f32 v[158:159], v[158:159], s[30:31] op_sel_hi:[1,0]
	v_pk_mul_f32 v[160:161], v[160:161], s[30:31] op_sel_hi:[1,0]
	v_pk_mul_f32 v[162:163], v[162:163], s[30:31] op_sel_hi:[1,0]
	v_pk_mul_f32 v[164:165], v[164:165], s[30:31] op_sel_hi:[1,0]
	v_pk_mul_f32 v[166:167], v[166:167], s[30:31] op_sel_hi:[1,0]
	v_pk_mul_f32 v[168:169], v[168:169], s[30:31] op_sel_hi:[1,0]
	v_pk_mul_f32 v[170:171], v[170:171], s[30:31] op_sel_hi:[1,0]
	v_pk_mul_f32 v[172:173], v[172:173], s[30:31] op_sel_hi:[1,0]
	v_pk_mul_f32 v[174:175], v[174:175], s[30:31] op_sel_hi:[1,0]
	v_pk_mul_f32 v[176:177], v[176:177], s[30:31] op_sel_hi:[1,0]
	v_pk_mul_f32 v[178:179], v[178:179], s[30:31] op_sel_hi:[1,0]
	v_pk_mul_f32 v[180:181], v[180:181], s[30:31] op_sel_hi:[1,0]
	v_pk_mul_f32 v[182:183], v[182:183], s[30:31] op_sel_hi:[1,0]
	v_pk_mul_f32 v[184:185], v[184:185], s[30:31] op_sel_hi:[1,0]
	v_pk_mul_f32 v[186:187], v[186:187], s[30:31] op_sel_hi:[1,0]
	v_pk_mul_f32 v[188:189], v[188:189], s[30:31] op_sel_hi:[1,0]
	v_pk_mul_f32 v[190:191], v[190:191], s[30:31] op_sel_hi:[1,0]
	v_pk_mul_f32 v[192:193], v[192:193], s[30:31] op_sel_hi:[1,0]
	v_med3_f32 v130, v130, s24, v237
	v_med3_f32 v131, v131, s24, v237
	v_med3_f32 v132, v132, s24, v237
	v_med3_f32 v133, v133, s24, v237
	v_med3_f32 v134, v134, s24, v237
	v_med3_f32 v135, v135, s24, v237
	v_med3_f32 v136, v136, s24, v237
	v_med3_f32 v137, v137, s24, v237
	v_med3_f32 v138, v138, s24, v237
	v_med3_f32 v139, v139, s24, v237
	v_med3_f32 v140, v140, s24, v237
	v_med3_f32 v141, v141, s24, v237
	v_med3_f32 v142, v142, s24, v237
	v_med3_f32 v143, v143, s24, v237
	v_med3_f32 v144, v144, s24, v237
	v_med3_f32 v145, v145, s24, v237
	v_med3_f32 v146, v146, s24, v237
	v_med3_f32 v147, v147, s24, v237
	v_med3_f32 v148, v148, s24, v237
	v_med3_f32 v149, v149, s24, v237
	v_med3_f32 v150, v150, s24, v237
	v_med3_f32 v151, v151, s24, v237
	v_med3_f32 v152, v152, s24, v237
	v_med3_f32 v153, v153, s24, v237
	v_med3_f32 v154, v154, s24, v237
	v_med3_f32 v155, v155, s24, v237
	v_med3_f32 v156, v156, s24, v237
	v_med3_f32 v157, v157, s24, v237
	v_med3_f32 v158, v158, s24, v237
	v_med3_f32 v159, v159, s24, v237
	v_med3_f32 v160, v160, s24, v237
	v_med3_f32 v161, v161, s24, v237
	v_med3_f32 v162, v162, s24, v237
	v_med3_f32 v163, v163, s24, v237
	v_med3_f32 v164, v164, s24, v237
	v_med3_f32 v165, v165, s24, v237
	v_med3_f32 v166, v166, s24, v237
	v_med3_f32 v167, v167, s24, v237
	v_med3_f32 v168, v168, s24, v237
	v_med3_f32 v169, v169, s24, v237
	v_med3_f32 v170, v170, s24, v237
	v_med3_f32 v171, v171, s24, v237
	v_med3_f32 v172, v172, s24, v237
	v_med3_f32 v173, v173, s24, v237
	v_med3_f32 v174, v174, s24, v237
	v_med3_f32 v175, v175, s24, v237
	v_med3_f32 v176, v176, s24, v237
	v_med3_f32 v177, v177, s24, v237
	v_med3_f32 v178, v178, s24, v237
	v_med3_f32 v179, v179, s24, v237
	v_med3_f32 v180, v180, s24, v237
	v_med3_f32 v181, v181, s24, v237
	v_med3_f32 v182, v182, s24, v237
	v_med3_f32 v183, v183, s24, v237
	v_med3_f32 v184, v184, s24, v237
	v_med3_f32 v185, v185, s24, v237
	v_med3_f32 v186, v186, s24, v237
	v_med3_f32 v187, v187, s24, v237
	v_med3_f32 v188, v188, s24, v237
	v_med3_f32 v189, v189, s24, v237
	v_med3_f32 v190, v190, s24, v237
	v_med3_f32 v191, v191, s24, v237
	v_med3_f32 v192, v192, s24, v237
	v_med3_f32 v193, v193, s24, v237
	v_cvt_pk_fp8_f32 v130, v130, v134
	v_cvt_pk_fp8_f32 v130, v138, v142 op_sel:[0,0,1]
	v_cvt_pk_fp8_f32 v134, v131, v135
	v_cvt_pk_fp8_f32 v134, v139, v143 op_sel:[0,0,1]
	v_cvt_pk_fp8_f32 v138, v132, v136
	v_cvt_pk_fp8_f32 v138, v140, v144 op_sel:[0,0,1]
	v_cvt_pk_fp8_f32 v142, v133, v137
	v_cvt_pk_fp8_f32 v142, v141, v145 op_sel:[0,0,1]
	v_cvt_pk_fp8_f32 v131, v146, v150
	v_cvt_pk_fp8_f32 v131, v154, v158 op_sel:[0,0,1]
	v_cvt_pk_fp8_f32 v135, v147, v151
	v_cvt_pk_fp8_f32 v135, v155, v159 op_sel:[0,0,1]
	v_cvt_pk_fp8_f32 v139, v148, v152
	v_cvt_pk_fp8_f32 v139, v156, v160 op_sel:[0,0,1]
	v_cvt_pk_fp8_f32 v143, v149, v153
	v_cvt_pk_fp8_f32 v143, v157, v161 op_sel:[0,0,1]
	v_cvt_pk_fp8_f32 v132, v162, v166
	v_cvt_pk_fp8_f32 v132, v170, v174 op_sel:[0,0,1]
	v_cvt_pk_fp8_f32 v136, v163, v167
	v_cvt_pk_fp8_f32 v136, v171, v175 op_sel:[0,0,1]
	v_cvt_pk_fp8_f32 v140, v164, v168
	v_cvt_pk_fp8_f32 v140, v172, v176 op_sel:[0,0,1]
	v_cvt_pk_fp8_f32 v144, v165, v169
	v_cvt_pk_fp8_f32 v144, v173, v177 op_sel:[0,0,1]
	v_cvt_pk_fp8_f32 v133, v178, v182
	v_cvt_pk_fp8_f32 v133, v186, v190 op_sel:[0,0,1]
	v_cvt_pk_fp8_f32 v137, v179, v183
	v_cvt_pk_fp8_f32 v137, v187, v191 op_sel:[0,0,1]
	v_cvt_pk_fp8_f32 v141, v180, v184
	v_cvt_pk_fp8_f32 v141, v188, v192 op_sel:[0,0,1]
	v_cvt_pk_fp8_f32 v145, v181, v185
	v_cvt_pk_fp8_f32 v145, v189, v193 op_sel:[0,0,1]
	global_store_dwordx4 v250, v[130:133], s[42:43] nt
	global_store_dwordx4 v250, v[134:137], s[42:43] offset:2048 nt
	global_store_dwordx4 v251, v[138:141], s[42:43] nt
	global_store_dwordx4 v251, v[142:145], s[42:43] offset:2048 nt
	s_add_u32 s42, s42, 0x200
	s_addc_u32 s43, s43, 0
	global_load_dwordx4 v[130:133], v246, s[4:5] nt
	global_load_dwordx4 v[134:137], v247, s[4:5] nt
	global_load_dwordx4 v[138:141], v248, s[4:5] nt
	global_load_dwordx4 v[142:145], v249, s[4:5] nt
	global_load_dwordx4 v[146:149], v246, s[6:7] nt
	global_load_dwordx4 v[150:153], v247, s[6:7] nt
	global_load_dwordx4 v[154:157], v248, s[6:7] nt
	global_load_dwordx4 v[158:161], v249, s[6:7] nt
	global_load_dwordx4 v[162:165], v246, s[8:9] nt
	global_load_dwordx4 v[166:169], v247, s[8:9] nt
	global_load_dwordx4 v[170:173], v248, s[8:9] nt
	global_load_dwordx4 v[174:177], v249, s[8:9] nt
	global_load_dwordx4 v[178:181], v246, s[38:39] nt
	global_load_dwordx4 v[182:185], v247, s[38:39] nt
	global_load_dwordx4 v[186:189], v248, s[38:39] nt
	global_load_dwordx4 v[190:193], v249, s[38:39] nt
	s_add_u32 s4, s4, 0x400000
	s_addc_u32 s5, s5, 0
	s_add_u32 s6, s6, 0x400000
	s_addc_u32 s7, s7, 0
	s_add_u32 s8, s8, 0x400000
	s_addc_u32 s9, s9, 0
	s_add_u32 s38, s38, 0x400000
	s_addc_u32 s39, s39, 0
	s_waitcnt vmcnt(40)
; #define GAS __attribute__((address_space(1)))
; template <bool GAIN, bool NT = false> __device__ __forceinline__ void titem8_load(const TItem& d, int lane, f32x4 (&r)[16], f32x4 (&g)[4]) {
;     const int q = lane & 7, kg = lane >> 3; const unsigned lo = (unsigned)((16 * kg) * d.N + 4 * q) * 4u;
;     const GAS char* base = (const GAS char*)d.src;
; #pragma unroll
;     for (int j = 0; j < 16; ++j) { const GAS f32x4* p = (const GAS f32x4*)(base + (size_t)j * (size_t)d.N * 4 + lo); r[j] = NT ? __builtin_nontemporal_load(p) : *p; }
;     if constexpr (GAIN) { const GAS char* gb = (const GAS char*)d.gain; const unsigned go = (unsigned)(16 * kg) * 4u;
; #pragma unroll
;         for (int j4 = 0; j4 < 4; ++j4) g[j4] = *(const GAS f32x4*)(gb + 16 * j4 + go); }
;     asm volatile("" ::: "memory"); __builtin_amdgcn_sched_barrier(0);
; }
; template <bool GAIN, bool NT = false> __device__ __forceinline__ void titem8_store(const TItem& d, int lane, const f32x4 (&r)[16], const f32x4 (&g)[4]) {
;     const int q = lane & 7, kg = lane >> 3; const unsigned lo = (unsigned)((4 * q) * d.ldk + 16 * kg);
;     GAS char* base = (GAS char*)d.dst;
;     f32x4 s[16];
; #pragma unroll
;     for (int j = 0; j < 16; ++j) s[j] = r[j] * ((GAIN ? g[j >> 2][j & 3] : 1.0f) * W8_SCALE);
; #pragma unroll
;     for (int i = 0; i < 4; ++i) { v4u w;
;         w.x = pk4_fp8w(s[0][i], s[1][i], s[2][i], s[3][i]); w.y = pk4_fp8w(s[4][i], s[5][i], s[6][i], s[7][i]);
;         w.z = pk4_fp8w(s[8][i], s[9][i], s[10][i], s[11][i]); w.w = pk4_fp8w(s[12][i], s[13][i], s[14][i], s[15][i]);
;         GAS v4u* p = (GAS v4u*)(base + (size_t)i * (size_t)d.ldk + lo);
;         if (NT) __builtin_nontemporal_store(w, p); else *p = w; }
; }
	v_pk_mul_f32 v[0:1], v[0:1], s[30:31] op_sel_hi:[1,0]
	v_pk_mul_f32 v[2:3], v[2:3], s[30:31] op_sel_hi:[1,0]
	v_pk_mul_f32 v[4:5], v[4:5], s[30:31] op_sel_hi:[1,0]
	v_pk_mul_f32 v[6:7], v[6:7], s[30:31] op_sel_hi:[1,0]
	v_pk_mul_f32 v[8:9], v[8:9], s[30:31] op_sel_hi:[1,0]
	v_pk_mul_f32 v[10:11], v[10:11], s[30:31] op_sel_hi:[1,0]
	v_pk_mul_f32 v[12:13], v[12:13], s[30:31] op_sel_hi:[1,0]
	v_pk_mul_f32 v[14:15], v[14:15], s[30:31] op_sel_hi:[1,0]
	v_pk_mul_f32 v[16:17], v[16:17], s[30:31] op_sel_hi:[1,0]
	v_pk_mul_f32 v[18:19], v[18:19], s[30:31] op_sel_hi:[1,0]
	v_pk_mul_f32 v[20:21], v[20:21], s[30:31] op_sel_hi:[1,0]
	v_pk_mul_f32 v[22:23], v[22:23], s[30:31] op_sel_hi:[1,0]
	v_pk_mul_f32 v[24:25], v[24:25], s[30:31] op_sel_hi:[1,0]
	v_pk_mul_f32 v[26:27], v[26:27], s[30:31] op_sel_hi:[1,0]
	v_pk_mul_f32 v[28:29], v[28:29], s[30:31] op_sel_hi:[1,0]
	v_pk_mul_f32 v[30:31], v[30:31], s[30:31] op_sel_hi:[1,0]
	v_pk_mul_f32 v[32:33], v[32:33], s[30:31] op_sel_hi:[1,0]
	v_pk_mul_f32 v[34:35], v[34:35], s[30:31] op_sel_hi:[1,0]
	v_pk_mul_f32 v[36:37], v[36:37], s[30:31] op_sel_hi:[1,0]
	v_pk_mul_f32 v[38:39], v[38:39], s[30:31] op_sel_hi:[1,0]
	v_pk_mul_f32 v[40:41], v[40:41], s[30:31] op_sel_hi:[1,0]
	v_pk_mul_f32 v[42:43], v[42:43], s[30:31] op_sel_hi:[1,0]
	v_pk_mul_f32 v[44:45], v[44:45], s[30:31] op_sel_hi:[1,0]
	v_pk_mul_f32 v[46:47], v[46:47], s[30:31] op_sel_hi:[1,0]
	v_pk_mul_f32 v[48:49], v[48:49], s[30:31] op_sel_hi:[1,0]
	v_pk_mul_f32 v[50:51], v[50:51], s[30:31] op_sel_hi:[1,0]
	v_pk_mul_f32 v[52:53], v[52:53], s[30:31] op_sel_hi:[1,0]
	v_pk_mul_f32 v[54:55], v[54:55], s[30:31] op_sel_hi:[1,0]
	v_pk_mul_f32 v[56:57], v[56:57], s[30:31] op_sel_hi:[1,0]
	v_pk_mul_f32 v[58:59], v[58:59], s[30:31] op_sel_hi:[1,0]
	v_pk_mul_f32 v[60:61], v[60:61], s[30:31] op_sel_hi:[1,0]
	v_pk_mul_f32 v[62:63], v[62:63], s[30:31] op_sel_hi:[1,0]
	v_med3_f32 v0, v0, s24, v237
	v_med3_f32 v1, v1, s24, v237
	v_med3_f32 v2, v2, s24, v237
	v_med3_f32 v3, v3, s24, v237
	v_med3_f32 v4, v4, s24, v237
	v_med3_f32 v5, v5, s24, v237
	v_med3_f32 v6, v6, s24, v237
	v_med3_f32 v7, v7, s24, v237
	v_med3_f32 v8, v8, s24, v237
	v_med3_f32 v9, v9, s24, v237
	v_med3_f32 v10, v10, s24, v237
	v_med3_f32 v11, v11, s24, v237
	v_med3_f32 v12, v12, s24, v237
	v_med3_f32 v13, v13, s24, v237
	v_med3_f32 v14, v14, s24, v237
	v_med3_f32 v15, v15, s24, v237
	v_med3_f32 v16, v16, s24, v237
	v_med3_f32 v17, v17, s24, v237
	v_med3_f32 v18, v18, s24, v237
	v_med3_f32 v19, v19, s24, v237
	v_med3_f32 v20, v20, s24, v237
	v_med3_f32 v21, v21, s24, v237
	v_med3_f32 v22, v22, s24, v237
	v_med3_f32 v23, v23, s24, v237
	v_med3_f32 v24, v24, s24, v237
	v_med3_f32 v25, v25, s24, v237
	v_med3_f32 v26, v26, s24, v237
	v_med3_f32 v27, v27, s24, v237
	v_med3_f32 v28, v28, s24, v237
	v_med3_f32 v29, v29, s24, v237
	v_med3_f32 v30, v30, s24, v237
	v_med3_f32 v31, v31, s24, v237
	v_med3_f32 v32, v32, s24, v237
	v_med3_f32 v33, v33, s24, v237
	v_med3_f32 v34, v34, s24, v237
	v_med3_f32 v35, v35, s24, v237
	v_med3_f32 v36, v36, s24, v237
	v_med3_f32 v37, v37, s24, v237
	v_med3_f32 v38, v38, s24, v237
	v_med3_f32 v39, v39, s24, v237
	v_med3_f32 v40, v40, s24, v237
	v_med3_f32 v41, v41, s24, v237
	v_med3_f32 v42, v42, s24, v237
	v_med3_f32 v43, v43, s24, v237
	v_med3_f32 v44, v44, s24, v237
	v_med3_f32 v45, v45, s24, v237
	v_med3_f32 v46, v46, s24, v237
	v_med3_f32 v47, v47, s24, v237
	v_med3_f32 v48, v48, s24, v237
	v_med3_f32 v49, v49, s24, v237
	v_med3_f32 v50, v50, s24, v237
	v_med3_f32 v51, v51, s24, v237
	v_med3_f32 v52, v52, s24, v237
	v_med3_f32 v53, v53, s24, v237
	v_med3_f32 v54, v54, s24, v237
	v_med3_f32 v55, v55, s24, v237
	v_med3_f32 v56, v56, s24, v237
	v_med3_f32 v57, v57, s24, v237
	v_med3_f32 v58, v58, s24, v237
	v_med3_f32 v59, v59, s24, v237
	v_med3_f32 v60, v60, s24, v237
	v_med3_f32 v61, v61, s24, v237
	v_med3_f32 v62, v62, s24, v237
	v_med3_f32 v63, v63, s24, v237
	v_cvt_pk_fp8_f32 v0, v0, v4
	v_cvt_pk_fp8_f32 v0, v8, v12 op_sel:[0,0,1]
	v_cvt_pk_fp8_f32 v4, v1, v5
	v_cvt_pk_fp8_f32 v4, v9, v13 op_sel:[0,0,1]
	v_cvt_pk_fp8_f32 v8, v2, v6
	v_cvt_pk_fp8_f32 v8, v10, v14 op_sel:[0,0,1]
	v_cvt_pk_fp8_f32 v12, v3, v7
	v_cvt_pk_fp8_f32 v12, v11, v15 op_sel:[0,0,1]
	v_cvt_pk_fp8_f32 v1, v16, v20
	v_cvt_pk_fp8_f32 v1, v24, v28 op_sel:[0,0,1]
	v_cvt_pk_fp8_f32 v5, v17, v21
	v_cvt_pk_fp8_f32 v5, v25, v29 op_sel:[0,0,1]
	v_cvt_pk_fp8_f32 v9, v18, v22
	v_cvt_pk_fp8_f32 v9, v26, v30 op_sel:[0,0,1]
	v_cvt_pk_fp8_f32 v13, v19, v23
	v_cvt_pk_fp8_f32 v13, v27, v31 op_sel:[0,0,1]
	v_cvt_pk_fp8_f32 v2, v32, v36
	v_cvt_pk_fp8_f32 v2, v40, v44 op_sel:[0,0,1]
	v_cvt_pk_fp8_f32 v6, v33, v37
	v_cvt_pk_fp8_f32 v6, v41, v45 op_sel:[0,0,1]
	v_cvt_pk_fp8_f32 v10, v34, v38
	v_cvt_pk_fp8_f32 v10, v42, v46 op_sel:[0,0,1]
	v_cvt_pk_fp8_f32 v14, v35, v39
	v_cvt_pk_fp8_f32 v14, v43, v47 op_sel:[0,0,1]
	v_cvt_pk_fp8_f32 v3, v48, v52
	v_cvt_pk_fp8_f32 v3, v56, v60 op_sel:[0,0,1]
	v_cvt_pk_fp8_f32 v7, v49, v53
	v_cvt_pk_fp8_f32 v7, v57, v61 op_sel:[0,0,1]
	v_cvt_pk_fp8_f32 v11, v50, v54
	v_cvt_pk_fp8_f32 v11, v58, v62 op_sel:[0,0,1]
	v_cvt_pk_fp8_f32 v15, v51, v55
	v_cvt_pk_fp8_f32 v15, v59, v63 op_sel:[0,0,1]
	global_store_dwordx4 v250, v[0:3], s[42:43] nt
	global_store_dwordx4 v250, v[4:7], s[42:43] offset:2048 nt
	global_store_dwordx4 v251, v[8:11], s[42:43] nt
	global_store_dwordx4 v251, v[12:15], s[42:43] offset:2048 nt
	s_add_u32 s42, s42, 0x200
	s_addc_u32 s43, s43, 0
	global_load_dwordx4 v[0:3], v246, s[4:5] nt
	global_load_dwordx4 v[4:7], v247, s[4:5] nt
	global_load_dwordx4 v[8:11], v248, s[4:5] nt
	global_load_dwordx4 v[12:15], v249, s[4:5] nt
	global_load_dwordx4 v[16:19], v246, s[6:7] nt
	global_load_dwordx4 v[20:23], v247, s[6:7] nt
	global_load_dwordx4 v[24:27], v248, s[6:7] nt
	global_load_dwordx4 v[28:31], v249, s[6:7] nt
	global_load_dwordx4 v[32:35], v246, s[8:9] nt
	global_load_dwordx4 v[36:39], v247, s[8:9] nt
	global_load_dwordx4 v[40:43], v248, s[8:9] nt
	global_load_dwordx4 v[44:47], v249, s[8:9] nt
	global_load_dwordx4 v[48:51], v246, s[38:39] nt
	global_load_dwordx4 v[52:55], v247, s[38:39] nt
	global_load_dwordx4 v[56:59], v248, s[38:39] nt
	global_load_dwordx4 v[60:63], v249, s[38:39] nt
	s_add_u32 s4, s4, 0x400000
	s_addc_u32 s5, s5, 0
	s_add_u32 s6, s6, 0x400000
	s_addc_u32 s7, s7, 0
	s_add_u32 s8, s8, 0x400000
	s_addc_u32 s9, s9, 0
	s_add_u32 s38, s38, 0x400000
	s_addc_u32 s39, s39, 0
	s_waitcnt vmcnt(40)
; #define GAS __attribute__((address_space(1)))
; template <bool GAIN, bool NT = false> __device__ __forceinline__ void titem8_load(const TItem& d, int lane, f32x4 (&r)[16], f32x4 (&g)[4]) {
;     const int q = lane & 7, kg = lane >> 3; const unsigned lo = (unsigned)((16 * kg) * d.N + 4 * q) * 4u;
;     const GAS char* base = (const GAS char*)d.src;
; #pragma unroll
;     for (int j = 0; j < 16; ++j) { const GAS f32x4* p = (const GAS f32x4*)(base + (size_t)j * (size_t)d.N * 4 + lo); r[j] = NT ? __builtin_nontemporal_load(p) : *p; }
;     if constexpr (GAIN) { const GAS char* gb = (const GAS char*)d.gain; const unsigned go = (unsigned)(16 * kg) * 4u;
; #pragma unroll
;         for (int j4 = 0; j4 < 4; ++j4) g[j4] = *(const GAS f32x4*)(gb + 16 * j4 + go); }
;     asm volatile("" ::: "memory"); __builtin_amdgcn_sched_barrier(0);
; }
; template <bool GAIN, bool NT = false> __device__ __forceinline__ void titem8_store(const TItem& d, int lane, const f32x4 (&r)[16], const f32x4 (&g)[4]) {
;     const int q = lane & 7, kg = lane >> 3; const unsigned lo = (unsigned)((4 * q) * d.ldk + 16 * kg);
;     GAS char* base = (GAS char*)d.dst;
;     f32x4 s[16];
; #pragma unroll
;     for (int j = 0; j < 16; ++j) s[j] = r[j] * ((GAIN ? g[j >> 2][j & 3] : 1.0f) * W8_SCALE);
; #pragma unroll
;     for (int i = 0; i < 4; ++i) { v4u w;
;         w.x = pk4_fp8w(s[0][i], s[1][i], s[2][i], s[3][i]); w.y = pk4_fp8w(s[4][i], s[5][i], s[6][i], s[7][i]);
;         w.z = pk4_fp8w(s[8][i], s[9][i], s[10][i], s[11][i]); w.w = pk4_fp8w(s[12][i], s[13][i], s[14][i], s[15][i]);
;         GAS v4u* p = (GAS v4u*)(base + (size_t)i * (size_t)d.ldk + lo);
;         if (NT) __builtin_nontemporal_store(w, p); else *p = w; }
; }
	v_pk_mul_f32 v[66:67], v[66:67], s[30:31] op_sel_hi:[1,0]
	v_pk_mul_f32 v[68:69], v[68:69], s[30:31] op_sel_hi:[1,0]
	v_pk_mul_f32 v[70:71], v[70:71], s[30:31] op_sel_hi:[1,0]
	v_pk_mul_f32 v[72:73], v[72:73], s[30:31] op_sel_hi:[1,0]
	v_pk_mul_f32 v[74:75], v[74:75], s[30:31] op_sel_hi:[1,0]
	v_pk_mul_f32 v[76:77], v[76:77], s[30:31] op_sel_hi:[1,0]
	v_pk_mul_f32 v[78:79], v[78:79], s[30:31] op_sel_hi:[1,0]
	v_pk_mul_f32 v[80:81], v[80:81], s[30:31] op_sel_hi:[1,0]
	v_pk_mul_f32 v[82:83], v[82:83], s[30:31] op_sel_hi:[1,0]
	v_pk_mul_f32 v[84:85], v[84:85], s[30:31] op_sel_hi:[1,0]
	v_pk_mul_f32 v[86:87], v[86:87], s[30:31] op_sel_hi:[1,0]
	v_pk_mul_f32 v[88:89], v[88:89], s[30:31] op_sel_hi:[1,0]
	v_pk_mul_f32 v[90:91], v[90:91], s[30:31] op_sel_hi:[1,0]
	v_pk_mul_f32 v[92:93], v[92:93], s[30:31] op_sel_hi:[1,0]
	v_pk_mul_f32 v[94:95], v[94:95], s[30:31] op_sel_hi:[1,0]
	v_pk_mul_f32 v[96:97], v[96:97], s[30:31] op_sel_hi:[1,0]
	v_pk_mul_f32 v[98:99], v[98:99], s[30:31] op_sel_hi:[1,0]
	v_pk_mul_f32 v[100:101], v[100:101], s[30:31] op_sel_hi:[1,0]
	v_pk_mul_f32 v[102:103], v[102:103], s[30:31] op_sel_hi:[1,0]
	v_pk_mul_f32 v[104:105], v[104:105], s[30:31] op_sel_hi:[1,0]
	v_pk_mul_f32 v[106:107], v[106:107], s[30:31] op_sel_hi:[1,0]
	v_pk_mul_f32 v[108:109], v[108:109], s[30:31] op_sel_hi:[1,0]
	v_pk_mul_f32 v[110:111], v[110:111], s[30:31] op_sel_hi:[1,0]
	v_pk_mul_f32 v[112:113], v[112:113], s[30:31] op_sel_hi:[1,0]
	v_pk_mul_f32 v[114:115], v[114:115], s[30:31] op_sel_hi:[1,0]
	v_pk_mul_f32 v[116:117], v[116:117], s[30:31] op_sel_hi:[1,0]
	v_pk_mul_f32 v[118:119], v[118:119], s[30:31] op_sel_hi:[1,0]
	v_pk_mul_f32 v[120:121], v[120:121], s[30:31] op_sel_hi:[1,0]
	v_pk_mul_f32 v[122:123], v[122:123], s[30:31] op_sel_hi:[1,0]
	v_pk_mul_f32 v[124:125], v[124:125], s[30:31] op_sel_hi:[1,0]
	v_pk_mul_f32 v[126:127], v[126:127], s[30:31] op_sel_hi:[1,0]
	v_pk_mul_f32 v[128:129], v[128:129], s[30:31] op_sel_hi:[1,0]
	v_med3_f32 v66, v66, s24, v237
	v_med3_f32 v67, v67, s24, v237
	v_med3_f32 v68, v68, s24, v237
	v_med3_f32 v69, v69, s24, v237
	v_med3_f32 v70, v70, s24, v237
	v_med3_f32 v71, v71, s24, v237
	v_med3_f32 v72, v72, s24, v237
	v_med3_f32 v73, v73, s24, v237
	v_med3_f32 v74, v74, s24, v237
	v_med3_f32 v75, v75, s24, v237
	v_med3_f32 v76, v76, s24, v237
	v_med3_f32 v77, v77, s24, v237
	v_med3_f32 v78, v78, s24, v237
	v_med3_f32 v79, v79, s24, v237
	v_med3_f32 v80, v80, s24, v237
	v_med3_f32 v81, v81, s24, v237
	v_med3_f32 v82, v82, s24, v237
	v_med3_f32 v83, v83, s24, v237
	v_med3_f32 v84, v84, s24, v237
	v_med3_f32 v85, v85, s24, v237
	v_med3_f32 v86, v86, s24, v237
	v_med3_f32 v87, v87, s24, v237
	v_med3_f32 v88, v88, s24, v237
	v_med3_f32 v89, v89, s24, v237
	v_med3_f32 v90, v90, s24, v237
	v_med3_f32 v91, v91, s24, v237
	v_med3_f32 v92, v92, s24, v237
	v_med3_f32 v93, v93, s24, v237
	v_med3_f32 v94, v94, s24, v237
	v_med3_f32 v95, v95, s24, v237
	v_med3_f32 v96, v96, s24, v237
	v_med3_f32 v97, v97, s24, v237
	v_med3_f32 v98, v98, s24, v237
	v_med3_f32 v99, v99, s24, v237
	v_med3_f32 v100, v100, s24, v237
	v_med3_f32 v101, v101, s24, v237
	v_med3_f32 v102, v102, s24, v237
	v_med3_f32 v103, v103, s24, v237
	v_med3_f32 v104, v104, s24, v237
	v_med3_f32 v105, v105, s24, v237
	v_med3_f32 v106, v106, s24, v237
	v_med3_f32 v107, v107, s24, v237
	v_med3_f32 v108, v108, s24, v237
	v_med3_f32 v109, v109, s24, v237
	v_med3_f32 v110, v110, s24, v237
	v_med3_f32 v111, v111, s24, v237
	v_med3_f32 v112, v112, s24, v237
	v_med3_f32 v113, v113, s24, v237
	v_med3_f32 v114, v114, s24, v237
	v_med3_f32 v115, v115, s24, v237
	v_med3_f32 v116, v116, s24, v237
	v_med3_f32 v117, v117, s24, v237
	v_med3_f32 v118, v118, s24, v237
	v_med3_f32 v119, v119, s24, v237
	v_med3_f32 v120, v120, s24, v237
	v_med3_f32 v121, v121, s24, v237
	v_med3_f32 v122, v122, s24, v237
	v_med3_f32 v123, v123, s24, v237
	v_med3_f32 v124, v124, s24, v237
	v_med3_f32 v125, v125, s24, v237
	v_med3_f32 v126, v126, s24, v237
	v_med3_f32 v127, v127, s24, v237
	v_med3_f32 v128, v128, s24, v237
	v_med3_f32 v129, v129, s24, v237
	v_cvt_pk_fp8_f32 v66, v66, v70
	v_cvt_pk_fp8_f32 v66, v74, v78 op_sel:[0,0,1]
	v_cvt_pk_fp8_f32 v70, v67, v71
	v_cvt_pk_fp8_f32 v70, v75, v79 op_sel:[0,0,1]
	v_cvt_pk_fp8_f32 v74, v68, v72
	v_cvt_pk_fp8_f32 v74, v76, v80 op_sel:[0,0,1]
	v_cvt_pk_fp8_f32 v78, v69, v73
	v_cvt_pk_fp8_f32 v78, v77, v81 op_sel:[0,0,1]
	v_cvt_pk_fp8_f32 v67, v82, v86
	v_cvt_pk_fp8_f32 v67, v90, v94 op_sel:[0,0,1]
	v_cvt_pk_fp8_f32 v71, v83, v87
	v_cvt_pk_fp8_f32 v71, v91, v95 op_sel:[0,0,1]
	v_cvt_pk_fp8_f32 v75, v84, v88
	v_cvt_pk_fp8_f32 v75, v92, v96 op_sel:[0,0,1]
	v_cvt_pk_fp8_f32 v79, v85, v89
	v_cvt_pk_fp8_f32 v79, v93, v97 op_sel:[0,0,1]
	v_cvt_pk_fp8_f32 v68, v98, v102
	v_cvt_pk_fp8_f32 v68, v106, v110 op_sel:[0,0,1]
	v_cvt_pk_fp8_f32 v72, v99, v103
	v_cvt_pk_fp8_f32 v72, v107, v111 op_sel:[0,0,1]
	v_cvt_pk_fp8_f32 v76, v100, v104
	v_cvt_pk_fp8_f32 v76, v108, v112 op_sel:[0,0,1]
	v_cvt_pk_fp8_f32 v80, v101, v105
	v_cvt_pk_fp8_f32 v80, v109, v113 op_sel:[0,0,1]
	v_cvt_pk_fp8_f32 v69, v114, v118
	v_cvt_pk_fp8_f32 v69, v122, v126 op_sel:[0,0,1]
	v_cvt_pk_fp8_f32 v73, v115, v119
	v_cvt_pk_fp8_f32 v73, v123, v127 op_sel:[0,0,1]
	v_cvt_pk_fp8_f32 v77, v116, v120
	v_cvt_pk_fp8_f32 v77, v124, v128 op_sel:[0,0,1]
	v_cvt_pk_fp8_f32 v81, v117, v121
	v_cvt_pk_fp8_f32 v81, v125, v129 op_sel:[0,0,1]
	global_store_dwordx4 v250, v[66:69], s[42:43] nt
	global_store_dwordx4 v250, v[70:73], s[42:43] offset:2048 nt
	global_store_dwordx4 v251, v[74:77], s[42:43] nt
	global_store_dwordx4 v251, v[78:81], s[42:43] offset:2048 nt
	s_add_u32 s42, s42, 0x3ffa00
	s_addc_u32 s43, s43, 0
	global_load_dwordx4 v[66:69], v246, s[4:5] nt
	global_load_dwordx4 v[70:73], v247, s[4:5] nt
	global_load_dwordx4 v[74:77], v248, s[4:5] nt
	global_load_dwordx4 v[78:81], v249, s[4:5] nt
	global_load_dwordx4 v[82:85], v246, s[6:7] nt
	global_load_dwordx4 v[86:89], v247, s[6:7] nt
	global_load_dwordx4 v[90:93], v248, s[6:7] nt
	global_load_dwordx4 v[94:97], v249, s[6:7] nt
	global_load_dwordx4 v[98:101], v246, s[8:9] nt
	global_load_dwordx4 v[102:105], v247, s[8:9] nt
	global_load_dwordx4 v[106:109], v248, s[8:9] nt
	global_load_dwordx4 v[110:113], v249, s[8:9] nt
	global_load_dwordx4 v[114:117], v246, s[38:39] nt
	global_load_dwordx4 v[118:121], v247, s[38:39] nt
	global_load_dwordx4 v[122:125], v248, s[38:39] nt
	global_load_dwordx4 v[126:129], v249, s[38:39] nt
	s_add_u32 s4, s4, 0x400000
	s_addc_u32 s5, s5, 0
	s_add_u32 s6, s6, 0x400000
	s_addc_u32 s7, s7, 0
	s_add_u32 s8, s8, 0x400000
	s_addc_u32 s9, s9, 0
	s_add_u32 s38, s38, 0x400000
	s_addc_u32 s39, s39, 0
	s_waitcnt vmcnt(40)
; #define GAS __attribute__((address_space(1)))
; template <bool GAIN, bool NT = false> __device__ __forceinline__ void titem8_load(const TItem& d, int lane, f32x4 (&r)[16], f32x4 (&g)[4]) {
;     const int q = lane & 7, kg = lane >> 3; const unsigned lo = (unsigned)((16 * kg) * d.N + 4 * q) * 4u;
;     const GAS char* base = (const GAS char*)d.src;
; #pragma unroll
;     for (int j = 0; j < 16; ++j) { const GAS f32x4* p = (const GAS f32x4*)(base + (size_t)j * (size_t)d.N * 4 + lo); r[j] = NT ? __builtin_nontemporal_load(p) : *p; }
;     if constexpr (GAIN) { const GAS char* gb = (const GAS char*)d.gain; const unsigned go = (unsigned)(16 * kg) * 4u;
; #pragma unroll
;         for (int j4 = 0; j4 < 4; ++j4) g[j4] = *(const GAS f32x4*)(gb + 16 * j4 + go); }
;     asm volatile("" ::: "memory"); __builtin_amdgcn_sched_barrier(0);
; }
; template <bool GAIN, bool NT = false> __device__ __forceinline__ void titem8_store(const TItem& d, int lane, const f32x4 (&r)[16], const f32x4 (&g)[4]) {
;     const int q = lane & 7, kg = lane >> 3; const unsigned lo = (unsigned)((4 * q) * d.ldk + 16 * kg);
;     GAS char* base = (GAS char*)d.dst;
;     f32x4 s[16];
; #pragma unroll
;     for (int j = 0; j < 16; ++j) s[j] = r[j] * ((GAIN ? g[j >> 2][j & 3] : 1.0f) * W8_SCALE);
; #pragma unroll
;     for (int i = 0; i < 4; ++i) { v4u w;
;         w.x = pk4_fp8w(s[0][i], s[1][i], s[2][i], s[3][i]); w.y = pk4_fp8w(s[4][i], s[5][i], s[6][i], s[7][i]);
;         w.z = pk4_fp8w(s[8][i], s[9][i], s[10][i], s[11][i]); w.w = pk4_fp8w(s[12][i], s[13][i], s[14][i], s[15][i]);
;         GAS v4u* p = (GAS v4u*)(base + (size_t)i * (size_t)d.ldk + lo);
;         if (NT) __builtin_nontemporal_store(w, p); else *p = w; }
; }
	v_pk_mul_f32 v[130:131], v[130:131], s[30:31] op_sel_hi:[1,0]
	v_pk_mul_f32 v[132:133], v[132:133], s[30:31] op_sel_hi:[1,0]
	v_pk_mul_f32 v[134:135], v[134:135], s[30:31] op_sel_hi:[1,0]
	v_pk_mul_f32 v[136:137], v[136:137], s[30:31] op_sel_hi:[1,0]
	v_pk_mul_f32 v[138:139], v[138:139], s[30:31] op_sel_hi:[1,0]
	v_pk_mul_f32 v[140:141], v[140:141], s[30:31] op_sel_hi:[1,0]
	v_pk_mul_f32 v[142:143], v[142:143], s[30:31] op_sel_hi:[1,0]
	v_pk_mul_f32 v[144:145], v[144:145], s[30:31] op_sel_hi:[1,0]
	v_pk_mul_f32 v[146:147], v[146:147], s[30:31] op_sel_hi:[1,0]
	v_pk_mul_f32 v[148:149], v[148:149], s[30:31] op_sel_hi:[1,0]
	v_pk_mul_f32 v[150:151], v[150:151], s[30:31] op_sel_hi:[1,0]
	v_pk_mul_f32 v[152:153], v[152:153], s[30:31] op_sel_hi:[1,0]
	v_pk_mul_f32 v[154:155], v[154:155], s[30:31] op_sel_hi:[1,0]
	v_pk_mul_f32 v[156:157], v[156:157], s[30:31] op_sel_hi:[1,0]
	v_pk_mul_f32 v[158:159], v[158:159], s[30:31] op_sel_hi:[1,0]
	v_pk_mul_f32 v[160:161], v[160:161], s[30:31] op_sel_hi:[1,0]
	v_pk_mul_f32 v[162:163], v[162:163], s[30:31] op_sel_hi:[1,0]
	v_pk_mul_f32 v[164:165], v[164:165], s[30:31] op_sel_hi:[1,0]
	v_pk_mul_f32 v[166:167], v[166:167], s[30:31] op_sel_hi:[1,0]
	v_pk_mul_f32 v[168:169], v[168:169], s[30:31] op_sel_hi:[1,0]
	v_pk_mul_f32 v[170:171], v[170:171], s[30:31] op_sel_hi:[1,0]
	v_pk_mul_f32 v[172:173], v[172:173], s[30:31] op_sel_hi:[1,0]
	v_pk_mul_f32 v[174:175], v[174:175], s[30:31] op_sel_hi:[1,0]
	v_pk_mul_f32 v[176:177], v[176:177], s[30:31] op_sel_hi:[1,0]
	v_pk_mul_f32 v[178:179], v[178:179], s[30:31] op_sel_hi:[1,0]
	v_pk_mul_f32 v[180:181], v[180:181], s[30:31] op_sel_hi:[1,0]
	v_pk_mul_f32 v[182:183], v[182:183], s[30:31] op_sel_hi:[1,0]
	v_pk_mul_f32 v[184:185], v[184:185], s[30:31] op_sel_hi:[1,0]
	v_pk_mul_f32 v[186:187], v[186:187], s[30:31] op_sel_hi:[1,0]
	v_pk_mul_f32 v[188:189], v[188:189], s[30:31] op_sel_hi:[1,0]
	v_pk_mul_f32 v[190:191], v[190:191], s[30:31] op_sel_hi:[1,0]
	v_pk_mul_f32 v[192:193], v[192:193], s[30:31] op_sel_hi:[1,0]
	v_med3_f32 v130, v130, s24, v237
	v_med3_f32 v131, v131, s24, v237
	v_med3_f32 v132, v132, s24, v237
	v_med3_f32 v133, v133, s24, v237
	v_med3_f32 v134, v134, s24, v237
	v_med3_f32 v135, v135, s24, v237
	v_med3_f32 v136, v136, s24, v237
	v_med3_f32 v137, v137, s24, v237
	v_med3_f32 v138, v138, s24, v237
	v_med3_f32 v139, v139, s24, v237
	v_med3_f32 v140, v140, s24, v237
	v_med3_f32 v141, v141, s24, v237
	v_med3_f32 v142, v142, s24, v237
	v_med3_f32 v143, v143, s24, v237
	v_med3_f32 v144, v144, s24, v237
	v_med3_f32 v145, v145, s24, v237
	v_med3_f32 v146, v146, s24, v237
	v_med3_f32 v147, v147, s24, v237
	v_med3_f32 v148, v148, s24, v237
	v_med3_f32 v149, v149, s24, v237
	v_med3_f32 v150, v150, s24, v237
	v_med3_f32 v151, v151, s24, v237
	v_med3_f32 v152, v152, s24, v237
	v_med3_f32 v153, v153, s24, v237
	v_med3_f32 v154, v154, s24, v237
	v_med3_f32 v155, v155, s24, v237
	v_med3_f32 v156, v156, s24, v237
	v_med3_f32 v157, v157, s24, v237
	v_med3_f32 v158, v158, s24, v237
	v_med3_f32 v159, v159, s24, v237
	v_med3_f32 v160, v160, s24, v237
	v_med3_f32 v161, v161, s24, v237
	v_med3_f32 v162, v162, s24, v237
	v_med3_f32 v163, v163, s24, v237
	v_med3_f32 v164, v164, s24, v237
	v_med3_f32 v165, v165, s24, v237
	v_med3_f32 v166, v166, s24, v237
	v_med3_f32 v167, v167, s24, v237
	v_med3_f32 v168, v168, s24, v237
	v_med3_f32 v169, v169, s24, v237
	v_med3_f32 v170, v170, s24, v237
	v_med3_f32 v171, v171, s24, v237
	v_med3_f32 v172, v172, s24, v237
	v_med3_f32 v173, v173, s24, v237
	v_med3_f32 v174, v174, s24, v237
	v_med3_f32 v175, v175, s24, v237
	v_med3_f32 v176, v176, s24, v237
	v_med3_f32 v177, v177, s24, v237
	v_med3_f32 v178, v178, s24, v237
	v_med3_f32 v179, v179, s24, v237
	v_med3_f32 v180, v180, s24, v237
	v_med3_f32 v181, v181, s24, v237
	v_med3_f32 v182, v182, s24, v237
	v_med3_f32 v183, v183, s24, v237
	v_med3_f32 v184, v184, s24, v237
	v_med3_f32 v185, v185, s24, v237
	v_med3_f32 v186, v186, s24, v237
	v_med3_f32 v187, v187, s24, v237
	v_med3_f32 v188, v188, s24, v237
	v_med3_f32 v189, v189, s24, v237
	v_med3_f32 v190, v190, s24, v237
	v_med3_f32 v191, v191, s24, v237
	v_med3_f32 v192, v192, s24, v237
	v_med3_f32 v193, v193, s24, v237
	v_cvt_pk_fp8_f32 v130, v130, v134
	v_cvt_pk_fp8_f32 v130, v138, v142 op_sel:[0,0,1]
	v_cvt_pk_fp8_f32 v134, v131, v135
	v_cvt_pk_fp8_f32 v134, v139, v143 op_sel:[0,0,1]
	v_cvt_pk_fp8_f32 v138, v132, v136
	v_cvt_pk_fp8_f32 v138, v140, v144 op_sel:[0,0,1]
	v_cvt_pk_fp8_f32 v142, v133, v137
	v_cvt_pk_fp8_f32 v142, v141, v145 op_sel:[0,0,1]
	v_cvt_pk_fp8_f32 v131, v146, v150
	v_cvt_pk_fp8_f32 v131, v154, v158 op_sel:[0,0,1]
	v_cvt_pk_fp8_f32 v135, v147, v151
	v_cvt_pk_fp8_f32 v135, v155, v159 op_sel:[0,0,1]
	v_cvt_pk_fp8_f32 v139, v148, v152
	v_cvt_pk_fp8_f32 v139, v156, v160 op_sel:[0,0,1]
	v_cvt_pk_fp8_f32 v143, v149, v153
	v_cvt_pk_fp8_f32 v143, v157, v161 op_sel:[0,0,1]
	v_cvt_pk_fp8_f32 v132, v162, v166
	v_cvt_pk_fp8_f32 v132, v170, v174 op_sel:[0,0,1]
	v_cvt_pk_fp8_f32 v136, v163, v167
	v_cvt_pk_fp8_f32 v136, v171, v175 op_sel:[0,0,1]
	v_cvt_pk_fp8_f32 v140, v164, v168
	v_cvt_pk_fp8_f32 v140, v172, v176 op_sel:[0,0,1]
	v_cvt_pk_fp8_f32 v144, v165, v169
	v_cvt_pk_fp8_f32 v144, v173, v177 op_sel:[0,0,1]
	v_cvt_pk_fp8_f32 v133, v178, v182
	v_cvt_pk_fp8_f32 v133, v186, v190 op_sel:[0,0,1]
	v_cvt_pk_fp8_f32 v137, v179, v183
	v_cvt_pk_fp8_f32 v137, v187, v191 op_sel:[0,0,1]
	v_cvt_pk_fp8_f32 v141, v180, v184
	v_cvt_pk_fp8_f32 v141, v188, v192 op_sel:[0,0,1]
	v_cvt_pk_fp8_f32 v145, v181, v185
	v_cvt_pk_fp8_f32 v145, v189, v193 op_sel:[0,0,1]
	global_store_dwordx4 v250, v[130:133], s[42:43] nt
	global_store_dwordx4 v250, v[134:137], s[42:43] offset:2048 nt
	global_store_dwordx4 v251, v[138:141], s[42:43] nt
	global_store_dwordx4 v251, v[142:145], s[42:43] offset:2048 nt
	s_add_u32 s42, s42, 0x200
	s_addc_u32 s43, s43, 0
	global_load_dwordx4 v[130:133], v246, s[4:5] nt
	global_load_dwordx4 v[134:137], v247, s[4:5] nt
	global_load_dwordx4 v[138:141], v248, s[4:5] nt
	global_load_dwordx4 v[142:145], v249, s[4:5] nt
	global_load_dwordx4 v[146:149], v246, s[6:7] nt
	global_load_dwordx4 v[150:153], v247, s[6:7] nt
	global_load_dwordx4 v[154:157], v248, s[6:7] nt
	global_load_dwordx4 v[158:161], v249, s[6:7] nt
	global_load_dwordx4 v[162:165], v246, s[8:9] nt
	global_load_dwordx4 v[166:169], v247, s[8:9] nt
	global_load_dwordx4 v[170:173], v248, s[8:9] nt
	global_load_dwordx4 v[174:177], v249, s[8:9] nt
	global_load_dwordx4 v[178:181], v246, s[38:39] nt
	global_load_dwordx4 v[182:185], v247, s[38:39] nt
	global_load_dwordx4 v[186:189], v248, s[38:39] nt
	global_load_dwordx4 v[190:193], v249, s[38:39] nt
	s_add_u32 s4, s4, 0x400000
	s_addc_u32 s5, s5, 0
	s_add_u32 s6, s6, 0x400000
	s_addc_u32 s7, s7, 0
	s_add_u32 s8, s8, 0x400000
	s_addc_u32 s9, s9, 0
	s_add_u32 s38, s38, 0x400000
	s_addc_u32 s39, s39, 0
	s_waitcnt vmcnt(40)
; #define GAS __attribute__((address_space(1)))
; template <bool GAIN, bool NT = false> __device__ __forceinline__ void titem8_load(const TItem& d, int lane, f32x4 (&r)[16], f32x4 (&g)[4]) {
;     const int q = lane & 7, kg = lane >> 3; const unsigned lo = (unsigned)((16 * kg) * d.N + 4 * q) * 4u;
;     const GAS char* base = (const GAS char*)d.src;
; #pragma unroll
;     for (int j = 0; j < 16; ++j) { const GAS f32x4* p = (const GAS f32x4*)(base + (size_t)j * (size_t)d.N * 4 + lo); r[j] = NT ? __builtin_nontemporal_load(p) : *p; }
;     if constexpr (GAIN) { const GAS char* gb = (const GAS char*)d.gain; const unsigned go = (unsigned)(16 * kg) * 4u;
; #pragma unroll
;         for (int j4 = 0; j4 < 4; ++j4) g[j4] = *(const GAS f32x4*)(gb + 16 * j4 + go); }
;     asm volatile("" ::: "memory"); __builtin_amdgcn_sched_barrier(0);
; }
; template <bool GAIN, bool NT = false> __device__ __forceinline__ void titem8_store(const TItem& d, int lane, const f32x4 (&r)[16], const f32x4 (&g)[4]) {
;     const int q = lane & 7, kg = lane >> 3; const unsigned lo = (unsigned)((4 * q) * d.ldk + 16 * kg);
;     GAS char* base = (GAS char*)d.dst;
;     f32x4 s[16];
; #pragma unroll
;     for (int j = 0; j < 16; ++j) s[j] = r[j] * ((GAIN ? g[j >> 2][j & 3] : 1.0f) * W8_SCALE);
; #pragma unroll
;     for (int i = 0; i < 4; ++i) { v4u w;
;         w.x = pk4_fp8w(s[0][i], s[1][i], s[2][i], s[3][i]); w.y = pk4_fp8w(s[4][i], s[5][i], s[6][i], s[7][i]);
;         w.z = pk4_fp8w(s[8][i], s[9][i], s[10][i], s[11][i]); w.w = pk4_fp8w(s[12][i], s[13][i], s[14][i], s[15][i]);
;         GAS v4u* p = (GAS v4u*)(base + (size_t)i * (size_t)d.ldk + lo);
;         if (NT) __builtin_nontemporal_store(w, p); else *p = w; }
; }
	v_pk_mul_f32 v[0:1], v[0:1], s[30:31] op_sel_hi:[1,0]
	v_pk_mul_f32 v[2:3], v[2:3], s[30:31] op_sel_hi:[1,0]
	v_pk_mul_f32 v[4:5], v[4:5], s[30:31] op_sel_hi:[1,0]
	v_pk_mul_f32 v[6:7], v[6:7], s[30:31] op_sel_hi:[1,0]
	v_pk_mul_f32 v[8:9], v[8:9], s[30:31] op_sel_hi:[1,0]
	v_pk_mul_f32 v[10:11], v[10:11], s[30:31] op_sel_hi:[1,0]
	v_pk_mul_f32 v[12:13], v[12:13], s[30:31] op_sel_hi:[1,0]
	v_pk_mul_f32 v[14:15], v[14:15], s[30:31] op_sel_hi:[1,0]
	v_pk_mul_f32 v[16:17], v[16:17], s[30:31] op_sel_hi:[1,0]
	v_pk_mul_f32 v[18:19], v[18:19], s[30:31] op_sel_hi:[1,0]
	v_pk_mul_f32 v[20:21], v[20:21], s[30:31] op_sel_hi:[1,0]
	v_pk_mul_f32 v[22:23], v[22:23], s[30:31] op_sel_hi:[1,0]
	v_pk_mul_f32 v[24:25], v[24:25], s[30:31] op_sel_hi:[1,0]
	v_pk_mul_f32 v[26:27], v[26:27], s[30:31] op_sel_hi:[1,0]
	v_pk_mul_f32 v[28:29], v[28:29], s[30:31] op_sel_hi:[1,0]
	v_pk_mul_f32 v[30:31], v[30:31], s[30:31] op_sel_hi:[1,0]
	v_pk_mul_f32 v[32:33], v[32:33], s[30:31] op_sel_hi:[1,0]
	v_pk_mul_f32 v[34:35], v[34:35], s[30:31] op_sel_hi:[1,0]
	v_pk_mul_f32 v[36:37], v[36:37], s[30:31] op_sel_hi:[1,0]
	v_pk_mul_f32 v[38:39], v[38:39], s[30:31] op_sel_hi:[1,0]
	v_pk_mul_f32 v[40:41], v[40:41], s[30:31] op_sel_hi:[1,0]
	v_pk_mul_f32 v[42:43], v[42:43], s[30:31] op_sel_hi:[1,0]
	v_pk_mul_f32 v[44:45], v[44:45], s[30:31] op_sel_hi:[1,0]
	v_pk_mul_f32 v[46:47], v[46:47], s[30:31] op_sel_hi:[1,0]
	v_pk_mul_f32 v[48:49], v[48:49], s[30:31] op_sel_hi:[1,0]
	v_pk_mul_f32 v[50:51], v[50:51], s[30:31] op_sel_hi:[1,0]
	v_pk_mul_f32 v[52:53], v[52:53], s[30:31] op_sel_hi:[1,0]
	v_pk_mul_f32 v[54:55], v[54:55], s[30:31] op_sel_hi:[1,0]
	v_pk_mul_f32 v[56:57], v[56:57], s[30:31] op_sel_hi:[1,0]
	v_pk_mul_f32 v[58:59], v[58:59], s[30:31] op_sel_hi:[1,0]
	v_pk_mul_f32 v[60:61], v[60:61], s[30:31] op_sel_hi:[1,0]
	v_pk_mul_f32 v[62:63], v[62:63], s[30:31] op_sel_hi:[1,0]
	v_med3_f32 v0, v0, s24, v237
	v_med3_f32 v1, v1, s24, v237
	v_med3_f32 v2, v2, s24, v237
	v_med3_f32 v3, v3, s24, v237
	v_med3_f32 v4, v4, s24, v237
	v_med3_f32 v5, v5, s24, v237
	v_med3_f32 v6, v6, s24, v237
	v_med3_f32 v7, v7, s24, v237
	v_med3_f32 v8, v8, s24, v237
	v_med3_f32 v9, v9, s24, v237
	v_med3_f32 v10, v10, s24, v237
	v_med3_f32 v11, v11, s24, v237
	v_med3_f32 v12, v12, s24, v237
	v_med3_f32 v13, v13, s24, v237
	v_med3_f32 v14, v14, s24, v237
	v_med3_f32 v15, v15, s24, v237
	v_med3_f32 v16, v16, s24, v237
	v_med3_f32 v17, v17, s24, v237
	v_med3_f32 v18, v18, s24, v237
	v_med3_f32 v19, v19, s24, v237
	v_med3_f32 v20, v20, s24, v237
	v_med3_f32 v21, v21, s24, v237
	v_med3_f32 v22, v22, s24, v237
	v_med3_f32 v23, v23, s24, v237
	v_med3_f32 v24, v24, s24, v237
	v_med3_f32 v25, v25, s24, v237
	v_med3_f32 v26, v26, s24, v237
	v_med3_f32 v27, v27, s24, v237
	v_med3_f32 v28, v28, s24, v237
	v_med3_f32 v29, v29, s24, v237
	v_med3_f32 v30, v30, s24, v237
	v_med3_f32 v31, v31, s24, v237
	v_med3_f32 v32, v32, s24, v237
	v_med3_f32 v33, v33, s24, v237
	v_med3_f32 v34, v34, s24, v237
	v_med3_f32 v35, v35, s24, v237
	v_med3_f32 v36, v36, s24, v237
	v_med3_f32 v37, v37, s24, v237
	v_med3_f32 v38, v38, s24, v237
	v_med3_f32 v39, v39, s24, v237
	v_med3_f32 v40, v40, s24, v237
	v_med3_f32 v41, v41, s24, v237
	v_med3_f32 v42, v42, s24, v237
	v_med3_f32 v43, v43, s24, v237
	v_med3_f32 v44, v44, s24, v237
	v_med3_f32 v45, v45, s24, v237
	v_med3_f32 v46, v46, s24, v237
	v_med3_f32 v47, v47, s24, v237
	v_med3_f32 v48, v48, s24, v237
	v_med3_f32 v49, v49, s24, v237
	v_med3_f32 v50, v50, s24, v237
	v_med3_f32 v51, v51, s24, v237
	v_med3_f32 v52, v52, s24, v237
	v_med3_f32 v53, v53, s24, v237
	v_med3_f32 v54, v54, s24, v237
	v_med3_f32 v55, v55, s24, v237
	v_med3_f32 v56, v56, s24, v237
	v_med3_f32 v57, v57, s24, v237
	v_med3_f32 v58, v58, s24, v237
	v_med3_f32 v59, v59, s24, v237
	v_med3_f32 v60, v60, s24, v237
	v_med3_f32 v61, v61, s24, v237
	v_med3_f32 v62, v62, s24, v237
	v_med3_f32 v63, v63, s24, v237
	v_cvt_pk_fp8_f32 v0, v0, v4
	v_cvt_pk_fp8_f32 v0, v8, v12 op_sel:[0,0,1]
	v_cvt_pk_fp8_f32 v4, v1, v5
	v_cvt_pk_fp8_f32 v4, v9, v13 op_sel:[0,0,1]
	v_cvt_pk_fp8_f32 v8, v2, v6
	v_cvt_pk_fp8_f32 v8, v10, v14 op_sel:[0,0,1]
	v_cvt_pk_fp8_f32 v12, v3, v7
	v_cvt_pk_fp8_f32 v12, v11, v15 op_sel:[0,0,1]
	v_cvt_pk_fp8_f32 v1, v16, v20
	v_cvt_pk_fp8_f32 v1, v24, v28 op_sel:[0,0,1]
	v_cvt_pk_fp8_f32 v5, v17, v21
	v_cvt_pk_fp8_f32 v5, v25, v29 op_sel:[0,0,1]
	v_cvt_pk_fp8_f32 v9, v18, v22
	v_cvt_pk_fp8_f32 v9, v26, v30 op_sel:[0,0,1]
	v_cvt_pk_fp8_f32 v13, v19, v23
	v_cvt_pk_fp8_f32 v13, v27, v31 op_sel:[0,0,1]
	v_cvt_pk_fp8_f32 v2, v32, v36
	v_cvt_pk_fp8_f32 v2, v40, v44 op_sel:[0,0,1]
	v_cvt_pk_fp8_f32 v6, v33, v37
	v_cvt_pk_fp8_f32 v6, v41, v45 op_sel:[0,0,1]
	v_cvt_pk_fp8_f32 v10, v34, v38
	v_cvt_pk_fp8_f32 v10, v42, v46 op_sel:[0,0,1]
	v_cvt_pk_fp8_f32 v14, v35, v39
	v_cvt_pk_fp8_f32 v14, v43, v47 op_sel:[0,0,1]
	v_cvt_pk_fp8_f32 v3, v48, v52
	v_cvt_pk_fp8_f32 v3, v56, v60 op_sel:[0,0,1]
	v_cvt_pk_fp8_f32 v7, v49, v53
	v_cvt_pk_fp8_f32 v7, v57, v61 op_sel:[0,0,1]
	v_cvt_pk_fp8_f32 v11, v50, v54
	v_cvt_pk_fp8_f32 v11, v58, v62 op_sel:[0,0,1]
	v_cvt_pk_fp8_f32 v15, v51, v55
	v_cvt_pk_fp8_f32 v15, v59, v63 op_sel:[0,0,1]
	global_store_dwordx4 v250, v[0:3], s[42:43] nt
	global_store_dwordx4 v250, v[4:7], s[42:43] offset:2048 nt
	global_store_dwordx4 v251, v[8:11], s[42:43] nt
	global_store_dwordx4 v251, v[12:15], s[42:43] offset:2048 nt
	s_add_u32 s42, s42, 0x200
	s_addc_u32 s43, s43, 0
	global_load_dwordx4 v[0:3], v246, s[4:5] nt
	global_load_dwordx4 v[4:7], v247, s[4:5] nt
	global_load_dwordx4 v[8:11], v248, s[4:5] nt
	global_load_dwordx4 v[12:15], v249, s[4:5] nt
	global_load_dwordx4 v[16:19], v246, s[6:7] nt
	global_load_dwordx4 v[20:23], v247, s[6:7] nt
	global_load_dwordx4 v[24:27], v248, s[6:7] nt
	global_load_dwordx4 v[28:31], v249, s[6:7] nt
	global_load_dwordx4 v[32:35], v246, s[8:9] nt
	global_load_dwordx4 v[36:39], v247, s[8:9] nt
	global_load_dwordx4 v[40:43], v248, s[8:9] nt
	global_load_dwordx4 v[44:47], v249, s[8:9] nt
	global_load_dwordx4 v[48:51], v246, s[38:39] nt
	global_load_dwordx4 v[52:55], v247, s[38:39] nt
	global_load_dwordx4 v[56:59], v248, s[38:39] nt
	global_load_dwordx4 v[60:63], v249, s[38:39] nt
	s_add_u32 s4, s4, 0x400000
	s_addc_u32 s5, s5, 0
	s_add_u32 s6, s6, 0x400000
	s_addc_u32 s7, s7, 0
	s_add_u32 s8, s8, 0x400000
	s_addc_u32 s9, s9, 0
	s_add_u32 s38, s38, 0x400000
	s_addc_u32 s39, s39, 0
	s_waitcnt vmcnt(40)
; #define GAS __attribute__((address_space(1)))
; template <bool GAIN, bool NT = false> __device__ __forceinline__ void titem8_load(const TItem& d, int lane, f32x4 (&r)[16], f32x4 (&g)[4]) {
;     const int q = lane & 7, kg = lane >> 3; const unsigned lo = (unsigned)((16 * kg) * d.N + 4 * q) * 4u;
;     const GAS char* base = (const GAS char*)d.src;
; #pragma unroll
;     for (int j = 0; j < 16; ++j) { const GAS f32x4* p = (const GAS f32x4*)(base + (size_t)j * (size_t)d.N * 4 + lo); r[j] = NT ? __builtin_nontemporal_load(p) : *p; }
;     if constexpr (GAIN) { const GAS char* gb = (const GAS char*)d.gain; const unsigned go = (unsigned)(16 * kg) * 4u;
; #pragma unroll
;         for (int j4 = 0; j4 < 4; ++j4) g[j4] = *(const GAS f32x4*)(gb + 16 * j4 + go); }
;     asm volatile("" ::: "memory"); __builtin_amdgcn_sched_barrier(0);
; }
; template <bool GAIN, bool NT = false> __device__ __forceinline__ void titem8_store(const TItem& d, int lane, const f32x4 (&r)[16], const f32x4 (&g)[4]) {
;     const int q = lane & 7, kg = lane >> 3; const unsigned lo = (unsigned)((4 * q) * d.ldk + 16 * kg);
;     GAS char* base = (GAS char*)d.dst;
;     f32x4 s[16];
; #pragma unroll
;     for (int j = 0; j < 16; ++j) s[j] = r[j] * ((GAIN ? g[j >> 2][j & 3] : 1.0f) * W8_SCALE);
; #pragma unroll
;     for (int i = 0; i < 4; ++i) { v4u w;
;         w.x = pk4_fp8w(s[0][i], s[1][i], s[2][i], s[3][i]); w.y = pk4_fp8w(s[4][i], s[5][i], s[6][i], s[7][i]);
;         w.z = pk4_fp8w(s[8][i], s[9][i], s[10][i], s[11][i]); w.w = pk4_fp8w(s[12][i], s[13][i], s[14][i], s[15][i]);
;         GAS v4u* p = (GAS v4u*)(base + (size_t)i * (size_t)d.ldk + lo);
;         if (NT) __builtin_nontemporal_store(w, p); else *p = w; }
; }
	v_pk_mul_f32 v[66:67], v[66:67], s[30:31] op_sel_hi:[1,0]
	v_pk_mul_f32 v[68:69], v[68:69], s[30:31] op_sel_hi:[1,0]
	v_pk_mul_f32 v[70:71], v[70:71], s[30:31] op_sel_hi:[1,0]
	v_pk_mul_f32 v[72:73], v[72:73], s[30:31] op_sel_hi:[1,0]
	v_pk_mul_f32 v[74:75], v[74:75], s[30:31] op_sel_hi:[1,0]
	v_pk_mul_f32 v[76:77], v[76:77], s[30:31] op_sel_hi:[1,0]
	v_pk_mul_f32 v[78:79], v[78:79], s[30:31] op_sel_hi:[1,0]
	v_pk_mul_f32 v[80:81], v[80:81], s[30:31] op_sel_hi:[1,0]
	v_pk_mul_f32 v[82:83], v[82:83], s[30:31] op_sel_hi:[1,0]
	v_pk_mul_f32 v[84:85], v[84:85], s[30:31] op_sel_hi:[1,0]
	v_pk_mul_f32 v[86:87], v[86:87], s[30:31] op_sel_hi:[1,0]
	v_pk_mul_f32 v[88:89], v[88:89], s[30:31] op_sel_hi:[1,0]
	v_pk_mul_f32 v[90:91], v[90:91], s[30:31] op_sel_hi:[1,0]
	v_pk_mul_f32 v[92:93], v[92:93], s[30:31] op_sel_hi:[1,0]
	v_pk_mul_f32 v[94:95], v[94:95], s[30:31] op_sel_hi:[1,0]
	v_pk_mul_f32 v[96:97], v[96:97], s[30:31] op_sel_hi:[1,0]
	v_pk_mul_f32 v[98:99], v[98:99], s[30:31] op_sel_hi:[1,0]
	v_pk_mul_f32 v[100:101], v[100:101], s[30:31] op_sel_hi:[1,0]
	v_pk_mul_f32 v[102:103], v[102:103], s[30:31] op_sel_hi:[1,0]
	v_pk_mul_f32 v[104:105], v[104:105], s[30:31] op_sel_hi:[1,0]
	v_pk_mul_f32 v[106:107], v[106:107], s[30:31] op_sel_hi:[1,0]
	v_pk_mul_f32 v[108:109], v[108:109], s[30:31] op_sel_hi:[1,0]
	v_pk_mul_f32 v[110:111], v[110:111], s[30:31] op_sel_hi:[1,0]
	v_pk_mul_f32 v[112:113], v[112:113], s[30:31] op_sel_hi:[1,0]
	v_pk_mul_f32 v[114:115], v[114:115], s[30:31] op_sel_hi:[1,0]
	v_pk_mul_f32 v[116:117], v[116:117], s[30:31] op_sel_hi:[1,0]
	v_pk_mul_f32 v[118:119], v[118:119], s[30:31] op_sel_hi:[1,0]
	v_pk_mul_f32 v[120:121], v[120:121], s[30:31] op_sel_hi:[1,0]
	v_pk_mul_f32 v[122:123], v[122:123], s[30:31] op_sel_hi:[1,0]
	v_pk_mul_f32 v[124:125], v[124:125], s[30:31] op_sel_hi:[1,0]
	v_pk_mul_f32 v[126:127], v[126:127], s[30:31] op_sel_hi:[1,0]
	v_pk_mul_f32 v[128:129], v[128:129], s[30:31] op_sel_hi:[1,0]
	v_med3_f32 v66, v66, s24, v237
	v_med3_f32 v67, v67, s24, v237
	v_med3_f32 v68, v68, s24, v237
	v_med3_f32 v69, v69, s24, v237
	v_med3_f32 v70, v70, s24, v237
	v_med3_f32 v71, v71, s24, v237
	v_med3_f32 v72, v72, s24, v237
	v_med3_f32 v73, v73, s24, v237
	v_med3_f32 v74, v74, s24, v237
	v_med3_f32 v75, v75, s24, v237
	v_med3_f32 v76, v76, s24, v237
	v_med3_f32 v77, v77, s24, v237
	v_med3_f32 v78, v78, s24, v237
	v_med3_f32 v79, v79, s24, v237
	v_med3_f32 v80, v80, s24, v237
	v_med3_f32 v81, v81, s24, v237
	v_med3_f32 v82, v82, s24, v237
	v_med3_f32 v83, v83, s24, v237
	v_med3_f32 v84, v84, s24, v237
	v_med3_f32 v85, v85, s24, v237
	v_med3_f32 v86, v86, s24, v237
	v_med3_f32 v87, v87, s24, v237
	v_med3_f32 v88, v88, s24, v237
	v_med3_f32 v89, v89, s24, v237
	v_med3_f32 v90, v90, s24, v237
	v_med3_f32 v91, v91, s24, v237
	v_med3_f32 v92, v92, s24, v237
	v_med3_f32 v93, v93, s24, v237
	v_med3_f32 v94, v94, s24, v237
	v_med3_f32 v95, v95, s24, v237
	v_med3_f32 v96, v96, s24, v237
	v_med3_f32 v97, v97, s24, v237
	v_med3_f32 v98, v98, s24, v237
	v_med3_f32 v99, v99, s24, v237
	v_med3_f32 v100, v100, s24, v237
	v_med3_f32 v101, v101, s24, v237
	v_med3_f32 v102, v102, s24, v237
	v_med3_f32 v103, v103, s24, v237
	v_med3_f32 v104, v104, s24, v237
	v_med3_f32 v105, v105, s24, v237
	v_med3_f32 v106, v106, s24, v237
	v_med3_f32 v107, v107, s24, v237
	v_med3_f32 v108, v108, s24, v237
	v_med3_f32 v109, v109, s24, v237
	v_med3_f32 v110, v110, s24, v237
	v_med3_f32 v111, v111, s24, v237
	v_med3_f32 v112, v112, s24, v237
	v_med3_f32 v113, v113, s24, v237
	v_med3_f32 v114, v114, s24, v237
	v_med3_f32 v115, v115, s24, v237
	v_med3_f32 v116, v116, s24, v237
	v_med3_f32 v117, v117, s24, v237
	v_med3_f32 v118, v118, s24, v237
	v_med3_f32 v119, v119, s24, v237
	v_med3_f32 v120, v120, s24, v237
	v_med3_f32 v121, v121, s24, v237
	v_med3_f32 v122, v122, s24, v237
	v_med3_f32 v123, v123, s24, v237
	v_med3_f32 v124, v124, s24, v237
	v_med3_f32 v125, v125, s24, v237
	v_med3_f32 v126, v126, s24, v237
	v_med3_f32 v127, v127, s24, v237
	v_med3_f32 v128, v128, s24, v237
	v_med3_f32 v129, v129, s24, v237
	v_cvt_pk_fp8_f32 v66, v66, v70
	v_cvt_pk_fp8_f32 v66, v74, v78 op_sel:[0,0,1]
	v_cvt_pk_fp8_f32 v70, v67, v71
	v_cvt_pk_fp8_f32 v70, v75, v79 op_sel:[0,0,1]
	v_cvt_pk_fp8_f32 v74, v68, v72
	v_cvt_pk_fp8_f32 v74, v76, v80 op_sel:[0,0,1]
	v_cvt_pk_fp8_f32 v78, v69, v73
	v_cvt_pk_fp8_f32 v78, v77, v81 op_sel:[0,0,1]
	v_cvt_pk_fp8_f32 v67, v82, v86
	v_cvt_pk_fp8_f32 v67, v90, v94 op_sel:[0,0,1]
	v_cvt_pk_fp8_f32 v71, v83, v87
	v_cvt_pk_fp8_f32 v71, v91, v95 op_sel:[0,0,1]
	v_cvt_pk_fp8_f32 v75, v84, v88
	v_cvt_pk_fp8_f32 v75, v92, v96 op_sel:[0,0,1]
	v_cvt_pk_fp8_f32 v79, v85, v89
	v_cvt_pk_fp8_f32 v79, v93, v97 op_sel:[0,0,1]
	v_cvt_pk_fp8_f32 v68, v98, v102
	v_cvt_pk_fp8_f32 v68, v106, v110 op_sel:[0,0,1]
	v_cvt_pk_fp8_f32 v72, v99, v103
	v_cvt_pk_fp8_f32 v72, v107, v111 op_sel:[0,0,1]
	v_cvt_pk_fp8_f32 v76, v100, v104
	v_cvt_pk_fp8_f32 v76, v108, v112 op_sel:[0,0,1]
	v_cvt_pk_fp8_f32 v80, v101, v105
	v_cvt_pk_fp8_f32 v80, v109, v113 op_sel:[0,0,1]
	v_cvt_pk_fp8_f32 v69, v114, v118
	v_cvt_pk_fp8_f32 v69, v122, v126 op_sel:[0,0,1]
	v_cvt_pk_fp8_f32 v73, v115, v119
	v_cvt_pk_fp8_f32 v73, v123, v127 op_sel:[0,0,1]
	v_cvt_pk_fp8_f32 v77, v116, v120
	v_cvt_pk_fp8_f32 v77, v124, v128 op_sel:[0,0,1]
	v_cvt_pk_fp8_f32 v81, v117, v121
	v_cvt_pk_fp8_f32 v81, v125, v129 op_sel:[0,0,1]
	global_store_dwordx4 v250, v[66:69], s[42:43] nt
	global_store_dwordx4 v250, v[70:73], s[42:43] offset:2048 nt
	global_store_dwordx4 v251, v[74:77], s[42:43] nt
	global_store_dwordx4 v251, v[78:81], s[42:43] offset:2048 nt
	s_add_u32 s42, s42, 0x200
	s_addc_u32 s43, s43, 0
	global_load_dwordx4 v[66:69], v246, s[4:5] nt
	global_load_dwordx4 v[70:73], v247, s[4:5] nt
	global_load_dwordx4 v[74:77], v248, s[4:5] nt
	global_load_dwordx4 v[78:81], v249, s[4:5] nt
	global_load_dwordx4 v[82:85], v246, s[6:7] nt
	global_load_dwordx4 v[86:89], v247, s[6:7] nt
	global_load_dwordx4 v[90:93], v248, s[6:7] nt
	global_load_dwordx4 v[94:97], v249, s[6:7] nt
	global_load_dwordx4 v[98:101], v246, s[8:9] nt
	global_load_dwordx4 v[102:105], v247, s[8:9] nt
	global_load_dwordx4 v[106:109], v248, s[8:9] nt
	global_load_dwordx4 v[110:113], v249, s[8:9] nt
	global_load_dwordx4 v[114:117], v246, s[38:39] nt
	global_load_dwordx4 v[118:121], v247, s[38:39] nt
	global_load_dwordx4 v[122:125], v248, s[38:39] nt
	global_load_dwordx4 v[126:129], v249, s[38:39] nt
	s_add_u32 s4, s4, 0x400000
	s_addc_u32 s5, s5, 0
	s_add_u32 s6, s6, 0x400000
	s_addc_u32 s7, s7, 0
	s_add_u32 s8, s8, 0x400000
	s_addc_u32 s9, s9, 0
	s_add_u32 s38, s38, 0x400000
	s_addc_u32 s39, s39, 0
	s_waitcnt vmcnt(40)
; #define GAS __attribute__((address_space(1)))
; template <bool GAIN, bool NT = false> __device__ __forceinline__ void titem8_load(const TItem& d, int lane, f32x4 (&r)[16], f32x4 (&g)[4]) {
;     const int q = lane & 7, kg = lane >> 3; const unsigned lo = (unsigned)((16 * kg) * d.N + 4 * q) * 4u;
;     const GAS char* base = (const GAS char*)d.src;
; #pragma unroll
;     for (int j = 0; j < 16; ++j) { const GAS f32x4* p = (const GAS f32x4*)(base + (size_t)j * (size_t)d.N * 4 + lo); r[j] = NT ? __builtin_nontemporal_load(p) : *p; }
;     if constexpr (GAIN) { const GAS char* gb = (const GAS char*)d.gain; const unsigned go = (unsigned)(16 * kg) * 4u;
; #pragma unroll
;         for (int j4 = 0; j4 < 4; ++j4) g[j4] = *(const GAS f32x4*)(gb + 16 * j4 + go); }
;     asm volatile("" ::: "memory"); __builtin_amdgcn_sched_barrier(0);
; }
; template <bool GAIN, bool NT = false> __device__ __forceinline__ void titem8_store(const TItem& d, int lane, const f32x4 (&r)[16], const f32x4 (&g)[4]) {
;     const int q = lane & 7, kg = lane >> 3; const unsigned lo = (unsigned)((4 * q) * d.ldk + 16 * kg);
;     GAS char* base = (GAS char*)d.dst;
;     f32x4 s[16];
; #pragma unroll
;     for (int j = 0; j < 16; ++j) s[j] = r[j] * ((GAIN ? g[j >> 2][j & 3] : 1.0f) * W8_SCALE);
; #pragma unroll
;     for (int i = 0; i < 4; ++i) { v4u w;
;         w.x = pk4_fp8w(s[0][i], s[1][i], s[2][i], s[3][i]); w.y = pk4_fp8w(s[4][i], s[5][i], s[6][i], s[7][i]);
;         w.z = pk4_fp8w(s[8][i], s[9][i], s[10][i], s[11][i]); w.w = pk4_fp8w(s[12][i], s[13][i], s[14][i], s[15][i]);
;         GAS v4u* p = (GAS v4u*)(base + (size_t)i * (size_t)d.ldk + lo);
;         if (NT) __builtin_nontemporal_store(w, p); else *p = w; }
; }
	v_pk_mul_f32 v[130:131], v[130:131], s[30:31] op_sel_hi:[1,0]
	v_pk_mul_f32 v[132:133], v[132:133], s[30:31] op_sel_hi:[1,0]
	v_pk_mul_f32 v[134:135], v[134:135], s[30:31] op_sel_hi:[1,0]
	v_pk_mul_f32 v[136:137], v[136:137], s[30:31] op_sel_hi:[1,0]
	v_pk_mul_f32 v[138:139], v[138:139], s[30:31] op_sel_hi:[1,0]
	v_pk_mul_f32 v[140:141], v[140:141], s[30:31] op_sel_hi:[1,0]
	v_pk_mul_f32 v[142:143], v[142:143], s[30:31] op_sel_hi:[1,0]
	v_pk_mul_f32 v[144:145], v[144:145], s[30:31] op_sel_hi:[1,0]
	v_pk_mul_f32 v[146:147], v[146:147], s[30:31] op_sel_hi:[1,0]
	v_pk_mul_f32 v[148:149], v[148:149], s[30:31] op_sel_hi:[1,0]
	v_pk_mul_f32 v[150:151], v[150:151], s[30:31] op_sel_hi:[1,0]
	v_pk_mul_f32 v[152:153], v[152:153], s[30:31] op_sel_hi:[1,0]
	v_pk_mul_f32 v[154:155], v[154:155], s[30:31] op_sel_hi:[1,0]
	v_pk_mul_f32 v[156:157], v[156:157], s[30:31] op_sel_hi:[1,0]
	v_pk_mul_f32 v[158:159], v[158:159], s[30:31] op_sel_hi:[1,0]
	v_pk_mul_f32 v[160:161], v[160:161], s[30:31] op_sel_hi:[1,0]
	v_pk_mul_f32 v[162:163], v[162:163], s[30:31] op_sel_hi:[1,0]
	v_pk_mul_f32 v[164:165], v[164:165], s[30:31] op_sel_hi:[1,0]
	v_pk_mul_f32 v[166:167], v[166:167], s[30:31] op_sel_hi:[1,0]
	v_pk_mul_f32 v[168:169], v[168:169], s[30:31] op_sel_hi:[1,0]
	v_pk_mul_f32 v[170:171], v[170:171], s[30:31] op_sel_hi:[1,0]
	v_pk_mul_f32 v[172:173], v[172:173], s[30:31] op_sel_hi:[1,0]
	v_pk_mul_f32 v[174:175], v[174:175], s[30:31] op_sel_hi:[1,0]
	v_pk_mul_f32 v[176:177], v[176:177], s[30:31] op_sel_hi:[1,0]
	v_pk_mul_f32 v[178:179], v[178:179], s[30:31] op_sel_hi:[1,0]
	v_pk_mul_f32 v[180:181], v[180:181], s[30:31] op_sel_hi:[1,0]
	v_pk_mul_f32 v[182:183], v[182:183], s[30:31] op_sel_hi:[1,0]
	v_pk_mul_f32 v[184:185], v[184:185], s[30:31] op_sel_hi:[1,0]
	v_pk_mul_f32 v[186:187], v[186:187], s[30:31] op_sel_hi:[1,0]
	v_pk_mul_f32 v[188:189], v[188:189], s[30:31] op_sel_hi:[1,0]
	v_pk_mul_f32 v[190:191], v[190:191], s[30:31] op_sel_hi:[1,0]
	v_pk_mul_f32 v[192:193], v[192:193], s[30:31] op_sel_hi:[1,0]
	v_med3_f32 v130, v130, s24, v237
	v_med3_f32 v131, v131, s24, v237
	v_med3_f32 v132, v132, s24, v237
	v_med3_f32 v133, v133, s24, v237
	v_med3_f32 v134, v134, s24, v237
	v_med3_f32 v135, v135, s24, v237
	v_med3_f32 v136, v136, s24, v237
	v_med3_f32 v137, v137, s24, v237
	v_med3_f32 v138, v138, s24, v237
	v_med3_f32 v139, v139, s24, v237
	v_med3_f32 v140, v140, s24, v237
	v_med3_f32 v141, v141, s24, v237
	v_med3_f32 v142, v142, s24, v237
	v_med3_f32 v143, v143, s24, v237
	v_med3_f32 v144, v144, s24, v237
	v_med3_f32 v145, v145, s24, v237
	v_med3_f32 v146, v146, s24, v237
	v_med3_f32 v147, v147, s24, v237
	v_med3_f32 v148, v148, s24, v237
	v_med3_f32 v149, v149, s24, v237
	v_med3_f32 v150, v150, s24, v237
	v_med3_f32 v151, v151, s24, v237
	v_med3_f32 v152, v152, s24, v237
	v_med3_f32 v153, v153, s24, v237
	v_med3_f32 v154, v154, s24, v237
	v_med3_f32 v155, v155, s24, v237
	v_med3_f32 v156, v156, s24, v237
	v_med3_f32 v157, v157, s24, v237
	v_med3_f32 v158, v158, s24, v237
	v_med3_f32 v159, v159, s24, v237
	v_med3_f32 v160, v160, s24, v237
	v_med3_f32 v161, v161, s24, v237
	v_med3_f32 v162, v162, s24, v237
	v_med3_f32 v163, v163, s24, v237
	v_med3_f32 v164, v164, s24, v237
	v_med3_f32 v165, v165, s24, v237
	v_med3_f32 v166, v166, s24, v237
	v_med3_f32 v167, v167, s24, v237
	v_med3_f32 v168, v168, s24, v237
	v_med3_f32 v169, v169, s24, v237
	v_med3_f32 v170, v170, s24, v237
	v_med3_f32 v171, v171, s24, v237
	v_med3_f32 v172, v172, s24, v237
	v_med3_f32 v173, v173, s24, v237
	v_med3_f32 v174, v174, s24, v237
	v_med3_f32 v175, v175, s24, v237
	v_med3_f32 v176, v176, s24, v237
	v_med3_f32 v177, v177, s24, v237
	v_med3_f32 v178, v178, s24, v237
	v_med3_f32 v179, v179, s24, v237
	v_med3_f32 v180, v180, s24, v237
	v_med3_f32 v181, v181, s24, v237
	v_med3_f32 v182, v182, s24, v237
	v_med3_f32 v183, v183, s24, v237
	v_med3_f32 v184, v184, s24, v237
	v_med3_f32 v185, v185, s24, v237
	v_med3_f32 v186, v186, s24, v237
	v_med3_f32 v187, v187, s24, v237
	v_med3_f32 v188, v188, s24, v237
	v_med3_f32 v189, v189, s24, v237
	v_med3_f32 v190, v190, s24, v237
	v_med3_f32 v191, v191, s24, v237
	v_med3_f32 v192, v192, s24, v237
	v_med3_f32 v193, v193, s24, v237
	v_cvt_pk_fp8_f32 v130, v130, v134
	v_cvt_pk_fp8_f32 v130, v138, v142 op_sel:[0,0,1]
	v_cvt_pk_fp8_f32 v134, v131, v135
	v_cvt_pk_fp8_f32 v134, v139, v143 op_sel:[0,0,1]
	v_cvt_pk_fp8_f32 v138, v132, v136
	v_cvt_pk_fp8_f32 v138, v140, v144 op_sel:[0,0,1]
	v_cvt_pk_fp8_f32 v142, v133, v137
	v_cvt_pk_fp8_f32 v142, v141, v145 op_sel:[0,0,1]
	v_cvt_pk_fp8_f32 v131, v146, v150
	v_cvt_pk_fp8_f32 v131, v154, v158 op_sel:[0,0,1]
	v_cvt_pk_fp8_f32 v135, v147, v151
	v_cvt_pk_fp8_f32 v135, v155, v159 op_sel:[0,0,1]
	v_cvt_pk_fp8_f32 v139, v148, v152
	v_cvt_pk_fp8_f32 v139, v156, v160 op_sel:[0,0,1]
	v_cvt_pk_fp8_f32 v143, v149, v153
	v_cvt_pk_fp8_f32 v143, v157, v161 op_sel:[0,0,1]
	v_cvt_pk_fp8_f32 v132, v162, v166
	v_cvt_pk_fp8_f32 v132, v170, v174 op_sel:[0,0,1]
	v_cvt_pk_fp8_f32 v136, v163, v167
	v_cvt_pk_fp8_f32 v136, v171, v175 op_sel:[0,0,1]
	v_cvt_pk_fp8_f32 v140, v164, v168
	v_cvt_pk_fp8_f32 v140, v172, v176 op_sel:[0,0,1]
	v_cvt_pk_fp8_f32 v144, v165, v169
	v_cvt_pk_fp8_f32 v144, v173, v177 op_sel:[0,0,1]
	v_cvt_pk_fp8_f32 v133, v178, v182
	v_cvt_pk_fp8_f32 v133, v186, v190 op_sel:[0,0,1]
	v_cvt_pk_fp8_f32 v137, v179, v183
	v_cvt_pk_fp8_f32 v137, v187, v191 op_sel:[0,0,1]
	v_cvt_pk_fp8_f32 v141, v180, v184
	v_cvt_pk_fp8_f32 v141, v188, v192 op_sel:[0,0,1]
	v_cvt_pk_fp8_f32 v145, v181, v185
	v_cvt_pk_fp8_f32 v145, v189, v193 op_sel:[0,0,1]
	global_store_dwordx4 v250, v[130:133], s[42:43] nt
	global_store_dwordx4 v250, v[134:137], s[42:43] offset:2048 nt
	global_store_dwordx4 v251, v[138:141], s[42:43] nt
	global_store_dwordx4 v251, v[142:145], s[42:43] offset:2048 nt
	s_add_u32 s42, s42, 0x3ffa00
	s_addc_u32 s43, s43, 0
	global_load_dwordx4 v[130:133], v246, s[4:5] nt
	global_load_dwordx4 v[134:137], v247, s[4:5] nt
	global_load_dwordx4 v[138:141], v248, s[4:5] nt
	global_load_dwordx4 v[142:145], v249, s[4:5] nt
	global_load_dwordx4 v[146:149], v246, s[6:7] nt
	global_load_dwordx4 v[150:153], v247, s[6:7] nt
	global_load_dwordx4 v[154:157], v248, s[6:7] nt
	global_load_dwordx4 v[158:161], v249, s[6:7] nt
	global_load_dwordx4 v[162:165], v246, s[8:9] nt
	global_load_dwordx4 v[166:169], v247, s[8:9] nt
	global_load_dwordx4 v[170:173], v248, s[8:9] nt
	global_load_dwordx4 v[174:177], v249, s[8:9] nt
	global_load_dwordx4 v[178:181], v246, s[38:39] nt
	global_load_dwordx4 v[182:185], v247, s[38:39] nt
	global_load_dwordx4 v[186:189], v248, s[38:39] nt
	global_load_dwordx4 v[190:193], v249, s[38:39] nt
	s_add_u32 s4, s4, 0x400000
	s_addc_u32 s5, s5, 0
	s_add_u32 s6, s6, 0x400000
	s_addc_u32 s7, s7, 0
	s_add_u32 s8, s8, 0x400000
	s_addc_u32 s9, s9, 0
	s_add_u32 s38, s38, 0x400000
	s_addc_u32 s39, s39, 0
	s_waitcnt vmcnt(40)
; #define GAS __attribute__((address_space(1)))
; template <bool GAIN, bool NT = false> __device__ __forceinline__ void titem8_load(const TItem& d, int lane, f32x4 (&r)[16], f32x4 (&g)[4]) {
;     const int q = lane & 7, kg = lane >> 3; const unsigned lo = (unsigned)((16 * kg) * d.N + 4 * q) * 4u;
;     const GAS char* base = (const GAS char*)d.src;
; #pragma unroll
;     for (int j = 0; j < 16; ++j) { const GAS f32x4* p = (const GAS f32x4*)(base + (size_t)j * (size_t)d.N * 4 + lo); r[j] = NT ? __builtin_nontemporal_load(p) : *p; }
;     if constexpr (GAIN) { const GAS char* gb = (const GAS char*)d.gain; const unsigned go = (unsigned)(16 * kg) * 4u;
; #pragma unroll
;         for (int j4 = 0; j4 < 4; ++j4) g[j4] = *(const GAS f32x4*)(gb + 16 * j4 + go); }
;     asm volatile("" ::: "memory"); __builtin_amdgcn_sched_barrier(0);
; }
; template <bool GAIN, bool NT = false> __device__ __forceinline__ void titem8_store(const TItem& d, int lane, const f32x4 (&r)[16], const f32x4 (&g)[4]) {
;     const int q = lane & 7, kg = lane >> 3; const unsigned lo = (unsigned)((4 * q) * d.ldk + 16 * kg);
;     GAS char* base = (GAS char*)d.dst;
;     f32x4 s[16];
; #pragma unroll
;     for (int j = 0; j < 16; ++j) s[j] = r[j] * ((GAIN ? g[j >> 2][j & 3] : 1.0f) * W8_SCALE);
; #pragma unroll
;     for (int i = 0; i < 4; ++i) { v4u w;
;         w.x = pk4_fp8w(s[0][i], s[1][i], s[2][i], s[3][i]); w.y = pk4_fp8w(s[4][i], s[5][i], s[6][i], s[7][i]);
;         w.z = pk4_fp8w(s[8][i], s[9][i], s[10][i], s[11][i]); w.w = pk4_fp8w(s[12][i], s[13][i], s[14][i], s[15][i]);
;         GAS v4u* p = (GAS v4u*)(base + (size_t)i * (size_t)d.ldk + lo);
;         if (NT) __builtin_nontemporal_store(w, p); else *p = w; }
; }
	v_pk_mul_f32 v[0:1], v[0:1], s[30:31] op_sel_hi:[1,0]
	v_pk_mul_f32 v[2:3], v[2:3], s[30:31] op_sel_hi:[1,0]
	v_pk_mul_f32 v[4:5], v[4:5], s[30:31] op_sel_hi:[1,0]
	v_pk_mul_f32 v[6:7], v[6:7], s[30:31] op_sel_hi:[1,0]
	v_pk_mul_f32 v[8:9], v[8:9], s[30:31] op_sel_hi:[1,0]
	v_pk_mul_f32 v[10:11], v[10:11], s[30:31] op_sel_hi:[1,0]
	v_pk_mul_f32 v[12:13], v[12:13], s[30:31] op_sel_hi:[1,0]
	v_pk_mul_f32 v[14:15], v[14:15], s[30:31] op_sel_hi:[1,0]
	v_pk_mul_f32 v[16:17], v[16:17], s[30:31] op_sel_hi:[1,0]
	v_pk_mul_f32 v[18:19], v[18:19], s[30:31] op_sel_hi:[1,0]
	v_pk_mul_f32 v[20:21], v[20:21], s[30:31] op_sel_hi:[1,0]
	v_pk_mul_f32 v[22:23], v[22:23], s[30:31] op_sel_hi:[1,0]
	v_pk_mul_f32 v[24:25], v[24:25], s[30:31] op_sel_hi:[1,0]
	v_pk_mul_f32 v[26:27], v[26:27], s[30:31] op_sel_hi:[1,0]
	v_pk_mul_f32 v[28:29], v[28:29], s[30:31] op_sel_hi:[1,0]
	v_pk_mul_f32 v[30:31], v[30:31], s[30:31] op_sel_hi:[1,0]
	v_pk_mul_f32 v[32:33], v[32:33], s[30:31] op_sel_hi:[1,0]
	v_pk_mul_f32 v[34:35], v[34:35], s[30:31] op_sel_hi:[1,0]
	v_pk_mul_f32 v[36:37], v[36:37], s[30:31] op_sel_hi:[1,0]
	v_pk_mul_f32 v[38:39], v[38:39], s[30:31] op_sel_hi:[1,0]
	v_pk_mul_f32 v[40:41], v[40:41], s[30:31] op_sel_hi:[1,0]
	v_pk_mul_f32 v[42:43], v[42:43], s[30:31] op_sel_hi:[1,0]
	v_pk_mul_f32 v[44:45], v[44:45], s[30:31] op_sel_hi:[1,0]
	v_pk_mul_f32 v[46:47], v[46:47], s[30:31] op_sel_hi:[1,0]
	v_pk_mul_f32 v[48:49], v[48:49], s[30:31] op_sel_hi:[1,0]
	v_pk_mul_f32 v[50:51], v[50:51], s[30:31] op_sel_hi:[1,0]
	v_pk_mul_f32 v[52:53], v[52:53], s[30:31] op_sel_hi:[1,0]
	v_pk_mul_f32 v[54:55], v[54:55], s[30:31] op_sel_hi:[1,0]
	v_pk_mul_f32 v[56:57], v[56:57], s[30:31] op_sel_hi:[1,0]
	v_pk_mul_f32 v[58:59], v[58:59], s[30:31] op_sel_hi:[1,0]
	v_pk_mul_f32 v[60:61], v[60:61], s[30:31] op_sel_hi:[1,0]
	v_pk_mul_f32 v[62:63], v[62:63], s[30:31] op_sel_hi:[1,0]
	v_med3_f32 v0, v0, s24, v237
	v_med3_f32 v1, v1, s24, v237
	v_med3_f32 v2, v2, s24, v237
	v_med3_f32 v3, v3, s24, v237
	v_med3_f32 v4, v4, s24, v237
	v_med3_f32 v5, v5, s24, v237
	v_med3_f32 v6, v6, s24, v237
	v_med3_f32 v7, v7, s24, v237
	v_med3_f32 v8, v8, s24, v237
	v_med3_f32 v9, v9, s24, v237
	v_med3_f32 v10, v10, s24, v237
	v_med3_f32 v11, v11, s24, v237
	v_med3_f32 v12, v12, s24, v237
	v_med3_f32 v13, v13, s24, v237
	v_med3_f32 v14, v14, s24, v237
	v_med3_f32 v15, v15, s24, v237
	v_med3_f32 v16, v16, s24, v237
	v_med3_f32 v17, v17, s24, v237
	v_med3_f32 v18, v18, s24, v237
	v_med3_f32 v19, v19, s24, v237
	v_med3_f32 v20, v20, s24, v237
	v_med3_f32 v21, v21, s24, v237
	v_med3_f32 v22, v22, s24, v237
	v_med3_f32 v23, v23, s24, v237
	v_med3_f32 v24, v24, s24, v237
	v_med3_f32 v25, v25, s24, v237
	v_med3_f32 v26, v26, s24, v237
	v_med3_f32 v27, v27, s24, v237
	v_med3_f32 v28, v28, s24, v237
	v_med3_f32 v29, v29, s24, v237
	v_med3_f32 v30, v30, s24, v237
	v_med3_f32 v31, v31, s24, v237
	v_med3_f32 v32, v32, s24, v237
	v_med3_f32 v33, v33, s24, v237
	v_med3_f32 v34, v34, s24, v237
	v_med3_f32 v35, v35, s24, v237
	v_med3_f32 v36, v36, s24, v237
	v_med3_f32 v37, v37, s24, v237
	v_med3_f32 v38, v38, s24, v237
	v_med3_f32 v39, v39, s24, v237
	v_med3_f32 v40, v40, s24, v237
	v_med3_f32 v41, v41, s24, v237
	v_med3_f32 v42, v42, s24, v237
	v_med3_f32 v43, v43, s24, v237
	v_med3_f32 v44, v44, s24, v237
	v_med3_f32 v45, v45, s24, v237
	v_med3_f32 v46, v46, s24, v237
	v_med3_f32 v47, v47, s24, v237
	v_med3_f32 v48, v48, s24, v237
	v_med3_f32 v49, v49, s24, v237
	v_med3_f32 v50, v50, s24, v237
	v_med3_f32 v51, v51, s24, v237
	v_med3_f32 v52, v52, s24, v237
	v_med3_f32 v53, v53, s24, v237
	v_med3_f32 v54, v54, s24, v237
	v_med3_f32 v55, v55, s24, v237
	v_med3_f32 v56, v56, s24, v237
	v_med3_f32 v57, v57, s24, v237
	v_med3_f32 v58, v58, s24, v237
	v_med3_f32 v59, v59, s24, v237
	v_med3_f32 v60, v60, s24, v237
	v_med3_f32 v61, v61, s24, v237
	v_med3_f32 v62, v62, s24, v237
	v_med3_f32 v63, v63, s24, v237
	v_cvt_pk_fp8_f32 v0, v0, v4
	v_cvt_pk_fp8_f32 v0, v8, v12 op_sel:[0,0,1]
	v_cvt_pk_fp8_f32 v4, v1, v5
	v_cvt_pk_fp8_f32 v4, v9, v13 op_sel:[0,0,1]
	v_cvt_pk_fp8_f32 v8, v2, v6
	v_cvt_pk_fp8_f32 v8, v10, v14 op_sel:[0,0,1]
	v_cvt_pk_fp8_f32 v12, v3, v7
	v_cvt_pk_fp8_f32 v12, v11, v15 op_sel:[0,0,1]
	v_cvt_pk_fp8_f32 v1, v16, v20
	v_cvt_pk_fp8_f32 v1, v24, v28 op_sel:[0,0,1]
	v_cvt_pk_fp8_f32 v5, v17, v21
	v_cvt_pk_fp8_f32 v5, v25, v29 op_sel:[0,0,1]
	v_cvt_pk_fp8_f32 v9, v18, v22
	v_cvt_pk_fp8_f32 v9, v26, v30 op_sel:[0,0,1]
	v_cvt_pk_fp8_f32 v13, v19, v23
	v_cvt_pk_fp8_f32 v13, v27, v31 op_sel:[0,0,1]
	v_cvt_pk_fp8_f32 v2, v32, v36
	v_cvt_pk_fp8_f32 v2, v40, v44 op_sel:[0,0,1]
	v_cvt_pk_fp8_f32 v6, v33, v37
	v_cvt_pk_fp8_f32 v6, v41, v45 op_sel:[0,0,1]
	v_cvt_pk_fp8_f32 v10, v34, v38
	v_cvt_pk_fp8_f32 v10, v42, v46 op_sel:[0,0,1]
	v_cvt_pk_fp8_f32 v14, v35, v39
	v_cvt_pk_fp8_f32 v14, v43, v47 op_sel:[0,0,1]
	v_cvt_pk_fp8_f32 v3, v48, v52
	v_cvt_pk_fp8_f32 v3, v56, v60 op_sel:[0,0,1]
	v_cvt_pk_fp8_f32 v7, v49, v53
	v_cvt_pk_fp8_f32 v7, v57, v61 op_sel:[0,0,1]
	v_cvt_pk_fp8_f32 v11, v50, v54
	v_cvt_pk_fp8_f32 v11, v58, v62 op_sel:[0,0,1]
	v_cvt_pk_fp8_f32 v15, v51, v55
	v_cvt_pk_fp8_f32 v15, v59, v63 op_sel:[0,0,1]
	global_store_dwordx4 v250, v[0:3], s[42:43] nt
	global_store_dwordx4 v250, v[4:7], s[42:43] offset:2048 nt
	global_store_dwordx4 v251, v[8:11], s[42:43] nt
	global_store_dwordx4 v251, v[12:15], s[42:43] offset:2048 nt
	s_add_u32 s42, s42, 0x200
	s_addc_u32 s43, s43, 0
	global_load_dwordx4 v[0:3], v246, s[4:5] nt
	global_load_dwordx4 v[4:7], v247, s[4:5] nt
	global_load_dwordx4 v[8:11], v248, s[4:5] nt
	global_load_dwordx4 v[12:15], v249, s[4:5] nt
	global_load_dwordx4 v[16:19], v246, s[6:7] nt
	global_load_dwordx4 v[20:23], v247, s[6:7] nt
	global_load_dwordx4 v[24:27], v248, s[6:7] nt
	global_load_dwordx4 v[28:31], v249, s[6:7] nt
	global_load_dwordx4 v[32:35], v246, s[8:9] nt
	global_load_dwordx4 v[36:39], v247, s[8:9] nt
	global_load_dwordx4 v[40:43], v248, s[8:9] nt
	global_load_dwordx4 v[44:47], v249, s[8:9] nt
	global_load_dwordx4 v[48:51], v246, s[38:39] nt
	global_load_dwordx4 v[52:55], v247, s[38:39] nt
	global_load_dwordx4 v[56:59], v248, s[38:39] nt
	global_load_dwordx4 v[60:63], v249, s[38:39] nt
	s_add_u32 s4, s4, 0x400000
	s_addc_u32 s5, s5, 0
	s_add_u32 s6, s6, 0x400000
	s_addc_u32 s7, s7, 0
	s_add_u32 s8, s8, 0x400000
	s_addc_u32 s9, s9, 0
	s_add_u32 s38, s38, 0x400000
	s_addc_u32 s39, s39, 0
	s_waitcnt vmcnt(40)
; #define GAS __attribute__((address_space(1)))
; template <bool GAIN, bool NT = false> __device__ __forceinline__ void titem8_store(const TItem& d, int lane, const f32x4 (&r)[16], const f32x4 (&g)[4]) {
;     const int q = lane & 7, kg = lane >> 3; const unsigned lo = (unsigned)((4 * q) * d.ldk + 16 * kg);
;     GAS char* base = (GAS char*)d.dst;
;     f32x4 s[16];
; #pragma unroll
;     for (int j = 0; j < 16; ++j) s[j] = r[j] * ((GAIN ? g[j >> 2][j & 3] : 1.0f) * W8_SCALE);
; #pragma unroll
;     for (int i = 0; i < 4; ++i) { v4u w;
;         w.x = pk4_fp8w(s[0][i], s[1][i], s[2][i], s[3][i]); w.y = pk4_fp8w(s[4][i], s[5][i], s[6][i], s[7][i]);
;         w.z = pk4_fp8w(s[8][i], s[9][i], s[10][i], s[11][i]); w.w = pk4_fp8w(s[12][i], s[13][i], s[14][i], s[15][i]);
;         GAS v4u* p = (GAS v4u*)(base + (size_t)i * (size_t)d.ldk + lo);
;         if (NT) __builtin_nontemporal_store(w, p); else *p = w; }
; }
	v_pk_mul_f32 v[66:67], v[66:67], s[30:31] op_sel_hi:[1,0]
	v_pk_mul_f32 v[68:69], v[68:69], s[30:31] op_sel_hi:[1,0]
	v_pk_mul_f32 v[70:71], v[70:71], s[30:31] op_sel_hi:[1,0]
	v_pk_mul_f32 v[72:73], v[72:73], s[30:31] op_sel_hi:[1,0]
	v_pk_mul_f32 v[74:75], v[74:75], s[30:31] op_sel_hi:[1,0]
	v_pk_mul_f32 v[76:77], v[76:77], s[30:31] op_sel_hi:[1,0]
	v_pk_mul_f32 v[78:79], v[78:79], s[30:31] op_sel_hi:[1,0]
	v_pk_mul_f32 v[80:81], v[80:81], s[30:31] op_sel_hi:[1,0]
	v_pk_mul_f32 v[82:83], v[82:83], s[30:31] op_sel_hi:[1,0]
	v_pk_mul_f32 v[84:85], v[84:85], s[30:31] op_sel_hi:[1,0]
	v_pk_mul_f32 v[86:87], v[86:87], s[30:31] op_sel_hi:[1,0]
	v_pk_mul_f32 v[88:89], v[88:89], s[30:31] op_sel_hi:[1,0]
	v_pk_mul_f32 v[90:91], v[90:91], s[30:31] op_sel_hi:[1,0]
	v_pk_mul_f32 v[92:93], v[92:93], s[30:31] op_sel_hi:[1,0]
	v_pk_mul_f32 v[94:95], v[94:95], s[30:31] op_sel_hi:[1,0]
	v_pk_mul_f32 v[96:97], v[96:97], s[30:31] op_sel_hi:[1,0]
	v_pk_mul_f32 v[98:99], v[98:99], s[30:31] op_sel_hi:[1,0]
	v_pk_mul_f32 v[100:101], v[100:101], s[30:31] op_sel_hi:[1,0]
	v_pk_mul_f32 v[102:103], v[102:103], s[30:31] op_sel_hi:[1,0]
	v_pk_mul_f32 v[104:105], v[104:105], s[30:31] op_sel_hi:[1,0]
	v_pk_mul_f32 v[106:107], v[106:107], s[30:31] op_sel_hi:[1,0]
	v_pk_mul_f32 v[108:109], v[108:109], s[30:31] op_sel_hi:[1,0]
	v_pk_mul_f32 v[110:111], v[110:111], s[30:31] op_sel_hi:[1,0]
	v_pk_mul_f32 v[112:113], v[112:113], s[30:31] op_sel_hi:[1,0]
	v_pk_mul_f32 v[114:115], v[114:115], s[30:31] op_sel_hi:[1,0]
	v_pk_mul_f32 v[116:117], v[116:117], s[30:31] op_sel_hi:[1,0]
	v_pk_mul_f32 v[118:119], v[118:119], s[30:31] op_sel_hi:[1,0]
	v_pk_mul_f32 v[120:121], v[120:121], s[30:31] op_sel_hi:[1,0]
	v_pk_mul_f32 v[122:123], v[122:123], s[30:31] op_sel_hi:[1,0]
	v_pk_mul_f32 v[124:125], v[124:125], s[30:31] op_sel_hi:[1,0]
	v_pk_mul_f32 v[126:127], v[126:127], s[30:31] op_sel_hi:[1,0]
	v_pk_mul_f32 v[128:129], v[128:129], s[30:31] op_sel_hi:[1,0]
	v_med3_f32 v66, v66, s24, v237
	v_med3_f32 v67, v67, s24, v237
	v_med3_f32 v68, v68, s24, v237
	v_med3_f32 v69, v69, s24, v237
	v_med3_f32 v70, v70, s24, v237
	v_med3_f32 v71, v71, s24, v237
	v_med3_f32 v72, v72, s24, v237
	v_med3_f32 v73, v73, s24, v237
	v_med3_f32 v74, v74, s24, v237
	v_med3_f32 v75, v75, s24, v237
	v_med3_f32 v76, v76, s24, v237
	v_med3_f32 v77, v77, s24, v237
	v_med3_f32 v78, v78, s24, v237
	v_med3_f32 v79, v79, s24, v237
	v_med3_f32 v80, v80, s24, v237
	v_med3_f32 v81, v81, s24, v237
	v_med3_f32 v82, v82, s24, v237
	v_med3_f32 v83, v83, s24, v237
	v_med3_f32 v84, v84, s24, v237
	v_med3_f32 v85, v85, s24, v237
	v_med3_f32 v86, v86, s24, v237
	v_med3_f32 v87, v87, s24, v237
	v_med3_f32 v88, v88, s24, v237
	v_med3_f32 v89, v89, s24, v237
	v_med3_f32 v90, v90, s24, v237
	v_med3_f32 v91, v91, s24, v237
	v_med3_f32 v92, v92, s24, v237
	v_med3_f32 v93, v93, s24, v237
	v_med3_f32 v94, v94, s24, v237
	v_med3_f32 v95, v95, s24, v237
	v_med3_f32 v96, v96, s24, v237
	v_med3_f32 v97, v97, s24, v237
	v_med3_f32 v98, v98, s24, v237
	v_med3_f32 v99, v99, s24, v237
	v_med3_f32 v100, v100, s24, v237
	v_med3_f32 v101, v101, s24, v237
	v_med3_f32 v102, v102, s24, v237
	v_med3_f32 v103, v103, s24, v237
	v_med3_f32 v104, v104, s24, v237
	v_med3_f32 v105, v105, s24, v237
	v_med3_f32 v106, v106, s24, v237
	v_med3_f32 v107, v107, s24, v237
	v_med3_f32 v108, v108, s24, v237
	v_med3_f32 v109, v109, s24, v237
	v_med3_f32 v110, v110, s24, v237
	v_med3_f32 v111, v111, s24, v237
	v_med3_f32 v112, v112, s24, v237
	v_med3_f32 v113, v113, s24, v237
	v_med3_f32 v114, v114, s24, v237
	v_med3_f32 v115, v115, s24, v237
	v_med3_f32 v116, v116, s24, v237
	v_med3_f32 v117, v117, s24, v237
	v_med3_f32 v118, v118, s24, v237
	v_med3_f32 v119, v119, s24, v237
	v_med3_f32 v120, v120, s24, v237
	v_med3_f32 v121, v121, s24, v237
	v_med3_f32 v122, v122, s24, v237
	v_med3_f32 v123, v123, s24, v237
	v_med3_f32 v124, v124, s24, v237
	v_med3_f32 v125, v125, s24, v237
	v_med3_f32 v126, v126, s24, v237
	v_med3_f32 v127, v127, s24, v237
	v_med3_f32 v128, v128, s24, v237
	v_med3_f32 v129, v129, s24, v237
	v_cvt_pk_fp8_f32 v66, v66, v70
	v_cvt_pk_fp8_f32 v66, v74, v78 op_sel:[0,0,1]
	v_cvt_pk_fp8_f32 v70, v67, v71
	v_cvt_pk_fp8_f32 v70, v75, v79 op_sel:[0,0,1]
	v_cvt_pk_fp8_f32 v74, v68, v72
	v_cvt_pk_fp8_f32 v74, v76, v80 op_sel:[0,0,1]
	v_cvt_pk_fp8_f32 v78, v69, v73
	v_cvt_pk_fp8_f32 v78, v77, v81 op_sel:[0,0,1]
	v_cvt_pk_fp8_f32 v67, v82, v86
	v_cvt_pk_fp8_f32 v67, v90, v94 op_sel:[0,0,1]
	v_cvt_pk_fp8_f32 v71, v83, v87
	v_cvt_pk_fp8_f32 v71, v91, v95 op_sel:[0,0,1]
	v_cvt_pk_fp8_f32 v75, v84, v88
	v_cvt_pk_fp8_f32 v75, v92, v96 op_sel:[0,0,1]
	v_cvt_pk_fp8_f32 v79, v85, v89
	v_cvt_pk_fp8_f32 v79, v93, v97 op_sel:[0,0,1]
	v_cvt_pk_fp8_f32 v68, v98, v102
	v_cvt_pk_fp8_f32 v68, v106, v110 op_sel:[0,0,1]
	v_cvt_pk_fp8_f32 v72, v99, v103
	v_cvt_pk_fp8_f32 v72, v107, v111 op_sel:[0,0,1]
	v_cvt_pk_fp8_f32 v76, v100, v104
	v_cvt_pk_fp8_f32 v76, v108, v112 op_sel:[0,0,1]
	v_cvt_pk_fp8_f32 v80, v101, v105
	v_cvt_pk_fp8_f32 v80, v109, v113 op_sel:[0,0,1]
	v_cvt_pk_fp8_f32 v69, v114, v118
	v_cvt_pk_fp8_f32 v69, v122, v126 op_sel:[0,0,1]
	v_cvt_pk_fp8_f32 v73, v115, v119
	v_cvt_pk_fp8_f32 v73, v123, v127 op_sel:[0,0,1]
	v_cvt_pk_fp8_f32 v77, v116, v120
	v_cvt_pk_fp8_f32 v77, v124, v128 op_sel:[0,0,1]
	v_cvt_pk_fp8_f32 v81, v117, v121
	v_cvt_pk_fp8_f32 v81, v125, v129 op_sel:[0,0,1]
	global_store_dwordx4 v250, v[66:69], s[42:43] nt
	global_store_dwordx4 v250, v[70:73], s[42:43] offset:2048 nt
	global_store_dwordx4 v251, v[74:77], s[42:43] nt
	global_store_dwordx4 v251, v[78:81], s[42:43] offset:2048 nt
	s_add_u32 s42, s42, 0x200
	s_addc_u32 s43, s43, 0
	s_waitcnt vmcnt(24)
; #define GAS __attribute__((address_space(1)))
; template <bool GAIN, bool NT = false> __device__ __forceinline__ void titem8_store(const TItem& d, int lane, const f32x4 (&r)[16], const f32x4 (&g)[4]) {
;     const int q = lane & 7, kg = lane >> 3; const unsigned lo = (unsigned)((4 * q) * d.ldk + 16 * kg);
;     GAS char* base = (GAS char*)d.dst;
;     f32x4 s[16];
; #pragma unroll
;     for (int j = 0; j < 16; ++j) s[j] = r[j] * ((GAIN ? g[j >> 2][j & 3] : 1.0f) * W8_SCALE);
; #pragma unroll
;     for (int i = 0; i < 4; ++i) { v4u w;
;         w.x = pk4_fp8w(s[0][i], s[1][i], s[2][i], s[3][i]); w.y = pk4_fp8w(s[4][i], s[5][i], s[6][i], s[7][i]);
;         w.z = pk4_fp8w(s[8][i], s[9][i], s[10][i], s[11][i]); w.w = pk4_fp8w(s[12][i], s[13][i], s[14][i], s[15][i]);
;         GAS v4u* p = (GAS v4u*)(base + (size_t)i * (size_t)d.ldk + lo);
;         if (NT) __builtin_nontemporal_store(w, p); else *p = w; }
; }
	v_pk_mul_f32 v[130:131], v[130:131], s[30:31] op_sel_hi:[1,0]
	v_pk_mul_f32 v[132:133], v[132:133], s[30:31] op_sel_hi:[1,0]
	v_pk_mul_f32 v[134:135], v[134:135], s[30:31] op_sel_hi:[1,0]
	v_pk_mul_f32 v[136:137], v[136:137], s[30:31] op_sel_hi:[1,0]
	v_pk_mul_f32 v[138:139], v[138:139], s[30:31] op_sel_hi:[1,0]
	v_pk_mul_f32 v[140:141], v[140:141], s[30:31] op_sel_hi:[1,0]
	v_pk_mul_f32 v[142:143], v[142:143], s[30:31] op_sel_hi:[1,0]
	v_pk_mul_f32 v[144:145], v[144:145], s[30:31] op_sel_hi:[1,0]
	v_pk_mul_f32 v[146:147], v[146:147], s[30:31] op_sel_hi:[1,0]
	v_pk_mul_f32 v[148:149], v[148:149], s[30:31] op_sel_hi:[1,0]
	v_pk_mul_f32 v[150:151], v[150:151], s[30:31] op_sel_hi:[1,0]
	v_pk_mul_f32 v[152:153], v[152:153], s[30:31] op_sel_hi:[1,0]
	v_pk_mul_f32 v[154:155], v[154:155], s[30:31] op_sel_hi:[1,0]
	v_pk_mul_f32 v[156:157], v[156:157], s[30:31] op_sel_hi:[1,0]
	v_pk_mul_f32 v[158:159], v[158:159], s[30:31] op_sel_hi:[1,0]
	v_pk_mul_f32 v[160:161], v[160:161], s[30:31] op_sel_hi:[1,0]
	v_pk_mul_f32 v[162:163], v[162:163], s[30:31] op_sel_hi:[1,0]
	v_pk_mul_f32 v[164:165], v[164:165], s[30:31] op_sel_hi:[1,0]
	v_pk_mul_f32 v[166:167], v[166:167], s[30:31] op_sel_hi:[1,0]
	v_pk_mul_f32 v[168:169], v[168:169], s[30:31] op_sel_hi:[1,0]
	v_pk_mul_f32 v[170:171], v[170:171], s[30:31] op_sel_hi:[1,0]
	v_pk_mul_f32 v[172:173], v[172:173], s[30:31] op_sel_hi:[1,0]
	v_pk_mul_f32 v[174:175], v[174:175], s[30:31] op_sel_hi:[1,0]
	v_pk_mul_f32 v[176:177], v[176:177], s[30:31] op_sel_hi:[1,0]
	v_pk_mul_f32 v[178:179], v[178:179], s[30:31] op_sel_hi:[1,0]
	v_pk_mul_f32 v[180:181], v[180:181], s[30:31] op_sel_hi:[1,0]
	v_pk_mul_f32 v[182:183], v[182:183], s[30:31] op_sel_hi:[1,0]
	v_pk_mul_f32 v[184:185], v[184:185], s[30:31] op_sel_hi:[1,0]
	v_pk_mul_f32 v[186:187], v[186:187], s[30:31] op_sel_hi:[1,0]
	v_pk_mul_f32 v[188:189], v[188:189], s[30:31] op_sel_hi:[1,0]
	v_pk_mul_f32 v[190:191], v[190:191], s[30:31] op_sel_hi:[1,0]
	v_pk_mul_f32 v[192:193], v[192:193], s[30:31] op_sel_hi:[1,0]
	v_med3_f32 v130, v130, s24, v237
	v_med3_f32 v131, v131, s24, v237
	v_med3_f32 v132, v132, s24, v237
	v_med3_f32 v133, v133, s24, v237
	v_med3_f32 v134, v134, s24, v237
	v_med3_f32 v135, v135, s24, v237
	v_med3_f32 v136, v136, s24, v237
	v_med3_f32 v137, v137, s24, v237
	v_med3_f32 v138, v138, s24, v237
	v_med3_f32 v139, v139, s24, v237
	v_med3_f32 v140, v140, s24, v237
	v_med3_f32 v141, v141, s24, v237
	v_med3_f32 v142, v142, s24, v237
	v_med3_f32 v143, v143, s24, v237
	v_med3_f32 v144, v144, s24, v237
	v_med3_f32 v145, v145, s24, v237
	v_med3_f32 v146, v146, s24, v237
	v_med3_f32 v147, v147, s24, v237
	v_med3_f32 v148, v148, s24, v237
	v_med3_f32 v149, v149, s24, v237
	v_med3_f32 v150, v150, s24, v237
	v_med3_f32 v151, v151, s24, v237
	v_med3_f32 v152, v152, s24, v237
	v_med3_f32 v153, v153, s24, v237
	v_med3_f32 v154, v154, s24, v237
	v_med3_f32 v155, v155, s24, v237
	v_med3_f32 v156, v156, s24, v237
	v_med3_f32 v157, v157, s24, v237
	v_med3_f32 v158, v158, s24, v237
	v_med3_f32 v159, v159, s24, v237
	v_med3_f32 v160, v160, s24, v237
	v_med3_f32 v161, v161, s24, v237
	v_med3_f32 v162, v162, s24, v237
	v_med3_f32 v163, v163, s24, v237
	v_med3_f32 v164, v164, s24, v237
	v_med3_f32 v165, v165, s24, v237
	v_med3_f32 v166, v166, s24, v237
	v_med3_f32 v167, v167, s24, v237
	v_med3_f32 v168, v168, s24, v237
	v_med3_f32 v169, v169, s24, v237
	v_med3_f32 v170, v170, s24, v237
	v_med3_f32 v171, v171, s24, v237
	v_med3_f32 v172, v172, s24, v237
	v_med3_f32 v173, v173, s24, v237
	v_med3_f32 v174, v174, s24, v237
	v_med3_f32 v175, v175, s24, v237
	v_med3_f32 v176, v176, s24, v237
	v_med3_f32 v177, v177, s24, v237
	v_med3_f32 v178, v178, s24, v237
	v_med3_f32 v179, v179, s24, v237
	v_med3_f32 v180, v180, s24, v237
	v_med3_f32 v181, v181, s24, v237
	v_med3_f32 v182, v182, s24, v237
	v_med3_f32 v183, v183, s24, v237
	v_med3_f32 v184, v184, s24, v237
	v_med3_f32 v185, v185, s24, v237
	v_med3_f32 v186, v186, s24, v237
	v_med3_f32 v187, v187, s24, v237
	v_med3_f32 v188, v188, s24, v237
	v_med3_f32 v189, v189, s24, v237
	v_med3_f32 v190, v190, s24, v237
	v_med3_f32 v191, v191, s24, v237
	v_med3_f32 v192, v192, s24, v237
	v_med3_f32 v193, v193, s24, v237
	v_cvt_pk_fp8_f32 v130, v130, v134
	v_cvt_pk_fp8_f32 v130, v138, v142 op_sel:[0,0,1]
	v_cvt_pk_fp8_f32 v134, v131, v135
	v_cvt_pk_fp8_f32 v134, v139, v143 op_sel:[0,0,1]
	v_cvt_pk_fp8_f32 v138, v132, v136
	v_cvt_pk_fp8_f32 v138, v140, v144 op_sel:[0,0,1]
	v_cvt_pk_fp8_f32 v142, v133, v137
	v_cvt_pk_fp8_f32 v142, v141, v145 op_sel:[0,0,1]
	v_cvt_pk_fp8_f32 v131, v146, v150
	v_cvt_pk_fp8_f32 v131, v154, v158 op_sel:[0,0,1]
	v_cvt_pk_fp8_f32 v135, v147, v151
	v_cvt_pk_fp8_f32 v135, v155, v159 op_sel:[0,0,1]
	v_cvt_pk_fp8_f32 v139, v148, v152
	v_cvt_pk_fp8_f32 v139, v156, v160 op_sel:[0,0,1]
	v_cvt_pk_fp8_f32 v143, v149, v153
	v_cvt_pk_fp8_f32 v143, v157, v161 op_sel:[0,0,1]
	v_cvt_pk_fp8_f32 v132, v162, v166
	v_cvt_pk_fp8_f32 v132, v170, v174 op_sel:[0,0,1]
	v_cvt_pk_fp8_f32 v136, v163, v167
	v_cvt_pk_fp8_f32 v136, v171, v175 op_sel:[0,0,1]
	v_cvt_pk_fp8_f32 v140, v164, v168
	v_cvt_pk_fp8_f32 v140, v172, v176 op_sel:[0,0,1]
	v_cvt_pk_fp8_f32 v144, v165, v169
	v_cvt_pk_fp8_f32 v144, v173, v177 op_sel:[0,0,1]
	v_cvt_pk_fp8_f32 v133, v178, v182
	v_cvt_pk_fp8_f32 v133, v186, v190 op_sel:[0,0,1]
	v_cvt_pk_fp8_f32 v137, v179, v183
	v_cvt_pk_fp8_f32 v137, v187, v191 op_sel:[0,0,1]
	v_cvt_pk_fp8_f32 v141, v180, v184
	v_cvt_pk_fp8_f32 v141, v188, v192 op_sel:[0,0,1]
	v_cvt_pk_fp8_f32 v145, v181, v185
	v_cvt_pk_fp8_f32 v145, v189, v193 op_sel:[0,0,1]
	global_store_dwordx4 v250, v[130:133], s[42:43] nt
	global_store_dwordx4 v250, v[134:137], s[42:43] offset:2048 nt
	global_store_dwordx4 v251, v[138:141], s[42:43] nt
	global_store_dwordx4 v251, v[142:145], s[42:43] offset:2048 nt
	s_add_u32 s42, s42, 0x200
	s_addc_u32 s43, s43, 0
	s_waitcnt vmcnt(8)
; #define GAS __attribute__((address_space(1)))
; template <bool GAIN, bool NT = false> __device__ __forceinline__ void titem8_store(const TItem& d, int lane, const f32x4 (&r)[16], const f32x4 (&g)[4]) {
;     const int q = lane & 7, kg = lane >> 3; const unsigned lo = (unsigned)((4 * q) * d.ldk + 16 * kg);
;     GAS char* base = (GAS char*)d.dst;
;     f32x4 s[16];
; #pragma unroll
;     for (int j = 0; j < 16; ++j) s[j] = r[j] * ((GAIN ? g[j >> 2][j & 3] : 1.0f) * W8_SCALE);
; #pragma unroll
;     for (int i = 0; i < 4; ++i) { v4u w;
;         w.x = pk4_fp8w(s[0][i], s[1][i], s[2][i], s[3][i]); w.y = pk4_fp8w(s[4][i], s[5][i], s[6][i], s[7][i]);
;         w.z = pk4_fp8w(s[8][i], s[9][i], s[10][i], s[11][i]); w.w = pk4_fp8w(s[12][i], s[13][i], s[14][i], s[15][i]);
;         GAS v4u* p = (GAS v4u*)(base + (size_t)i * (size_t)d.ldk + lo);
;         if (NT) __builtin_nontemporal_store(w, p); else *p = w; }
; }
	v_pk_mul_f32 v[0:1], v[0:1], s[30:31] op_sel_hi:[1,0]
	v_pk_mul_f32 v[2:3], v[2:3], s[30:31] op_sel_hi:[1,0]
	v_pk_mul_f32 v[4:5], v[4:5], s[30:31] op_sel_hi:[1,0]
	v_pk_mul_f32 v[6:7], v[6:7], s[30:31] op_sel_hi:[1,0]
	v_pk_mul_f32 v[8:9], v[8:9], s[30:31] op_sel_hi:[1,0]
	v_pk_mul_f32 v[10:11], v[10:11], s[30:31] op_sel_hi:[1,0]
	v_pk_mul_f32 v[12:13], v[12:13], s[30:31] op_sel_hi:[1,0]
	v_pk_mul_f32 v[14:15], v[14:15], s[30:31] op_sel_hi:[1,0]
	v_pk_mul_f32 v[16:17], v[16:17], s[30:31] op_sel_hi:[1,0]
	v_pk_mul_f32 v[18:19], v[18:19], s[30:31] op_sel_hi:[1,0]
	v_pk_mul_f32 v[20:21], v[20:21], s[30:31] op_sel_hi:[1,0]
	v_pk_mul_f32 v[22:23], v[22:23], s[30:31] op_sel_hi:[1,0]
	v_pk_mul_f32 v[24:25], v[24:25], s[30:31] op_sel_hi:[1,0]
	v_pk_mul_f32 v[26:27], v[26:27], s[30:31] op_sel_hi:[1,0]
	v_pk_mul_f32 v[28:29], v[28:29], s[30:31] op_sel_hi:[1,0]
	v_pk_mul_f32 v[30:31], v[30:31], s[30:31] op_sel_hi:[1,0]
	v_pk_mul_f32 v[32:33], v[32:33], s[30:31] op_sel_hi:[1,0]
	v_pk_mul_f32 v[34:35], v[34:35], s[30:31] op_sel_hi:[1,0]
	v_pk_mul_f32 v[36:37], v[36:37], s[30:31] op_sel_hi:[1,0]
	v_pk_mul_f32 v[38:39], v[38:39], s[30:31] op_sel_hi:[1,0]
	v_pk_mul_f32 v[40:41], v[40:41], s[30:31] op_sel_hi:[1,0]
	v_pk_mul_f32 v[42:43], v[42:43], s[30:31] op_sel_hi:[1,0]
	v_pk_mul_f32 v[44:45], v[44:45], s[30:31] op_sel_hi:[1,0]
	v_pk_mul_f32 v[46:47], v[46:47], s[30:31] op_sel_hi:[1,0]
	v_pk_mul_f32 v[48:49], v[48:49], s[30:31] op_sel_hi:[1,0]
	v_pk_mul_f32 v[50:51], v[50:51], s[30:31] op_sel_hi:[1,0]
	v_pk_mul_f32 v[52:53], v[52:53], s[30:31] op_sel_hi:[1,0]
	v_pk_mul_f32 v[54:55], v[54:55], s[30:31] op_sel_hi:[1,0]
	v_pk_mul_f32 v[56:57], v[56:57], s[30:31] op_sel_hi:[1,0]
	v_pk_mul_f32 v[58:59], v[58:59], s[30:31] op_sel_hi:[1,0]
	v_pk_mul_f32 v[60:61], v[60:61], s[30:31] op_sel_hi:[1,0]
	v_pk_mul_f32 v[62:63], v[62:63], s[30:31] op_sel_hi:[1,0]
	v_med3_f32 v0, v0, s24, v237
	v_med3_f32 v1, v1, s24, v237
	v_med3_f32 v2, v2, s24, v237
	v_med3_f32 v3, v3, s24, v237
	v_med3_f32 v4, v4, s24, v237
	v_med3_f32 v5, v5, s24, v237
	v_med3_f32 v6, v6, s24, v237
	v_med3_f32 v7, v7, s24, v237
	v_med3_f32 v8, v8, s24, v237
	v_med3_f32 v9, v9, s24, v237
	v_med3_f32 v10, v10, s24, v237
	v_med3_f32 v11, v11, s24, v237
	v_med3_f32 v12, v12, s24, v237
	v_med3_f32 v13, v13, s24, v237
	v_med3_f32 v14, v14, s24, v237
	v_med3_f32 v15, v15, s24, v237
	v_med3_f32 v16, v16, s24, v237
	v_med3_f32 v17, v17, s24, v237
	v_med3_f32 v18, v18, s24, v237
	v_med3_f32 v19, v19, s24, v237
	v_med3_f32 v20, v20, s24, v237
	v_med3_f32 v21, v21, s24, v237
	v_med3_f32 v22, v22, s24, v237
	v_med3_f32 v23, v23, s24, v237
	v_med3_f32 v24, v24, s24, v237
	v_med3_f32 v25, v25, s24, v237
	v_med3_f32 v26, v26, s24, v237
	v_med3_f32 v27, v27, s24, v237
	v_med3_f32 v28, v28, s24, v237
	v_med3_f32 v29, v29, s24, v237
	v_med3_f32 v30, v30, s24, v237
	v_med3_f32 v31, v31, s24, v237
	v_med3_f32 v32, v32, s24, v237
	v_med3_f32 v33, v33, s24, v237
	v_med3_f32 v34, v34, s24, v237
	v_med3_f32 v35, v35, s24, v237
	v_med3_f32 v36, v36, s24, v237
	v_med3_f32 v37, v37, s24, v237
	v_med3_f32 v38, v38, s24, v237
	v_med3_f32 v39, v39, s24, v237
	v_med3_f32 v40, v40, s24, v237
	v_med3_f32 v41, v41, s24, v237
	v_med3_f32 v42, v42, s24, v237
	v_med3_f32 v43, v43, s24, v237
	v_med3_f32 v44, v44, s24, v237
	v_med3_f32 v45, v45, s24, v237
	v_med3_f32 v46, v46, s24, v237
	v_med3_f32 v47, v47, s24, v237
	v_med3_f32 v48, v48, s24, v237
	v_med3_f32 v49, v49, s24, v237
	v_med3_f32 v50, v50, s24, v237
	v_med3_f32 v51, v51, s24, v237
	v_med3_f32 v52, v52, s24, v237
	v_med3_f32 v53, v53, s24, v237
	v_med3_f32 v54, v54, s24, v237
	v_med3_f32 v55, v55, s24, v237
	v_med3_f32 v56, v56, s24, v237
	v_med3_f32 v57, v57, s24, v237
	v_med3_f32 v58, v58, s24, v237
	v_med3_f32 v59, v59, s24, v237
	v_med3_f32 v60, v60, s24, v237
	v_med3_f32 v61, v61, s24, v237
	v_med3_f32 v62, v62, s24, v237
	v_med3_f32 v63, v63, s24, v237
	v_cvt_pk_fp8_f32 v0, v0, v4
	v_cvt_pk_fp8_f32 v0, v8, v12 op_sel:[0,0,1]
	v_cvt_pk_fp8_f32 v4, v1, v5
	v_cvt_pk_fp8_f32 v4, v9, v13 op_sel:[0,0,1]
	v_cvt_pk_fp8_f32 v8, v2, v6
	v_cvt_pk_fp8_f32 v8, v10, v14 op_sel:[0,0,1]
	v_cvt_pk_fp8_f32 v12, v3, v7
	v_cvt_pk_fp8_f32 v12, v11, v15 op_sel:[0,0,1]
	v_cvt_pk_fp8_f32 v1, v16, v20
	v_cvt_pk_fp8_f32 v1, v24, v28 op_sel:[0,0,1]
	v_cvt_pk_fp8_f32 v5, v17, v21
	v_cvt_pk_fp8_f32 v5, v25, v29 op_sel:[0,0,1]
	v_cvt_pk_fp8_f32 v9, v18, v22
	v_cvt_pk_fp8_f32 v9, v26, v30 op_sel:[0,0,1]
	v_cvt_pk_fp8_f32 v13, v19, v23
	v_cvt_pk_fp8_f32 v13, v27, v31 op_sel:[0,0,1]
	v_cvt_pk_fp8_f32 v2, v32, v36
	v_cvt_pk_fp8_f32 v2, v40, v44 op_sel:[0,0,1]
	v_cvt_pk_fp8_f32 v6, v33, v37
	v_cvt_pk_fp8_f32 v6, v41, v45 op_sel:[0,0,1]
	v_cvt_pk_fp8_f32 v10, v34, v38
	v_cvt_pk_fp8_f32 v10, v42, v46 op_sel:[0,0,1]
	v_cvt_pk_fp8_f32 v14, v35, v39
	v_cvt_pk_fp8_f32 v14, v43, v47 op_sel:[0,0,1]
	v_cvt_pk_fp8_f32 v3, v48, v52
	v_cvt_pk_fp8_f32 v3, v56, v60 op_sel:[0,0,1]
	v_cvt_pk_fp8_f32 v7, v49, v53
	v_cvt_pk_fp8_f32 v7, v57, v61 op_sel:[0,0,1]
	v_cvt_pk_fp8_f32 v11, v50, v54
	v_cvt_pk_fp8_f32 v11, v58, v62 op_sel:[0,0,1]
	v_cvt_pk_fp8_f32 v15, v51, v55
	v_cvt_pk_fp8_f32 v15, v59, v63 op_sel:[0,0,1]
	global_store_dwordx4 v250, v[0:3], s[42:43] nt
	global_store_dwordx4 v250, v[4:7], s[42:43] offset:2048 nt
	global_store_dwordx4 v251, v[8:11], s[42:43] nt
	global_store_dwordx4 v251, v[12:15], s[42:43] offset:2048 nt
	s_add_u32 s42, s42, 0x3ffa00
	s_addc_u32 s43, s43, 0
	v_mov_b32_e32 v65, 0
